# GEMM K-loops: fragment ds_reads issued first in every load segment, loop-tail scalar updates moved among the last MFMAs (on top of the MLA ds_read hoist)
# baseline (speedup 1.0000x reference)
; #define PG8_STAGE(bufoff, gbase, voff) do { _Pragma("unroll") for (int _i = 0; _i < 2; ++_i) \
;         __builtin_amdgcn_global_load_lds((const unsigned*)((const char*)(gbase) + (voff)[_i]), (PG8_LAS unsigned*)(lds + (bufoff) + ldsw + _i * 8192), 16, 0, 0); } while (0)
; #define PG8_WAIT_V(n) asm volatile("s_waitcnt vmcnt(" #n ")" ::: "memory")
; #define PG8_WAIT_L(n) asm volatile("s_waitcnt lgkmcnt(" #n ")" ::: "memory")
; #define PG8_BAR __builtin_amdgcn_s_barrier()
; #define PG8_SCHED __builtin_amdgcn_sched_barrier(0)
; template <class Epi, class Sched, bool ALIGN_EPI = false, bool SP2 = false, bool F8 = false>
; __device__ __forceinline__ void gemm_phase(PG8_LAS unsigned char* lds, const Gemm g, const Sched& S, const Epi& E, const int tidb  ) {
;     ...
;         for (int t = 0; t < nt; t += 2) {
;             const bool last = (t == nt - 2);
;             if constexpr (Epi::PREFETCH) { if (t == 0) E.prefetch(cur, wid, lane); }
;             const char* a1 = cA + (size_t)(t + 1) * kstep;
;             const char* a2 = last ? nA : cA + (size_t)(t + 2) * kstep; const char* b2 = last ? nB : cB + (size_t)(t + 2) * kstep;
;             const char* a3 = a2 + kstep; const char* b3 = b2 + kstep;
;             if (last && has_next) S.a_ready(nxt);
;             if constexpr (SP2) {
;             PG8_LDB(B0, 0, 0); PG8_LDB(B1, 0, 1); PG8_SCHED; PG8_LDA(At, 0, 0); PG8_STAGE(PG8_SA(1, 1), a1 + hstep, voffA);
;             PG8_WAIT_V(8); PG8_WAIT_L(0); PG8_BAR; PG8_MMA(0, 0, At, B0); PG8_MMA(0, 1, At, B1); PG8_BAR; PG8_SCHED;
;             PG8_LDA(At, 0, 1); PG8_STAGE(PG8_SB(0, 0), b2, voffB); PG8_STAGE(PG8_SB(0, 1), b2 + hstep, voffB); PG8_STAGE(PG8_SA(0, 0), a2, voffA);
;             PG8_WAIT_V(8); PG8_WAIT_L(0); PG8_BAR; PG8_MMA(1, 0, At, B0); PG8_MMA(1, 1, At, B1); PG8_BAR; PG8_SCHED;
.LBB0_51:
	s_add_i32 s15, 0, 0x10000
	v_add_u32_e32 v0, s15, v190
	ds_read_b128 v[18:21], v0
	ds_read_b128 v[22:25], v0 offset:1024
	ds_read_b128 v[26:29], v0 offset:2048
	ds_read_b128 v[30:33], v0 offset:3072
	s_add_i32 s14, s6, 2
	s_add_u32 s8, s4, 0x80
	s_addc_u32 s7, s5, 0
	s_cmp_eq_u32 s97, s6
	s_cselect_b32 s7, s73, s7
	s_cselect_b32 s6, s72, s8
	s_cselect_b32 s9, s53, s13
	s_cselect_b32 s8, s52, s12
	s_add_i32 s54, 0, 0x14000
	v_add_u32_e32 v0, s54, v190
	ds_read_b128 v[2:5], v0
	ds_read_b128 v[6:9], v0 offset:1024
	ds_read_b128 v[10:13], v0 offset:2048
	ds_read_b128 v[14:17], v0 offset:3072
	v_lshl_add_u64 v[184:185], s[4:5], 0, v[172:173]
	s_add_i32 m0, s43, 0xc000
	ds_read_b128 v[176:179], v191
	ds_read_b128 v[180:183], v191 offset:1024
	ds_read_b128 v[204:207], v191 offset:2048
	ds_read_b128 v[208:211], v191 offset:3072
	ds_read_b128 v[212:215], v191 offset:4096
	ds_read_b128 v[216:219], v191 offset:5120
	ds_read_b128 v[220:223], v191 offset:6144
	ds_read_b128 v[224:227], v191 offset:7168
	global_load_lds_dwordx4 v[184:185], off
	v_lshl_add_u64 v[184:185], s[4:5], 0, v[174:175]
	s_add_i32 m0, s43, 0xe000
	s_nop 0
	global_load_lds_dwordx4 v[184:185], off
	s_waitcnt vmcnt(8)
	s_waitcnt lgkmcnt(0)
	s_barrier
	s_setprio 1
	s_waitcnt lgkmcnt(0)
	v_mfma_scale_f32_16x16x128_f8f6f4 v[158:161], v[18:25], v[176:183], v[158:161], v246, v247 op_sel_hi:[0,0,0]
	v_mfma_scale_f32_16x16x128_f8f6f4 v[154:157], v[26:33], v[176:183], v[154:157], v246, v247 op_sel_hi:[0,0,0]
	v_mfma_scale_f32_16x16x128_f8f6f4 v[150:153], v[18:25], v[204:211], v[150:153], v246, v247 op_sel_hi:[0,0,0]
	v_mfma_scale_f32_16x16x128_f8f6f4 v[146:149], v[26:33], v[204:211], v[146:149], v246, v247 op_sel_hi:[0,0,0]
	v_mfma_scale_f32_16x16x128_f8f6f4 v[142:145], v[18:25], v[212:219], v[142:145], v246, v247 op_sel_hi:[0,0,0]
	v_mfma_scale_f32_16x16x128_f8f6f4 v[138:141], v[26:33], v[212:219], v[138:141], v246, v247 op_sel_hi:[0,0,0]
	v_mfma_scale_f32_16x16x128_f8f6f4 v[134:137], v[18:25], v[220:227], v[134:137], v246, v247 op_sel_hi:[0,0,0]
	v_mfma_scale_f32_16x16x128_f8f6f4 v[130:133], v[26:33], v[220:227], v[130:133], v246, v247 op_sel_hi:[0,0,0]
	s_setprio 0
	s_setprio 1
	v_mfma_scale_f32_16x16x128_f8f6f4 v[94:97], v[2:9], v[176:183], v[94:97], v246, v247 op_sel_hi:[0,0,0]
	v_mfma_scale_f32_16x16x128_f8f6f4 v[90:93], v[10:17], v[176:183], v[90:93], v246, v247 op_sel_hi:[0,0,0]
	v_mfma_scale_f32_16x16x128_f8f6f4 v[86:89], v[2:9], v[204:211], v[86:89], v246, v247 op_sel_hi:[0,0,0]
	v_mfma_scale_f32_16x16x128_f8f6f4 v[82:85], v[10:17], v[204:211], v[82:85], v246, v247 op_sel_hi:[0,0,0]
	v_mfma_scale_f32_16x16x128_f8f6f4 v[78:81], v[2:9], v[212:219], v[78:81], v246, v247 op_sel_hi:[0,0,0]
	v_mfma_scale_f32_16x16x128_f8f6f4 v[74:77], v[10:17], v[212:219], v[74:77], v246, v247 op_sel_hi:[0,0,0]
	v_mfma_scale_f32_16x16x128_f8f6f4 v[70:73], v[2:9], v[220:227], v[70:73], v246, v247 op_sel_hi:[0,0,0]
	v_mfma_scale_f32_16x16x128_f8f6f4 v[66:69], v[10:17], v[220:227], v[66:69], v246, v247 op_sel_hi:[0,0,0]
	s_setprio 0
	s_barrier
	ds_read_b128 v[204:207], v191 offset:16384
	ds_read_b128 v[208:211], v191 offset:17408
	ds_read_b128 v[212:215], v191 offset:18432
	ds_read_b128 v[216:219], v191 offset:19456
	ds_read_b128 v[220:223], v191 offset:20480
	ds_read_b128 v[224:227], v191 offset:21504
	ds_read_b128 v[228:231], v191 offset:22528
	ds_read_b128 v[232:235], v191 offset:23552
	s_add_i32 s15, s15, s41
	v_lshl_add_u64 v[176:177], s[8:9], 0, v[166:167]
	s_mov_b32 m0, s15
	s_nop 0
	global_load_lds_dwordx4 v[176:177], off
	s_add_i32 m0, s15, 0x2000
	v_lshl_add_u64 v[178:179], s[8:9], 0, v[170:171]
	s_add_u32 s8, s8, s20
	s_addc_u32 s9, s9, s21
	s_add_i32 s15, s54, s41
	global_load_lds_dwordx4 v[178:179], off
	v_lshl_add_u64 v[180:181], s[8:9], 0, v[166:167]
	s_mov_b32 m0, s15
	v_lshl_add_u64 v[182:183], s[8:9], 0, v[170:171]
	global_load_lds_dwordx4 v[180:181], off
	s_add_i32 m0, s15, 0x2000
	v_lshl_add_u64 v[184:185], s[6:7], 0, v[164:165]
	global_load_lds_dwordx4 v[182:183], off
	s_mov_b32 m0, s43
	v_lshl_add_u64 v[186:187], s[6:7], 0, v[168:169]
	global_load_lds_dwordx4 v[184:185], off
	s_mov_b32 m0, s66
	s_nop 0
	global_load_lds_dwordx4 v[186:187], off
	s_waitcnt vmcnt(8)
	s_waitcnt lgkmcnt(0)
	s_barrier
	s_setprio 1
	s_waitcnt lgkmcnt(0)
	v_mfma_scale_f32_16x16x128_f8f6f4 v[126:129], v[18:25], v[204:211], v[126:129], v246, v247 op_sel_hi:[0,0,0]
	v_mfma_scale_f32_16x16x128_f8f6f4 v[122:125], v[26:33], v[204:211], v[122:125], v246, v247 op_sel_hi:[0,0,0]
	v_mfma_scale_f32_16x16x128_f8f6f4 v[118:121], v[18:25], v[212:219], v[118:121], v246, v247 op_sel_hi:[0,0,0]
	v_mfma_scale_f32_16x16x128_f8f6f4 v[114:117], v[26:33], v[212:219], v[114:117], v246, v247 op_sel_hi:[0,0,0]
	v_mfma_scale_f32_16x16x128_f8f6f4 v[110:113], v[18:25], v[220:227], v[110:113], v246, v247 op_sel_hi:[0,0,0]
	v_mfma_scale_f32_16x16x128_f8f6f4 v[106:109], v[26:33], v[220:227], v[106:109], v246, v247 op_sel_hi:[0,0,0]
	v_mfma_scale_f32_16x16x128_f8f6f4 v[102:105], v[18:25], v[228:235], v[102:105], v246, v247 op_sel_hi:[0,0,0]
	v_mfma_scale_f32_16x16x128_f8f6f4 v[98:101], v[26:33], v[228:235], v[98:101], v246, v247 op_sel_hi:[0,0,0]
	s_setprio 0
	s_setprio 1
	v_mfma_scale_f32_16x16x128_f8f6f4 v[62:65], v[2:9], v[204:211], v[62:65], v246, v247 op_sel_hi:[0,0,0]
	v_mfma_scale_f32_16x16x128_f8f6f4 v[58:61], v[10:17], v[204:211], v[58:61], v246, v247 op_sel_hi:[0,0,0]
	v_mfma_scale_f32_16x16x128_f8f6f4 v[54:57], v[2:9], v[212:219], v[54:57], v246, v247 op_sel_hi:[0,0,0]
	v_mfma_scale_f32_16x16x128_f8f6f4 v[50:53], v[10:17], v[212:219], v[50:53], v246, v247 op_sel_hi:[0,0,0]
	v_mfma_scale_f32_16x16x128_f8f6f4 v[46:49], v[2:9], v[220:227], v[46:49], v246, v247 op_sel_hi:[0,0,0]
	v_mfma_scale_f32_16x16x128_f8f6f4 v[42:45], v[10:17], v[220:227], v[42:45], v246, v247 op_sel_hi:[0,0,0]
	v_mfma_scale_f32_16x16x128_f8f6f4 v[38:41], v[2:9], v[228:235], v[38:41], v246, v247 op_sel_hi:[0,0,0]
	v_mfma_scale_f32_16x16x128_f8f6f4 v[34:37], v[10:17], v[228:235], v[34:37], v246, v247 op_sel_hi:[0,0,0]
	s_setprio 0
	s_barrier
; #define PG8_STAGE(bufoff, gbase, voff) do { _Pragma("unroll") for (int _i = 0; _i < 2; ++_i) \
;         __builtin_amdgcn_global_load_lds((const unsigned*)((const char*)(gbase) + (voff)[_i]), (PG8_LAS unsigned*)(lds + (bufoff) + ldsw + _i * 8192), 16, 0, 0); } while (0)
; #define PG8_WAIT_V(n) asm volatile("s_waitcnt vmcnt(" #n ")" ::: "memory")
; #define PG8_WAIT_L(n) asm volatile("s_waitcnt lgkmcnt(" #n ")" ::: "memory")
; #define PG8_BAR __builtin_amdgcn_s_barrier()
; #define PG8_SCHED __builtin_amdgcn_sched_barrier(0)
; template <class Epi, class Sched, bool ALIGN_EPI = false, bool SP2 = false, bool F8 = false>
; __device__ __forceinline__ void gemm_phase(PG8_LAS unsigned char* lds, const Gemm g, const Sched& S, const Epi& E, const int tidb  ) {
;     ...
;             PG8_LDB(B0, 1, 0); PG8_LDB(B1, 1, 1); PG8_SCHED; PG8_LDA(At, 1, 0); PG8_STAGE(PG8_SA(0, 1), a2 + hstep, voffA);
;             PG8_WAIT_V(8); PG8_WAIT_L(0); PG8_BAR; PG8_MMA(0, 0, At, B0); PG8_MMA(0, 1, At, B1); PG8_BAR; PG8_SCHED;
;             PG8_LDA(At, 1, 1); PG8_STAGE(PG8_SB(1, 0), b3, voffB); PG8_STAGE(PG8_SB(1, 1), b3 + hstep, voffB); PG8_STAGE(PG8_SA(1, 0), a3, voffA);
;             PG8_WAIT_V(8); PG8_WAIT_L(0); PG8_BAR; PG8_MMA(1, 0, At, B0); PG8_MMA(1, 1, At, B1); PG8_BAR; PG8_SCHED;
	s_add_i32 s8, 0, 0x18000
	v_add_u32_e32 v0, s8, v190
	s_add_i32 s9, 0, 0x1c000
	ds_read_b128 v[2:5], v0
	ds_read_b128 v[6:9], v0 offset:1024
	ds_read_b128 v[10:13], v0 offset:2048
	ds_read_b128 v[14:17], v0 offset:3072
	v_add_u32_e32 v0, s9, v190
	ds_read_b128 v[18:21], v0
	ds_read_b128 v[22:25], v0 offset:1024
	ds_read_b128 v[26:29], v0 offset:2048
	ds_read_b128 v[30:33], v0 offset:3072
	s_add_u32 s6, s6, s20
	s_addc_u32 s7, s7, s21
	s_mov_b32 m0, s48
	v_lshl_add_u64 v[192:193], s[6:7], 0, v[164:165]
	ds_read_b128 v[204:207], v191 offset:32768
	ds_read_b128 v[208:211], v191 offset:33792
	ds_read_b128 v[212:215], v191 offset:34816
	ds_read_b128 v[216:219], v191 offset:35840
	ds_read_b128 v[220:223], v191 offset:36864
	ds_read_b128 v[224:227], v191 offset:37888
	ds_read_b128 v[228:231], v191 offset:38912
	ds_read_b128 v[232:235], v191 offset:39936
	global_load_lds_dwordx4 v[192:193], off
	v_lshl_add_u64 v[192:193], s[6:7], 0, v[168:169]
	s_mov_b32 m0, s90
	s_nop 0
	global_load_lds_dwordx4 v[192:193], off
	s_waitcnt vmcnt(8)
	s_waitcnt lgkmcnt(0)
	s_barrier
	s_setprio 1
	s_waitcnt lgkmcnt(0)
	v_mfma_scale_f32_16x16x128_f8f6f4 v[158:161], v[2:9], v[204:211], v[158:161], v246, v247 op_sel_hi:[0,0,0]
	v_mfma_scale_f32_16x16x128_f8f6f4 v[154:157], v[10:17], v[204:211], v[154:157], v246, v247 op_sel_hi:[0,0,0]
	v_mfma_scale_f32_16x16x128_f8f6f4 v[150:153], v[2:9], v[212:219], v[150:153], v246, v247 op_sel_hi:[0,0,0]
	v_mfma_scale_f32_16x16x128_f8f6f4 v[146:149], v[10:17], v[212:219], v[146:149], v246, v247 op_sel_hi:[0,0,0]
	v_mfma_scale_f32_16x16x128_f8f6f4 v[142:145], v[2:9], v[220:227], v[142:145], v246, v247 op_sel_hi:[0,0,0]
	v_mfma_scale_f32_16x16x128_f8f6f4 v[138:141], v[10:17], v[220:227], v[138:141], v246, v247 op_sel_hi:[0,0,0]
	v_mfma_scale_f32_16x16x128_f8f6f4 v[134:137], v[2:9], v[228:235], v[134:137], v246, v247 op_sel_hi:[0,0,0]
	v_mfma_scale_f32_16x16x128_f8f6f4 v[130:133], v[10:17], v[228:235], v[130:133], v246, v247 op_sel_hi:[0,0,0]
	s_setprio 0
	s_setprio 1
	v_mfma_scale_f32_16x16x128_f8f6f4 v[94:97], v[18:25], v[204:211], v[94:97], v246, v247 op_sel_hi:[0,0,0]
	v_mfma_scale_f32_16x16x128_f8f6f4 v[90:93], v[26:33], v[204:211], v[90:93], v246, v247 op_sel_hi:[0,0,0]
	v_mfma_scale_f32_16x16x128_f8f6f4 v[86:89], v[18:25], v[212:219], v[86:89], v246, v247 op_sel_hi:[0,0,0]
	v_mfma_scale_f32_16x16x128_f8f6f4 v[82:85], v[26:33], v[212:219], v[82:85], v246, v247 op_sel_hi:[0,0,0]
	v_mfma_scale_f32_16x16x128_f8f6f4 v[78:81], v[18:25], v[220:227], v[78:81], v246, v247 op_sel_hi:[0,0,0]
	v_mfma_scale_f32_16x16x128_f8f6f4 v[74:77], v[26:33], v[220:227], v[74:77], v246, v247 op_sel_hi:[0,0,0]
	v_mfma_scale_f32_16x16x128_f8f6f4 v[70:73], v[18:25], v[228:235], v[70:73], v246, v247 op_sel_hi:[0,0,0]
	v_mfma_scale_f32_16x16x128_f8f6f4 v[66:69], v[26:33], v[228:235], v[66:69], v246, v247 op_sel_hi:[0,0,0]
	s_setprio 0
	s_barrier
	ds_read_b128 v[204:207], v191 offset:49152
	ds_read_b128 v[208:211], v191 offset:50176
	ds_read_b128 v[212:215], v191 offset:51200
	ds_read_b128 v[216:219], v191 offset:52224
	ds_read_b128 v[220:223], v191 offset:53248
	ds_read_b128 v[224:227], v191 offset:54272
	ds_read_b128 v[228:231], v191 offset:55296
	ds_read_b128 v[232:235], v191 offset:56320
	s_add_i32 s6, s8, s41
	v_lshl_add_u64 v[176:177], v[176:177], 0, s[92:93]
	s_mov_b32 m0, s6
	s_nop 0
	global_load_lds_dwordx4 v[176:177], off
	v_lshl_add_u64 v[176:177], v[178:179], 0, s[92:93]
	s_add_i32 m0, s6, 0x2000
	s_add_i32 s6, s9, s41
	global_load_lds_dwordx4 v[176:177], off
	v_lshl_add_u64 v[176:177], v[180:181], 0, s[92:93]
	s_mov_b32 m0, s6
	s_nop 0
	global_load_lds_dwordx4 v[176:177], off
	v_lshl_add_u64 v[176:177], v[182:183], 0, s[92:93]
	s_add_i32 m0, s6, 0x2000
	s_nop 0
	global_load_lds_dwordx4 v[176:177], off
	v_lshl_add_u64 v[176:177], v[184:185], 0, s[92:93]
	s_mov_b32 m0, s91
	s_nop 0
	global_load_lds_dwordx4 v[176:177], off
	v_lshl_add_u64 v[176:177], v[186:187], 0, s[92:93]
	s_mov_b32 m0, s51
	s_nop 0
	global_load_lds_dwordx4 v[176:177], off
	s_waitcnt vmcnt(8)
	s_waitcnt lgkmcnt(0)
	s_barrier
	s_setprio 1
	s_waitcnt lgkmcnt(0)
	v_mfma_scale_f32_16x16x128_f8f6f4 v[126:129], v[2:9], v[204:211], v[126:129], v246, v247 op_sel_hi:[0,0,0]
	v_mfma_scale_f32_16x16x128_f8f6f4 v[122:125], v[10:17], v[204:211], v[122:125], v246, v247 op_sel_hi:[0,0,0]
	v_mfma_scale_f32_16x16x128_f8f6f4 v[118:121], v[2:9], v[212:219], v[118:121], v246, v247 op_sel_hi:[0,0,0]
	v_mfma_scale_f32_16x16x128_f8f6f4 v[114:117], v[10:17], v[212:219], v[114:117], v246, v247 op_sel_hi:[0,0,0]
	v_mfma_scale_f32_16x16x128_f8f6f4 v[110:113], v[2:9], v[220:227], v[110:113], v246, v247 op_sel_hi:[0,0,0]
	v_mfma_scale_f32_16x16x128_f8f6f4 v[106:109], v[10:17], v[220:227], v[106:109], v246, v247 op_sel_hi:[0,0,0]
	v_mfma_scale_f32_16x16x128_f8f6f4 v[102:105], v[2:9], v[228:235], v[102:105], v246, v247 op_sel_hi:[0,0,0]
	v_mfma_scale_f32_16x16x128_f8f6f4 v[98:101], v[10:17], v[228:235], v[98:101], v246, v247 op_sel_hi:[0,0,0]
	s_setprio 0
	s_setprio 1
	v_mfma_scale_f32_16x16x128_f8f6f4 v[62:65], v[18:25], v[204:211], v[62:65], v246, v247 op_sel_hi:[0,0,0]
	v_mfma_scale_f32_16x16x128_f8f6f4 v[58:61], v[26:33], v[204:211], v[58:61], v246, v247 op_sel_hi:[0,0,0]
	v_mfma_scale_f32_16x16x128_f8f6f4 v[54:57], v[18:25], v[212:219], v[54:57], v246, v247 op_sel_hi:[0,0,0]
	v_mfma_scale_f32_16x16x128_f8f6f4 v[50:53], v[26:33], v[212:219], v[50:53], v246, v247 op_sel_hi:[0,0,0]
	s_add_u32 s4, s4, 0x100
	s_addc_u32 s5, s5, 0
	s_add_u32 s12, s12, 0x100
	s_addc_u32 s13, s13, 0
	s_cmp_ge_i32 s14, s84
	s_mov_b32 s6, s14
	v_mfma_scale_f32_16x16x128_f8f6f4 v[46:49], v[18:25], v[220:227], v[46:49], v246, v247 op_sel_hi:[0,0,0]
	v_mfma_scale_f32_16x16x128_f8f6f4 v[42:45], v[26:33], v[220:227], v[42:45], v246, v247 op_sel_hi:[0,0,0]
	v_mfma_scale_f32_16x16x128_f8f6f4 v[38:41], v[18:25], v[228:235], v[38:41], v246, v247 op_sel_hi:[0,0,0]
	v_mfma_scale_f32_16x16x128_f8f6f4 v[34:37], v[26:33], v[228:235], v[34:37], v246, v247 op_sel_hi:[0,0,0]
	s_setprio 0
	s_barrier
	s_cbranch_scc0 .LBB0_51

; template <class Epi, class Sched, bool ALIGN_EPI = false, bool SP2 = false, bool F8 = false>
; __device__ __forceinline__ void gemm_phase(PG8_LAS unsigned char* lds, const Gemm g, const Sched& S, const Epi& E, const int tidb  ) {
;     ...
; #pragma unroll
;         for (int a = 0; a < 2; ++a)
; #pragma unroll
;             for (int b = 0; b < 2; ++b)
; #pragma unroll
;                 for (int m = 0; m < 4; ++m)
; #pragma unroll
;                     for (int n = 0; n < 2; ++n) acc[a][b][m][n] = (f32x4){0.f, 0.f, 0.f, 0.f};
;         cur = nxt; cA = nA; cB = nB; ++ui;
.LBB0_391:
	v_mov_b32_e32 v125, 0
	s_andn2_b64 vcc, exec, s[16:17]
	v_mov_b32_e32 v124, v125
	v_mov_b32_e32 v123, v125
	v_mov_b32_e32 v122, v125
	v_mov_b32_e32 v129, v125
	v_mov_b32_e32 v128, v125
	v_mov_b32_e32 v127, v125
	v_mov_b32_e32 v126, v125
	v_mov_b32_e32 v121, v125
	v_mov_b32_e32 v120, v125
	v_mov_b32_e32 v119, v125
	v_mov_b32_e32 v118, v125
	v_mov_b32_e32 v117, v125
	v_mov_b32_e32 v116, v125
	v_mov_b32_e32 v115, v125
	v_mov_b32_e32 v114, v125
	v_mov_b32_e32 v113, v125
	v_mov_b32_e32 v112, v125
	v_mov_b32_e32 v111, v125
	v_mov_b32_e32 v110, v125
	v_mov_b32_e32 v109, v125
	v_mov_b32_e32 v108, v125
	v_mov_b32_e32 v107, v125
	v_mov_b32_e32 v106, v125
	v_mov_b32_e32 v105, v125
	v_mov_b32_e32 v104, v125
	v_mov_b32_e32 v103, v125
	v_mov_b32_e32 v102, v125
	v_mov_b32_e32 v101, v125
	v_mov_b32_e32 v100, v125
	v_mov_b32_e32 v99, v125
	v_mov_b32_e32 v98, v125
	v_mov_b32_e32 v65, v125
	v_mov_b32_e32 v64, v125
	v_mov_b32_e32 v63, v125
	v_mov_b32_e32 v62, v125
	v_mov_b32_e32 v61, v125
	v_mov_b32_e32 v60, v125
	v_mov_b32_e32 v59, v125
	v_mov_b32_e32 v58, v125
	v_mov_b32_e32 v57, v125
	v_mov_b32_e32 v56, v125
	v_mov_b32_e32 v55, v125
	v_mov_b32_e32 v54, v125
	v_mov_b32_e32 v53, v125
	v_mov_b32_e32 v52, v125
	v_mov_b32_e32 v51, v125
	v_mov_b32_e32 v50, v125
	v_mov_b32_e32 v49, v125
	v_mov_b32_e32 v48, v125
	v_mov_b32_e32 v47, v125
	v_mov_b32_e32 v46, v125
	v_mov_b32_e32 v45, v125
	v_mov_b32_e32 v44, v125
	v_mov_b32_e32 v43, v125
	v_mov_b32_e32 v42, v125
	v_mov_b32_e32 v41, v125
	v_mov_b32_e32 v40, v125
	v_mov_b32_e32 v39, v125
	v_mov_b32_e32 v38, v125
	v_mov_b32_e32 v37, v125
	v_mov_b32_e32 v36, v125
	v_mov_b32_e32 v35, v125
	v_mov_b32_e32 v34, v125
	v_mov_b32_e32 v97, v125
	v_mov_b32_e32 v96, v125
	v_mov_b32_e32 v95, v125
	v_mov_b32_e32 v94, v125
	v_mov_b32_e32 v93, v125
	v_mov_b32_e32 v92, v125
	v_mov_b32_e32 v91, v125
	v_mov_b32_e32 v90, v125
	v_mov_b32_e32 v89, v125
	v_mov_b32_e32 v88, v125
	v_mov_b32_e32 v87, v125
	v_mov_b32_e32 v86, v125
	v_mov_b32_e32 v85, v125
	v_mov_b32_e32 v84, v125
	v_mov_b32_e32 v83, v125
	v_mov_b32_e32 v82, v125
	v_mov_b32_e32 v81, v125
	v_mov_b32_e32 v80, v125
	v_mov_b32_e32 v79, v125
	v_mov_b32_e32 v78, v125
	v_mov_b32_e32 v77, v125
	v_mov_b32_e32 v76, v125
	v_mov_b32_e32 v75, v125
	v_mov_b32_e32 v74, v125
	v_mov_b32_e32 v73, v125
	v_mov_b32_e32 v72, v125
	v_mov_b32_e32 v71, v125
	v_mov_b32_e32 v70, v125
	v_mov_b32_e32 v69, v125
	v_mov_b32_e32 v68, v125
	v_mov_b32_e32 v67, v125
	v_mov_b32_e32 v66, v125
	v_mov_b32_e32 v33, v125
	v_mov_b32_e32 v32, v125
	v_mov_b32_e32 v31, v125
	v_mov_b32_e32 v30, v125
	v_mov_b32_e32 v29, v125
	v_mov_b32_e32 v28, v125
	v_mov_b32_e32 v27, v125
	v_mov_b32_e32 v26, v125
	v_mov_b32_e32 v25, v125
	v_mov_b32_e32 v24, v125
	v_mov_b32_e32 v23, v125
	v_mov_b32_e32 v22, v125
	v_mov_b32_e32 v21, v125
	v_mov_b32_e32 v20, v125
	v_mov_b32_e32 v19, v125
	v_mov_b32_e32 v18, v125
	v_mov_b32_e32 v17, v125
	v_mov_b32_e32 v16, v125
	v_mov_b32_e32 v15, v125
	v_mov_b32_e32 v14, v125
	v_mov_b32_e32 v13, v125
	v_mov_b32_e32 v12, v125
	v_mov_b32_e32 v11, v125
	v_mov_b32_e32 v10, v125
	v_mov_b32_e32 v9, v125
	v_mov_b32_e32 v8, v125
	v_mov_b32_e32 v7, v125
	v_mov_b32_e32 v6, v125
	v_mov_b32_e32 v5, v125
	v_mov_b32_e32 v4, v125
	v_mov_b32_e32 v3, v125
	v_mov_b32_e32 v2, v125
	s_cbranch_vccnz .LBB0_395
	s_add_u32 s4, s30, 0x80
	s_addc_u32 s5, s31, 0
	s_add_u32 s30, s28, 0x100
	v_mov_b32_e32 v2, 0
	s_addc_u32 s31, s29, 0
	s_mov_b32 s28, 0
	v_mov_b32_e32 v3, v2
	v_mov_b32_e32 v4, v2
	v_mov_b32_e32 v5, v2
	v_mov_b32_e32 v6, v2
	v_mov_b32_e32 v7, v2
	v_mov_b32_e32 v8, v2
	v_mov_b32_e32 v9, v2
	v_mov_b32_e32 v10, v2
	v_mov_b32_e32 v11, v2
	v_mov_b32_e32 v12, v2
	v_mov_b32_e32 v13, v2
	v_mov_b32_e32 v14, v2
	v_mov_b32_e32 v15, v2
	v_mov_b32_e32 v16, v2
	v_mov_b32_e32 v17, v2
	v_mov_b32_e32 v18, v2
	v_mov_b32_e32 v19, v2
	v_mov_b32_e32 v20, v2
	v_mov_b32_e32 v21, v2
	v_mov_b32_e32 v22, v2
	v_mov_b32_e32 v23, v2
	v_mov_b32_e32 v24, v2
	v_mov_b32_e32 v25, v2
	v_mov_b32_e32 v26, v2
	v_mov_b32_e32 v27, v2
	v_mov_b32_e32 v28, v2
	v_mov_b32_e32 v29, v2
	v_mov_b32_e32 v30, v2
	v_mov_b32_e32 v31, v2
	v_mov_b32_e32 v32, v2
	v_mov_b32_e32 v33, v2
	v_mov_b32_e32 v66, v2
	v_mov_b32_e32 v67, v2
	v_mov_b32_e32 v68, v2
	v_mov_b32_e32 v69, v2
	v_mov_b32_e32 v70, v2
	v_mov_b32_e32 v71, v2
	v_mov_b32_e32 v72, v2
	v_mov_b32_e32 v73, v2
	v_mov_b32_e32 v74, v2
	v_mov_b32_e32 v75, v2
	v_mov_b32_e32 v76, v2
	v_mov_b32_e32 v77, v2
	v_mov_b32_e32 v78, v2
	v_mov_b32_e32 v79, v2
	v_mov_b32_e32 v80, v2
	v_mov_b32_e32 v81, v2
	v_mov_b32_e32 v82, v2
	v_mov_b32_e32 v83, v2
	v_mov_b32_e32 v84, v2
	v_mov_b32_e32 v85, v2
	v_mov_b32_e32 v86, v2
	v_mov_b32_e32 v87, v2
	v_mov_b32_e32 v88, v2
	v_mov_b32_e32 v89, v2
	v_mov_b32_e32 v90, v2
	v_mov_b32_e32 v91, v2
	v_mov_b32_e32 v92, v2
	v_mov_b32_e32 v93, v2
	v_mov_b32_e32 v94, v2
	v_mov_b32_e32 v95, v2
	v_mov_b32_e32 v96, v2
	v_mov_b32_e32 v97, v2
	v_mov_b32_e32 v34, v2
	v_mov_b32_e32 v35, v2
	v_mov_b32_e32 v36, v2
	v_mov_b32_e32 v37, v2
	v_mov_b32_e32 v38, v2
	v_mov_b32_e32 v39, v2
	v_mov_b32_e32 v40, v2
	v_mov_b32_e32 v41, v2
	v_mov_b32_e32 v42, v2
	v_mov_b32_e32 v43, v2
	v_mov_b32_e32 v44, v2
	v_mov_b32_e32 v45, v2
	v_mov_b32_e32 v46, v2
	v_mov_b32_e32 v47, v2
	v_mov_b32_e32 v48, v2
	v_mov_b32_e32 v49, v2
	v_mov_b32_e32 v50, v2
	v_mov_b32_e32 v51, v2
	v_mov_b32_e32 v52, v2
	v_mov_b32_e32 v53, v2
	v_mov_b32_e32 v54, v2
	v_mov_b32_e32 v55, v2
	v_mov_b32_e32 v56, v2
	v_mov_b32_e32 v57, v2
	v_mov_b32_e32 v58, v2
	v_mov_b32_e32 v59, v2
	v_mov_b32_e32 v60, v2
	v_mov_b32_e32 v61, v2
	v_mov_b32_e32 v62, v2
	v_mov_b32_e32 v63, v2
	v_mov_b32_e32 v64, v2
	v_mov_b32_e32 v65, v2
	v_mov_b32_e32 v98, v2
	v_mov_b32_e32 v99, v2
	v_mov_b32_e32 v100, v2
	v_mov_b32_e32 v101, v2
	v_mov_b32_e32 v102, v2
	v_mov_b32_e32 v103, v2
	v_mov_b32_e32 v104, v2
	v_mov_b32_e32 v105, v2
	v_mov_b32_e32 v106, v2
	v_mov_b32_e32 v107, v2
	v_mov_b32_e32 v108, v2
	v_mov_b32_e32 v109, v2
	v_mov_b32_e32 v110, v2
	v_mov_b32_e32 v111, v2
	v_mov_b32_e32 v112, v2
	v_mov_b32_e32 v113, v2
	v_mov_b32_e32 v114, v2
	v_mov_b32_e32 v115, v2
	v_mov_b32_e32 v116, v2
	v_mov_b32_e32 v117, v2
	v_mov_b32_e32 v118, v2
	v_mov_b32_e32 v119, v2
	v_mov_b32_e32 v120, v2
	v_mov_b32_e32 v121, v2
	v_mov_b32_e32 v126, v2
	v_mov_b32_e32 v127, v2
	v_mov_b32_e32 v128, v2
	v_mov_b32_e32 v129, v2
	v_mov_b32_e32 v122, v2
	v_mov_b32_e32 v123, v2
	v_mov_b32_e32 v124, v2
	v_mov_b32_e32 v125, v2
	s_waitcnt vmcnt(0)
; #define PG8_STAGE(bufoff, gbase, voff) do { _Pragma("unroll") for (int _i = 0; _i < 2; ++_i) \
;         __builtin_amdgcn_global_load_lds((const unsigned*)((const char*)(gbase) + (voff)[_i]), (PG8_LAS unsigned*)(lds + (bufoff) + ldsw + _i * 8192), 16, 0, 0); } while (0)
; #define PG8_WAIT_V(n) asm volatile("s_waitcnt vmcnt(" #n ")" ::: "memory")
; #define PG8_WAIT_L(n) asm volatile("s_waitcnt lgkmcnt(" #n ")" ::: "memory")
; #define PG8_BAR __builtin_amdgcn_s_barrier()
; #define PG8_SCHED __builtin_amdgcn_sched_barrier(0)
; template <class Epi, class Sched, bool ALIGN_EPI = false, bool SP2 = false, bool F8 = false>
; __device__ __forceinline__ void gemm_phase(PG8_LAS unsigned char* lds, const Gemm g, const Sched& S, const Epi& E, const int tidb  ) {
;     ...
;         for (int t = 0; t < nt; t += 2) {
;             const bool last = (t == nt - 2);
;             if constexpr (Epi::PREFETCH) { if (t == 0) E.prefetch(cur, wid, lane); }
;             const char* a1 = cA + (size_t)(t + 1) * kstep;
;             const char* a2 = last ? nA : cA + (size_t)(t + 2) * kstep; const char* b2 = last ? nB : cB + (size_t)(t + 2) * kstep;
;             const char* a3 = a2 + kstep; const char* b3 = b2 + kstep;
;             if (last && has_next) S.a_ready(nxt);
;             if constexpr (SP2) {
;             PG8_LDB(B0, 0, 0); PG8_LDB(B1, 0, 1); PG8_SCHED; PG8_LDA(At, 0, 0); PG8_STAGE(PG8_SA(1, 1), a1 + hstep, voffA);
;             PG8_WAIT_V(8); PG8_WAIT_L(0); PG8_BAR; PG8_MMA(0, 0, At, B0); PG8_MMA(0, 1, At, B1); PG8_BAR; PG8_SCHED;
;             PG8_LDA(At, 0, 1); PG8_STAGE(PG8_SB(0, 0), b2, voffB); PG8_STAGE(PG8_SB(0, 1), b2 + hstep, voffB); PG8_STAGE(PG8_SA(0, 0), a2, voffA);
;             PG8_WAIT_V(8); PG8_WAIT_L(0); PG8_BAR; PG8_MMA(1, 0, At, B0); PG8_MMA(1, 1, At, B1); PG8_BAR; PG8_SCHED;
.LBB0_393:
	s_add_i32 s68, 0, 0x10000
	v_add_u32_e32 v0, s68, v152
	ds_read_b128 v[158:161], v0
	ds_read_b128 v[164:167], v0 offset:1024
	ds_read_b128 v[168:171], v0 offset:2048
	ds_read_b128 v[172:175], v0 offset:3072
	s_add_i32 s63, s28, 2
	s_add_u32 s65, s4, 0x80
	s_addc_u32 s29, s5, 0
	s_cmp_eq_u32 s55, s28
	s_cselect_b32 s29, s25, s29
	s_cselect_b32 s28, s24, s65
	s_cselect_b32 s67, s27, s31
	s_cselect_b32 s66, s26, s30
	s_add_i32 s65, 0, 0x14000
	v_add_u32_e32 v0, s65, v152
	ds_read_b128 v[176:179], v0
	ds_read_b128 v[180:183], v0 offset:1024
	ds_read_b128 v[184:187], v0 offset:2048
	ds_read_b128 v[188:191], v0 offset:3072
	v_lshl_add_u64 v[148:149], s[4:5], 0, v[144:145]
	s_add_i32 m0, s46, 0xc000
	ds_read_b128 v[192:195], v156
	ds_read_b128 v[204:207], v156 offset:1024
	ds_read_b128 v[208:211], v156 offset:2048
	ds_read_b128 v[212:215], v156 offset:3072
	ds_read_b128 v[216:219], v156 offset:4096
	ds_read_b128 v[220:223], v156 offset:5120
	ds_read_b128 v[224:227], v156 offset:6144
	ds_read_b128 v[228:231], v156 offset:7168
	global_load_lds_dwordx4 v[148:149], off
	v_lshl_add_u64 v[148:149], s[4:5], 0, v[146:147]
	s_add_i32 m0, s46, 0xe000
	s_nop 0
	global_load_lds_dwordx4 v[148:149], off
	s_waitcnt vmcnt(8)
	s_waitcnt lgkmcnt(0)
	s_barrier
	s_setprio 1
	s_waitcnt lgkmcnt(0)
	v_mfma_f32_16x16x32_bf16 v[122:125], v[158:161], v[192:195], v[122:125]
	v_mfma_f32_16x16x32_bf16 v[126:129], v[168:171], v[192:195], v[126:129]
	v_mfma_f32_16x16x32_bf16 v[118:121], v[158:161], v[208:211], v[118:121]
	v_mfma_f32_16x16x32_bf16 v[114:117], v[168:171], v[208:211], v[114:117]
	v_mfma_f32_16x16x32_bf16 v[110:113], v[158:161], v[216:219], v[110:113]
	v_mfma_f32_16x16x32_bf16 v[106:109], v[168:171], v[216:219], v[106:109]
	v_mfma_f32_16x16x32_bf16 v[102:105], v[158:161], v[224:227], v[102:105]
	v_mfma_f32_16x16x32_bf16 v[98:101], v[168:171], v[224:227], v[98:101]
	v_mfma_f32_16x16x32_bf16 v[122:125], v[164:167], v[204:207], v[122:125]
	v_mfma_f32_16x16x32_bf16 v[126:129], v[172:175], v[204:207], v[126:129]
	v_mfma_f32_16x16x32_bf16 v[118:121], v[164:167], v[212:215], v[118:121]
	v_mfma_f32_16x16x32_bf16 v[114:117], v[172:175], v[212:215], v[114:117]
	v_mfma_f32_16x16x32_bf16 v[110:113], v[164:167], v[220:223], v[110:113]
	v_mfma_f32_16x16x32_bf16 v[106:109], v[172:175], v[220:223], v[106:109]
	v_mfma_f32_16x16x32_bf16 v[102:105], v[164:167], v[228:231], v[102:105]
	v_mfma_f32_16x16x32_bf16 v[98:101], v[172:175], v[228:231], v[98:101]
	s_setprio 0
	s_setprio 1
	v_mfma_f32_16x16x32_bf16 v[62:65], v[176:179], v[192:195], v[62:65]
	v_mfma_f32_16x16x32_bf16 v[58:61], v[184:187], v[192:195], v[58:61]
	v_mfma_f32_16x16x32_bf16 v[54:57], v[176:179], v[208:211], v[54:57]
	v_mfma_f32_16x16x32_bf16 v[50:53], v[184:187], v[208:211], v[50:53]
	v_mfma_f32_16x16x32_bf16 v[46:49], v[176:179], v[216:219], v[46:49]
	v_mfma_f32_16x16x32_bf16 v[42:45], v[184:187], v[216:219], v[42:45]
	v_mfma_f32_16x16x32_bf16 v[38:41], v[176:179], v[224:227], v[38:41]
	v_mfma_f32_16x16x32_bf16 v[34:37], v[184:187], v[224:227], v[34:37]
	v_mfma_f32_16x16x32_bf16 v[62:65], v[180:183], v[204:207], v[62:65]
	v_mfma_f32_16x16x32_bf16 v[58:61], v[188:191], v[204:207], v[58:61]
	v_mfma_f32_16x16x32_bf16 v[54:57], v[180:183], v[212:215], v[54:57]
	v_mfma_f32_16x16x32_bf16 v[50:53], v[188:191], v[212:215], v[50:53]
	v_mfma_f32_16x16x32_bf16 v[46:49], v[180:183], v[220:223], v[46:49]
	v_mfma_f32_16x16x32_bf16 v[42:45], v[188:191], v[220:223], v[42:45]
	v_mfma_f32_16x16x32_bf16 v[38:41], v[180:183], v[228:231], v[38:41]
	v_mfma_f32_16x16x32_bf16 v[34:37], v[188:191], v[228:231], v[34:37]
	s_setprio 0
	s_barrier
	ds_read_b128 v[192:195], v156 offset:16384
	ds_read_b128 v[204:207], v156 offset:17408
	ds_read_b128 v[208:211], v156 offset:18432
	ds_read_b128 v[212:215], v156 offset:19456
	ds_read_b128 v[216:219], v156 offset:20480
	ds_read_b128 v[220:223], v156 offset:21504
	ds_read_b128 v[224:227], v156 offset:22528
	ds_read_b128 v[228:231], v156 offset:23552
	s_add_i32 s68, s68, s45
	v_lshl_add_u64 v[148:149], s[66:67], 0, v[132:133]
	s_mov_b32 m0, s68
	s_nop 0
	global_load_lds_dwordx4 v[148:149], off
	s_add_i32 m0, s68, 0x2000
	v_lshl_add_u64 v[196:197], s[66:67], 0, v[136:137]
	s_add_u32 s66, s66, s10
	s_addc_u32 s67, s67, s11
	s_add_i32 s65, s65, s45
	global_load_lds_dwordx4 v[196:197], off
	v_lshl_add_u64 v[200:201], s[66:67], 0, v[132:133]
	s_mov_b32 m0, s65
	v_lshl_add_u64 v[232:233], s[66:67], 0, v[136:137]
	global_load_lds_dwordx4 v[200:201], off
	s_add_i32 m0, s65, 0x2000
	v_lshl_add_u64 v[234:235], s[28:29], 0, v[130:131]
	global_load_lds_dwordx4 v[232:233], off
	s_mov_b32 m0, s46
	v_lshl_add_u64 v[236:237], s[28:29], 0, v[134:135]
	global_load_lds_dwordx4 v[234:235], off
	s_mov_b32 m0, s47
	s_nop 0
	global_load_lds_dwordx4 v[236:237], off
	s_waitcnt vmcnt(8)
	s_waitcnt lgkmcnt(0)
	s_barrier
; #define PG8_STAGE(bufoff, gbase, voff) do { _Pragma("unroll") for (int _i = 0; _i < 2; ++_i) \
;         __builtin_amdgcn_global_load_lds((const unsigned*)((const char*)(gbase) + (voff)[_i]), (PG8_LAS unsigned*)(lds + (bufoff) + ldsw + _i * 8192), 16, 0, 0); } while (0)
; #define PG8_WAIT_V(n) asm volatile("s_waitcnt vmcnt(" #n ")" ::: "memory")
; #define PG8_WAIT_L(n) asm volatile("s_waitcnt lgkmcnt(" #n ")" ::: "memory")
; #define PG8_BAR __builtin_amdgcn_s_barrier()
; #define PG8_SCHED __builtin_amdgcn_sched_barrier(0)
; template <class Epi, class Sched, bool ALIGN_EPI = false, bool SP2 = false, bool F8 = false>
; __device__ __forceinline__ void gemm_phase(PG8_LAS unsigned char* lds, const Gemm g, const Sched& S, const Epi& E, const int tidb  ) {
;     ...
;             PG8_WAIT_V(8); PG8_WAIT_L(0); PG8_BAR; PG8_MMA(1, 0, At, B0); PG8_MMA(1, 1, At, B1); PG8_BAR; PG8_SCHED;
;             PG8_LDB(B0, 1, 0); PG8_LDB(B1, 1, 1); PG8_SCHED; PG8_LDA(At, 1, 0); PG8_STAGE(PG8_SA(0, 1), a2 + hstep, voffA);
;             PG8_WAIT_V(8); PG8_WAIT_L(0); PG8_BAR; PG8_MMA(0, 0, At, B0); PG8_MMA(0, 1, At, B1); PG8_BAR; PG8_SCHED;
	s_setprio 1
	s_waitcnt lgkmcnt(0)
	v_mfma_f32_16x16x32_bf16 v[94:97], v[158:161], v[192:195], v[94:97]
	v_mfma_f32_16x16x32_bf16 v[90:93], v[168:171], v[192:195], v[90:93]
	v_mfma_f32_16x16x32_bf16 v[86:89], v[158:161], v[208:211], v[86:89]
	v_mfma_f32_16x16x32_bf16 v[82:85], v[168:171], v[208:211], v[82:85]
	v_mfma_f32_16x16x32_bf16 v[78:81], v[158:161], v[216:219], v[78:81]
	v_mfma_f32_16x16x32_bf16 v[74:77], v[168:171], v[216:219], v[74:77]
	v_mfma_f32_16x16x32_bf16 v[70:73], v[158:161], v[224:227], v[70:73]
	v_mfma_f32_16x16x32_bf16 v[66:69], v[168:171], v[224:227], v[66:69]
	v_mfma_f32_16x16x32_bf16 v[94:97], v[164:167], v[204:207], v[94:97]
	v_mfma_f32_16x16x32_bf16 v[90:93], v[172:175], v[204:207], v[90:93]
	v_mfma_f32_16x16x32_bf16 v[86:89], v[164:167], v[212:215], v[86:89]
	v_mfma_f32_16x16x32_bf16 v[82:85], v[172:175], v[212:215], v[82:85]
	v_mfma_f32_16x16x32_bf16 v[78:81], v[164:167], v[220:223], v[78:81]
	v_mfma_f32_16x16x32_bf16 v[74:77], v[172:175], v[220:223], v[74:77]
	v_mfma_f32_16x16x32_bf16 v[70:73], v[164:167], v[228:231], v[70:73]
	v_mfma_f32_16x16x32_bf16 v[66:69], v[172:175], v[228:231], v[66:69]
	s_setprio 0
	s_setprio 1
	v_mfma_f32_16x16x32_bf16 v[30:33], v[176:179], v[192:195], v[30:33]
	v_mfma_f32_16x16x32_bf16 v[26:29], v[184:187], v[192:195], v[26:29]
	v_mfma_f32_16x16x32_bf16 v[22:25], v[176:179], v[208:211], v[22:25]
	v_mfma_f32_16x16x32_bf16 v[18:21], v[184:187], v[208:211], v[18:21]
	v_mfma_f32_16x16x32_bf16 v[14:17], v[176:179], v[216:219], v[14:17]
	v_mfma_f32_16x16x32_bf16 v[10:13], v[184:187], v[216:219], v[10:13]
	v_mfma_f32_16x16x32_bf16 v[6:9], v[176:179], v[224:227], v[6:9]
	v_mfma_f32_16x16x32_bf16 v[2:5], v[184:187], v[224:227], v[2:5]
	v_mfma_f32_16x16x32_bf16 v[30:33], v[180:183], v[204:207], v[30:33]
	v_mfma_f32_16x16x32_bf16 v[26:29], v[188:191], v[204:207], v[26:29]
	v_mfma_f32_16x16x32_bf16 v[22:25], v[180:183], v[212:215], v[22:25]
	v_mfma_f32_16x16x32_bf16 v[18:21], v[188:191], v[212:215], v[18:21]
	v_mfma_f32_16x16x32_bf16 v[14:17], v[180:183], v[220:223], v[14:17]
	v_mfma_f32_16x16x32_bf16 v[10:13], v[188:191], v[220:223], v[10:13]
	v_mfma_f32_16x16x32_bf16 v[6:9], v[180:183], v[228:231], v[6:9]
	v_mfma_f32_16x16x32_bf16 v[2:5], v[188:191], v[228:231], v[2:5]
	s_setprio 0
	s_barrier
	s_add_i32 s65, 0, 0x18000
	v_add_u32_e32 v0, s65, v152
	s_add_i32 s66, 0, 0x1c000
	ds_read_b128 v[158:161], v0
	ds_read_b128 v[164:167], v0 offset:1024
	ds_read_b128 v[168:171], v0 offset:2048
	ds_read_b128 v[172:175], v0 offset:3072
	v_add_u32_e32 v0, s66, v152
	ds_read_b128 v[176:179], v0
	ds_read_b128 v[180:183], v0 offset:1024
	ds_read_b128 v[184:187], v0 offset:2048
	ds_read_b128 v[188:191], v0 offset:3072
	s_add_u32 s28, s28, s10
	s_addc_u32 s29, s29, s11
	s_mov_b32 m0, s48
	v_lshl_add_u64 v[238:239], s[28:29], 0, v[130:131]
	ds_read_b128 v[192:195], v156 offset:32768
	ds_read_b128 v[204:207], v156 offset:33792
	ds_read_b128 v[208:211], v156 offset:34816
	ds_read_b128 v[212:215], v156 offset:35840
	ds_read_b128 v[216:219], v156 offset:36864
	ds_read_b128 v[220:223], v156 offset:37888
	ds_read_b128 v[224:227], v156 offset:38912
	ds_read_b128 v[228:231], v156 offset:39936
	global_load_lds_dwordx4 v[238:239], off
	v_lshl_add_u64 v[238:239], s[28:29], 0, v[134:135]
	s_mov_b32 m0, s49
	s_nop 0
	global_load_lds_dwordx4 v[238:239], off
	s_waitcnt vmcnt(8)
	s_waitcnt lgkmcnt(0)
	s_barrier
	s_setprio 1
	s_waitcnt lgkmcnt(0)
	v_mfma_f32_16x16x32_bf16 v[122:125], v[158:161], v[192:195], v[122:125]
	v_mfma_f32_16x16x32_bf16 v[126:129], v[168:171], v[192:195], v[126:129]
	v_mfma_f32_16x16x32_bf16 v[118:121], v[158:161], v[208:211], v[118:121]
	v_mfma_f32_16x16x32_bf16 v[114:117], v[168:171], v[208:211], v[114:117]
	v_mfma_f32_16x16x32_bf16 v[110:113], v[158:161], v[216:219], v[110:113]
	v_mfma_f32_16x16x32_bf16 v[106:109], v[168:171], v[216:219], v[106:109]
	v_mfma_f32_16x16x32_bf16 v[102:105], v[158:161], v[224:227], v[102:105]
	v_mfma_f32_16x16x32_bf16 v[98:101], v[168:171], v[224:227], v[98:101]
	v_mfma_f32_16x16x32_bf16 v[122:125], v[164:167], v[204:207], v[122:125]
	v_mfma_f32_16x16x32_bf16 v[126:129], v[172:175], v[204:207], v[126:129]
	v_mfma_f32_16x16x32_bf16 v[118:121], v[164:167], v[212:215], v[118:121]
	v_mfma_f32_16x16x32_bf16 v[114:117], v[172:175], v[212:215], v[114:117]
	v_mfma_f32_16x16x32_bf16 v[110:113], v[164:167], v[220:223], v[110:113]
	v_mfma_f32_16x16x32_bf16 v[106:109], v[172:175], v[220:223], v[106:109]
	v_mfma_f32_16x16x32_bf16 v[102:105], v[164:167], v[228:231], v[102:105]
	v_mfma_f32_16x16x32_bf16 v[98:101], v[172:175], v[228:231], v[98:101]
	s_setprio 0
	s_setprio 1
	v_mfma_f32_16x16x32_bf16 v[62:65], v[176:179], v[192:195], v[62:65]
	v_mfma_f32_16x16x32_bf16 v[58:61], v[184:187], v[192:195], v[58:61]
	v_mfma_f32_16x16x32_bf16 v[54:57], v[176:179], v[208:211], v[54:57]
	v_mfma_f32_16x16x32_bf16 v[50:53], v[184:187], v[208:211], v[50:53]
	v_mfma_f32_16x16x32_bf16 v[46:49], v[176:179], v[216:219], v[46:49]
	v_mfma_f32_16x16x32_bf16 v[42:45], v[184:187], v[216:219], v[42:45]
	v_mfma_f32_16x16x32_bf16 v[38:41], v[176:179], v[224:227], v[38:41]
	v_mfma_f32_16x16x32_bf16 v[34:37], v[184:187], v[224:227], v[34:37]
	v_mfma_f32_16x16x32_bf16 v[62:65], v[180:183], v[204:207], v[62:65]
	v_mfma_f32_16x16x32_bf16 v[58:61], v[188:191], v[204:207], v[58:61]
	v_mfma_f32_16x16x32_bf16 v[54:57], v[180:183], v[212:215], v[54:57]
	v_mfma_f32_16x16x32_bf16 v[50:53], v[188:191], v[212:215], v[50:53]
	v_mfma_f32_16x16x32_bf16 v[46:49], v[180:183], v[220:223], v[46:49]
	v_mfma_f32_16x16x32_bf16 v[42:45], v[188:191], v[220:223], v[42:45]
	v_mfma_f32_16x16x32_bf16 v[38:41], v[180:183], v[228:231], v[38:41]
	v_mfma_f32_16x16x32_bf16 v[34:37], v[188:191], v[228:231], v[34:37]
	s_setprio 0
	s_barrier
; #define PG8_STAGE(bufoff, gbase, voff) do { _Pragma("unroll") for (int _i = 0; _i < 2; ++_i) \
;         __builtin_amdgcn_global_load_lds((const unsigned*)((const char*)(gbase) + (voff)[_i]), (PG8_LAS unsigned*)(lds + (bufoff) + ldsw + _i * 8192), 16, 0, 0); } while (0)
; #define PG8_WAIT_V(n) asm volatile("s_waitcnt vmcnt(" #n ")" ::: "memory")
; #define PG8_WAIT_L(n) asm volatile("s_waitcnt lgkmcnt(" #n ")" ::: "memory")
; #define PG8_BAR __builtin_amdgcn_s_barrier()
; #define PG8_SCHED __builtin_amdgcn_sched_barrier(0)
; template <class Epi, class Sched, bool ALIGN_EPI = false, bool SP2 = false, bool F8 = false>
; __device__ __forceinline__ void gemm_phase(PG8_LAS unsigned char* lds, const Gemm g, const Sched& S, const Epi& E, const int tidb  ) {
;     ...
;             PG8_LDA(At, 1, 1); PG8_STAGE(PG8_SB(1, 0), b3, voffB); PG8_STAGE(PG8_SB(1, 1), b3 + hstep, voffB); PG8_STAGE(PG8_SA(1, 0), a3, voffA);
;             PG8_WAIT_V(8); PG8_WAIT_L(0); PG8_BAR; PG8_MMA(1, 0, At, B0); PG8_MMA(1, 1, At, B1); PG8_BAR; PG8_SCHED;
	ds_read_b128 v[192:195], v156 offset:49152
	ds_read_b128 v[204:207], v156 offset:50176
	ds_read_b128 v[208:211], v156 offset:51200
	ds_read_b128 v[212:215], v156 offset:52224
	ds_read_b128 v[216:219], v156 offset:53248
	ds_read_b128 v[220:223], v156 offset:54272
	ds_read_b128 v[224:227], v156 offset:55296
	ds_read_b128 v[228:231], v156 offset:56320
	s_add_i32 s28, s65, s45
	v_lshl_add_u64 v[148:149], v[148:149], 0, s[92:93]
	s_mov_b32 m0, s28
	s_nop 0
	global_load_lds_dwordx4 v[148:149], off
	v_lshl_add_u64 v[148:149], v[196:197], 0, s[92:93]
	s_add_i32 m0, s28, 0x2000
	s_add_i32 s28, s66, s45
	global_load_lds_dwordx4 v[148:149], off
	v_lshl_add_u64 v[148:149], v[200:201], 0, s[92:93]
	s_mov_b32 m0, s28
	s_nop 0
	global_load_lds_dwordx4 v[148:149], off
	v_lshl_add_u64 v[148:149], v[232:233], 0, s[92:93]
	s_add_i32 m0, s28, 0x2000
	s_nop 0
	global_load_lds_dwordx4 v[148:149], off
	v_lshl_add_u64 v[148:149], v[234:235], 0, s[92:93]
	s_mov_b32 m0, s50
	s_nop 0
	global_load_lds_dwordx4 v[148:149], off
	v_lshl_add_u64 v[148:149], v[236:237], 0, s[92:93]
	s_mov_b32 m0, s51
	s_nop 0
	global_load_lds_dwordx4 v[148:149], off
	s_waitcnt vmcnt(8)
	s_waitcnt lgkmcnt(0)
	s_barrier
	s_setprio 1
	s_waitcnt lgkmcnt(0)
	v_mfma_f32_16x16x32_bf16 v[94:97], v[158:161], v[192:195], v[94:97]
	v_mfma_f32_16x16x32_bf16 v[90:93], v[168:171], v[192:195], v[90:93]
	v_mfma_f32_16x16x32_bf16 v[86:89], v[158:161], v[208:211], v[86:89]
	v_mfma_f32_16x16x32_bf16 v[82:85], v[168:171], v[208:211], v[82:85]
	v_mfma_f32_16x16x32_bf16 v[78:81], v[158:161], v[216:219], v[78:81]
	v_mfma_f32_16x16x32_bf16 v[74:77], v[168:171], v[216:219], v[74:77]
	v_mfma_f32_16x16x32_bf16 v[70:73], v[158:161], v[224:227], v[70:73]
	v_mfma_f32_16x16x32_bf16 v[66:69], v[168:171], v[224:227], v[66:69]
	v_mfma_f32_16x16x32_bf16 v[94:97], v[164:167], v[204:207], v[94:97]
	v_mfma_f32_16x16x32_bf16 v[90:93], v[172:175], v[204:207], v[90:93]
	v_mfma_f32_16x16x32_bf16 v[86:89], v[164:167], v[212:215], v[86:89]
	v_mfma_f32_16x16x32_bf16 v[82:85], v[172:175], v[212:215], v[82:85]
	v_mfma_f32_16x16x32_bf16 v[78:81], v[164:167], v[220:223], v[78:81]
	v_mfma_f32_16x16x32_bf16 v[74:77], v[172:175], v[220:223], v[74:77]
	v_mfma_f32_16x16x32_bf16 v[70:73], v[164:167], v[228:231], v[70:73]
	v_mfma_f32_16x16x32_bf16 v[66:69], v[172:175], v[228:231], v[66:69]
	s_setprio 0
	s_setprio 1
	v_mfma_f32_16x16x32_bf16 v[30:33], v[176:179], v[192:195], v[30:33]
	v_mfma_f32_16x16x32_bf16 v[26:29], v[184:187], v[192:195], v[26:29]
	v_mfma_f32_16x16x32_bf16 v[22:25], v[176:179], v[208:211], v[22:25]
	v_mfma_f32_16x16x32_bf16 v[18:21], v[184:187], v[208:211], v[18:21]
	v_mfma_f32_16x16x32_bf16 v[14:17], v[176:179], v[216:219], v[14:17]
	v_mfma_f32_16x16x32_bf16 v[10:13], v[184:187], v[216:219], v[10:13]
	v_mfma_f32_16x16x32_bf16 v[6:9], v[176:179], v[224:227], v[6:9]
	v_mfma_f32_16x16x32_bf16 v[2:5], v[184:187], v[224:227], v[2:5]
	v_mfma_f32_16x16x32_bf16 v[30:33], v[180:183], v[204:207], v[30:33]
	v_mfma_f32_16x16x32_bf16 v[26:29], v[188:191], v[204:207], v[26:29]
	v_mfma_f32_16x16x32_bf16 v[22:25], v[180:183], v[212:215], v[22:25]
	v_mfma_f32_16x16x32_bf16 v[18:21], v[188:191], v[212:215], v[18:21]
	s_add_u32 s4, s4, 0x100
	s_addc_u32 s5, s5, 0
	s_add_u32 s30, s30, 0x100
	s_addc_u32 s31, s31, 0
	s_cmp_ge_i32 s63, s52
	s_mov_b32 s28, s63
	v_mfma_f32_16x16x32_bf16 v[14:17], v[180:183], v[220:223], v[14:17]
	v_mfma_f32_16x16x32_bf16 v[10:13], v[188:191], v[220:223], v[10:13]
	v_mfma_f32_16x16x32_bf16 v[6:9], v[180:183], v[228:231], v[6:9]
	v_mfma_f32_16x16x32_bf16 v[2:5], v[188:191], v[228:231], v[2:5]
	s_setprio 0
	s_barrier
	s_cbranch_scc0 .LBB0_393
	s_movk_i32 s67, 0x300

; template <class Epi, class Sched, bool ALIGN_EPI = false, bool SP2 = false, bool F8 = false>
; __device__ __forceinline__ void gemm_phase(PG8_LAS unsigned char* lds, const Gemm g, const Sched& S, const Epi& E, const int tidb  ) {
;     ...
; #pragma unroll
;         for (int a = 0; a < 2; ++a)
; #pragma unroll
;             for (int b = 0; b < 2; ++b)
; #pragma unroll
;                 for (int m = 0; m < 4; ++m)
; #pragma unroll
;                     for (int n = 0; n < 2; ++n) acc[a][b][m][n] = (f32x4){0.f, 0.f, 0.f, 0.f};
;         cur = nxt; cA = nA; cB = nB; ++ui;
.LBB0_463:
	v_mov_b32_e32 v129, 0
	s_andn2_b64 vcc, exec, s[14:15]
	v_mov_b32_e32 v128, v129
	v_mov_b32_e32 v127, v129
	v_mov_b32_e32 v126, v129
	v_mov_b32_e32 v125, v129
	s_waitcnt lgkmcnt(0)
	v_mov_b32_e32 v124, v129
	v_mov_b32_e32 v123, v129
	v_mov_b32_e32 v122, v129
	v_mov_b32_e32 v121, v129
	v_mov_b32_e32 v120, v129
	v_mov_b32_e32 v119, v129
	v_mov_b32_e32 v118, v129
	v_mov_b32_e32 v117, v129
	v_mov_b32_e32 v116, v129
	v_mov_b32_e32 v115, v129
	v_mov_b32_e32 v114, v129
	v_mov_b32_e32 v113, v129
	v_mov_b32_e32 v112, v129
	v_mov_b32_e32 v111, v129
	v_mov_b32_e32 v110, v129
	v_mov_b32_e32 v109, v129
	v_mov_b32_e32 v108, v129
	v_mov_b32_e32 v107, v129
	v_mov_b32_e32 v106, v129
	v_mov_b32_e32 v105, v129
	v_mov_b32_e32 v104, v129
	v_mov_b32_e32 v103, v129
	v_mov_b32_e32 v102, v129
	v_mov_b32_e32 v101, v129
	v_mov_b32_e32 v100, v129
	v_mov_b32_e32 v99, v129
	v_mov_b32_e32 v98, v129
	v_mov_b32_e32 v65, v129
	v_mov_b32_e32 v64, v129
	v_mov_b32_e32 v63, v129
	v_mov_b32_e32 v62, v129
	v_mov_b32_e32 v61, v129
	v_mov_b32_e32 v60, v129
	v_mov_b32_e32 v59, v129
	v_mov_b32_e32 v58, v129
	v_mov_b32_e32 v57, v129
	v_mov_b32_e32 v56, v129
	v_mov_b32_e32 v55, v129
	v_mov_b32_e32 v54, v129
	v_mov_b32_e32 v53, v129
	v_mov_b32_e32 v52, v129
	v_mov_b32_e32 v51, v129
	v_mov_b32_e32 v50, v129
	v_mov_b32_e32 v49, v129
	v_mov_b32_e32 v48, v129
	v_mov_b32_e32 v47, v129
	v_mov_b32_e32 v46, v129
	v_mov_b32_e32 v45, v129
	v_mov_b32_e32 v44, v129
	v_mov_b32_e32 v43, v129
	v_mov_b32_e32 v42, v129
	v_mov_b32_e32 v41, v129
	v_mov_b32_e32 v40, v129
	v_mov_b32_e32 v39, v129
	v_mov_b32_e32 v38, v129
	v_mov_b32_e32 v37, v129
	v_mov_b32_e32 v36, v129
	v_mov_b32_e32 v35, v129
	v_mov_b32_e32 v34, v129
	v_mov_b32_e32 v97, v129
	v_mov_b32_e32 v96, v129
	v_mov_b32_e32 v95, v129
	v_mov_b32_e32 v94, v129
	v_mov_b32_e32 v93, v129
	v_mov_b32_e32 v92, v129
	v_mov_b32_e32 v91, v129
	v_mov_b32_e32 v90, v129
	v_mov_b32_e32 v89, v129
	v_mov_b32_e32 v88, v129
	v_mov_b32_e32 v87, v129
	v_mov_b32_e32 v86, v129
	v_mov_b32_e32 v85, v129
	v_mov_b32_e32 v84, v129
	v_mov_b32_e32 v83, v129
	v_mov_b32_e32 v82, v129
	v_mov_b32_e32 v81, v129
	v_mov_b32_e32 v80, v129
	v_mov_b32_e32 v79, v129
	v_mov_b32_e32 v78, v129
	v_mov_b32_e32 v77, v129
	v_mov_b32_e32 v76, v129
	v_mov_b32_e32 v75, v129
	v_mov_b32_e32 v74, v129
	v_mov_b32_e32 v73, v129
	v_mov_b32_e32 v72, v129
	v_mov_b32_e32 v71, v129
	v_mov_b32_e32 v70, v129
	v_mov_b32_e32 v69, v129
	v_mov_b32_e32 v68, v129
	v_mov_b32_e32 v67, v129
	v_mov_b32_e32 v66, v129
	v_mov_b32_e32 v33, v129
	v_mov_b32_e32 v32, v129
	v_mov_b32_e32 v31, v129
	v_mov_b32_e32 v30, v129
	v_mov_b32_e32 v29, v129
	v_mov_b32_e32 v28, v129
	v_mov_b32_e32 v27, v129
	v_mov_b32_e32 v26, v129
	v_mov_b32_e32 v25, v129
	v_mov_b32_e32 v24, v129
	v_mov_b32_e32 v23, v129
	v_mov_b32_e32 v22, v129
	v_mov_b32_e32 v21, v129
	v_mov_b32_e32 v20, v129
	v_mov_b32_e32 v19, v129
	v_mov_b32_e32 v18, v129
	v_mov_b32_e32 v17, v129
	v_mov_b32_e32 v16, v129
	v_mov_b32_e32 v15, v129
	v_mov_b32_e32 v14, v129
	v_mov_b32_e32 v13, v129
	v_mov_b32_e32 v12, v129
	v_mov_b32_e32 v11, v129
	v_mov_b32_e32 v10, v129
	v_mov_b32_e32 v9, v129
	v_mov_b32_e32 v8, v129
	v_mov_b32_e32 v7, v129
	v_mov_b32_e32 v6, v129
	v_mov_b32_e32 v5, v129
	v_mov_b32_e32 v4, v129
	v_mov_b32_e32 v3, v129
	v_mov_b32_e32 v2, v129
	s_cbranch_vccnz .LBB0_466
	s_add_u32 s4, s28, 0x80
	s_addc_u32 s5, s29, 0
	s_add_u32 s28, s6, 0x100
	v_mov_b32_e32 v2, 0
	s_addc_u32 s29, s7, 0
	s_mov_b32 s6, 0
	v_mov_b32_e32 v3, v2
	v_mov_b32_e32 v4, v2
	v_mov_b32_e32 v5, v2
	v_mov_b32_e32 v6, v2
	v_mov_b32_e32 v7, v2
	v_mov_b32_e32 v8, v2
	v_mov_b32_e32 v9, v2
	v_mov_b32_e32 v10, v2
	v_mov_b32_e32 v11, v2
	v_mov_b32_e32 v12, v2
	v_mov_b32_e32 v13, v2
	v_mov_b32_e32 v14, v2
	v_mov_b32_e32 v15, v2
	v_mov_b32_e32 v16, v2
	v_mov_b32_e32 v17, v2
	v_mov_b32_e32 v18, v2
	v_mov_b32_e32 v19, v2
	v_mov_b32_e32 v20, v2
	v_mov_b32_e32 v21, v2
	v_mov_b32_e32 v22, v2
	v_mov_b32_e32 v23, v2
	v_mov_b32_e32 v24, v2
	v_mov_b32_e32 v25, v2
	v_mov_b32_e32 v26, v2
	v_mov_b32_e32 v27, v2
	v_mov_b32_e32 v28, v2
	v_mov_b32_e32 v29, v2
	v_mov_b32_e32 v30, v2
	v_mov_b32_e32 v31, v2
	v_mov_b32_e32 v32, v2
	v_mov_b32_e32 v33, v2
	v_mov_b32_e32 v66, v2
	v_mov_b32_e32 v67, v2
	v_mov_b32_e32 v68, v2
	v_mov_b32_e32 v69, v2
	v_mov_b32_e32 v70, v2
	v_mov_b32_e32 v71, v2
	v_mov_b32_e32 v72, v2
	v_mov_b32_e32 v73, v2
	v_mov_b32_e32 v74, v2
	v_mov_b32_e32 v75, v2
	v_mov_b32_e32 v76, v2
	v_mov_b32_e32 v77, v2
	v_mov_b32_e32 v78, v2
	v_mov_b32_e32 v79, v2
	v_mov_b32_e32 v80, v2
	v_mov_b32_e32 v81, v2
	v_mov_b32_e32 v82, v2
	v_mov_b32_e32 v83, v2
	v_mov_b32_e32 v84, v2
	v_mov_b32_e32 v85, v2
	v_mov_b32_e32 v86, v2
	v_mov_b32_e32 v87, v2
	v_mov_b32_e32 v88, v2
	v_mov_b32_e32 v89, v2
	v_mov_b32_e32 v90, v2
	v_mov_b32_e32 v91, v2
	v_mov_b32_e32 v92, v2
	v_mov_b32_e32 v93, v2
	v_mov_b32_e32 v94, v2
	v_mov_b32_e32 v95, v2
	v_mov_b32_e32 v96, v2
	v_mov_b32_e32 v97, v2
	v_mov_b32_e32 v34, v2
	v_mov_b32_e32 v35, v2
	v_mov_b32_e32 v36, v2
	v_mov_b32_e32 v37, v2
	v_mov_b32_e32 v38, v2
	v_mov_b32_e32 v39, v2
	v_mov_b32_e32 v40, v2
	v_mov_b32_e32 v41, v2
	v_mov_b32_e32 v42, v2
	v_mov_b32_e32 v43, v2
	v_mov_b32_e32 v44, v2
	v_mov_b32_e32 v45, v2
	v_mov_b32_e32 v46, v2
	v_mov_b32_e32 v47, v2
	v_mov_b32_e32 v48, v2
	v_mov_b32_e32 v49, v2
	v_mov_b32_e32 v50, v2
	v_mov_b32_e32 v51, v2
	v_mov_b32_e32 v52, v2
	v_mov_b32_e32 v53, v2
	v_mov_b32_e32 v54, v2
	v_mov_b32_e32 v55, v2
	v_mov_b32_e32 v56, v2
	v_mov_b32_e32 v57, v2
	v_mov_b32_e32 v58, v2
	v_mov_b32_e32 v59, v2
	v_mov_b32_e32 v60, v2
	v_mov_b32_e32 v61, v2
	v_mov_b32_e32 v62, v2
	v_mov_b32_e32 v63, v2
	v_mov_b32_e32 v64, v2
	v_mov_b32_e32 v65, v2
	v_mov_b32_e32 v98, v2
	v_mov_b32_e32 v99, v2
	v_mov_b32_e32 v100, v2
	v_mov_b32_e32 v101, v2
	v_mov_b32_e32 v102, v2
	v_mov_b32_e32 v103, v2
	v_mov_b32_e32 v104, v2
	v_mov_b32_e32 v105, v2
	v_mov_b32_e32 v106, v2
	v_mov_b32_e32 v107, v2
	v_mov_b32_e32 v108, v2
	v_mov_b32_e32 v109, v2
	v_mov_b32_e32 v110, v2
	v_mov_b32_e32 v111, v2
	v_mov_b32_e32 v112, v2
	v_mov_b32_e32 v113, v2
	v_mov_b32_e32 v114, v2
	v_mov_b32_e32 v115, v2
	v_mov_b32_e32 v116, v2
	v_mov_b32_e32 v117, v2
	v_mov_b32_e32 v118, v2
	v_mov_b32_e32 v119, v2
	v_mov_b32_e32 v120, v2
	v_mov_b32_e32 v121, v2
	v_mov_b32_e32 v122, v2
	v_mov_b32_e32 v123, v2
	v_mov_b32_e32 v124, v2
	v_mov_b32_e32 v125, v2
	v_mov_b32_e32 v126, v2
	v_mov_b32_e32 v127, v2
	v_mov_b32_e32 v128, v2
	v_mov_b32_e32 v129, v2
	s_waitcnt vmcnt(0)
; #define PG8_STAGE(bufoff, gbase, voff) do { _Pragma("unroll") for (int _i = 0; _i < 2; ++_i) \
;         __builtin_amdgcn_global_load_lds((const unsigned*)((const char*)(gbase) + (voff)[_i]), (PG8_LAS unsigned*)(lds + (bufoff) + ldsw + _i * 8192), 16, 0, 0); } while (0)
; #define PG8_WAIT_V(n) asm volatile("s_waitcnt vmcnt(" #n ")" ::: "memory")
; #define PG8_WAIT_L(n) asm volatile("s_waitcnt lgkmcnt(" #n ")" ::: "memory")
; #define PG8_BAR __builtin_amdgcn_s_barrier()
; #define PG8_SCHED __builtin_amdgcn_sched_barrier(0)
; template <class Epi, class Sched, bool ALIGN_EPI = false, bool SP2 = false, bool F8 = false>
; __device__ __forceinline__ void gemm_phase(PG8_LAS unsigned char* lds, const Gemm g, const Sched& S, const Epi& E, const int tidb  ) {
;     ...
;         for (int t = 0; t < nt; t += 2) {
;             const bool last = (t == nt - 2);
;             if constexpr (Epi::PREFETCH) { if (t == 0) E.prefetch(cur, wid, lane); }
;             const char* a1 = cA + (size_t)(t + 1) * kstep;
;             const char* a2 = last ? nA : cA + (size_t)(t + 2) * kstep; const char* b2 = last ? nB : cB + (size_t)(t + 2) * kstep;
;             const char* a3 = a2 + kstep; const char* b3 = b2 + kstep;
;             if (last && has_next) S.a_ready(nxt);
;             if constexpr (SP2) {
;             PG8_LDB(B0, 0, 0); PG8_LDB(B1, 0, 1); PG8_SCHED; PG8_LDA(At, 0, 0); PG8_STAGE(PG8_SA(1, 1), a1 + hstep, voffA);
;             PG8_WAIT_V(8); PG8_WAIT_L(0); PG8_BAR; PG8_MMA(0, 0, At, B0); PG8_MMA(0, 1, At, B1); PG8_BAR; PG8_SCHED;
;             PG8_LDA(At, 0, 1); PG8_STAGE(PG8_SB(0, 0), b2, voffB); PG8_STAGE(PG8_SB(0, 1), b2 + hstep, voffB); PG8_STAGE(PG8_SA(0, 0), a2, voffA);
;             PG8_WAIT_V(8); PG8_WAIT_L(0); PG8_BAR; PG8_MMA(1, 0, At, B0); PG8_MMA(1, 1, At, B1); PG8_BAR; PG8_SCHED;
.LBB0_465:
	s_add_i32 s65, 0, 0x10000
	v_add_u32_e32 v0, s65, v159
	ds_read_b128 v[142:145], v0
	ds_read_b128 v[146:149], v0 offset:1024
	ds_read_b128 v[154:157], v0 offset:2048
	ds_read_b128 v[164:167], v0 offset:3072
	s_add_i32 s61, s6, 2
	s_add_u32 s62, s4, 0x80
	s_addc_u32 s7, s5, 0
	s_cmp_eq_u32 s54, s6
	s_cselect_b32 s7, s25, s7
	s_cselect_b32 s6, s24, s62
	s_cselect_b32 s63, s27, s29
	s_cselect_b32 s62, s26, s28
	s_add_i32 s66, 0, 0x14000
	v_add_u32_e32 v0, s66, v159
	ds_read_b128 v[168:171], v0
	ds_read_b128 v[172:175], v0 offset:1024
	ds_read_b128 v[176:179], v0 offset:2048
	ds_read_b128 v[180:183], v0 offset:3072
	v_lshl_add_u64 v[150:151], s[4:5], 0, v[138:139]
	s_add_i32 m0, s45, 0xc000
	ds_read_b128 v[184:187], v160
	ds_read_b128 v[188:191], v160 offset:1024
	ds_read_b128 v[192:195], v160 offset:2048
	ds_read_b128 v[204:207], v160 offset:3072
	ds_read_b128 v[208:211], v160 offset:4096
	ds_read_b128 v[212:215], v160 offset:5120
	ds_read_b128 v[216:219], v160 offset:6144
	ds_read_b128 v[220:223], v160 offset:7168
	global_load_lds_dwordx4 v[150:151], off
	v_lshl_add_u64 v[150:151], s[4:5], 0, v[140:141]
	s_add_i32 m0, s45, 0xe000
	s_nop 0
	global_load_lds_dwordx4 v[150:151], off
	s_waitcnt vmcnt(8)
	s_waitcnt lgkmcnt(0)
	s_barrier
	s_setprio 1
	s_waitcnt lgkmcnt(0)
	v_mfma_f32_16x16x32_bf16 v[126:129], v[142:145], v[184:187], v[126:129]
	v_mfma_f32_16x16x32_bf16 v[122:125], v[154:157], v[184:187], v[122:125]
	v_mfma_f32_16x16x32_bf16 v[118:121], v[142:145], v[192:195], v[118:121]
	v_mfma_f32_16x16x32_bf16 v[114:117], v[154:157], v[192:195], v[114:117]
	v_mfma_f32_16x16x32_bf16 v[110:113], v[142:145], v[208:211], v[110:113]
	v_mfma_f32_16x16x32_bf16 v[106:109], v[154:157], v[208:211], v[106:109]
	v_mfma_f32_16x16x32_bf16 v[102:105], v[142:145], v[216:219], v[102:105]
	v_mfma_f32_16x16x32_bf16 v[98:101], v[154:157], v[216:219], v[98:101]
	v_mfma_f32_16x16x32_bf16 v[126:129], v[146:149], v[188:191], v[126:129]
	v_mfma_f32_16x16x32_bf16 v[122:125], v[164:167], v[188:191], v[122:125]
	v_mfma_f32_16x16x32_bf16 v[118:121], v[146:149], v[204:207], v[118:121]
	v_mfma_f32_16x16x32_bf16 v[114:117], v[164:167], v[204:207], v[114:117]
	v_mfma_f32_16x16x32_bf16 v[110:113], v[146:149], v[212:215], v[110:113]
	v_mfma_f32_16x16x32_bf16 v[106:109], v[164:167], v[212:215], v[106:109]
	v_mfma_f32_16x16x32_bf16 v[102:105], v[146:149], v[220:223], v[102:105]
	v_mfma_f32_16x16x32_bf16 v[98:101], v[164:167], v[220:223], v[98:101]
	s_setprio 0
	s_setprio 1
	v_mfma_f32_16x16x32_bf16 v[62:65], v[168:171], v[184:187], v[62:65]
	v_mfma_f32_16x16x32_bf16 v[58:61], v[176:179], v[184:187], v[58:61]
	v_mfma_f32_16x16x32_bf16 v[54:57], v[168:171], v[192:195], v[54:57]
	v_mfma_f32_16x16x32_bf16 v[50:53], v[176:179], v[192:195], v[50:53]
	v_mfma_f32_16x16x32_bf16 v[46:49], v[168:171], v[208:211], v[46:49]
	v_mfma_f32_16x16x32_bf16 v[42:45], v[176:179], v[208:211], v[42:45]
	v_mfma_f32_16x16x32_bf16 v[38:41], v[168:171], v[216:219], v[38:41]
	v_mfma_f32_16x16x32_bf16 v[34:37], v[176:179], v[216:219], v[34:37]
	v_mfma_f32_16x16x32_bf16 v[62:65], v[172:175], v[188:191], v[62:65]
	v_mfma_f32_16x16x32_bf16 v[58:61], v[180:183], v[188:191], v[58:61]
	v_mfma_f32_16x16x32_bf16 v[54:57], v[172:175], v[204:207], v[54:57]
	v_mfma_f32_16x16x32_bf16 v[50:53], v[180:183], v[204:207], v[50:53]
	v_mfma_f32_16x16x32_bf16 v[46:49], v[172:175], v[212:215], v[46:49]
	v_mfma_f32_16x16x32_bf16 v[42:45], v[180:183], v[212:215], v[42:45]
	v_mfma_f32_16x16x32_bf16 v[38:41], v[172:175], v[220:223], v[38:41]
	v_mfma_f32_16x16x32_bf16 v[34:37], v[180:183], v[220:223], v[34:37]
	s_setprio 0
	s_barrier
	ds_read_b128 v[184:187], v160 offset:16384
	ds_read_b128 v[188:191], v160 offset:17408
	ds_read_b128 v[192:195], v160 offset:18432
	ds_read_b128 v[204:207], v160 offset:19456
	ds_read_b128 v[208:211], v160 offset:20480
	ds_read_b128 v[212:215], v160 offset:21504
	ds_read_b128 v[216:219], v160 offset:22528
	ds_read_b128 v[220:223], v160 offset:23552
	s_add_i32 s65, s65, s43
	v_lshl_add_u64 v[150:151], s[62:63], 0, v[132:133]
	s_mov_b32 m0, s65
	s_nop 0
	global_load_lds_dwordx4 v[150:151], off
	s_add_i32 m0, s65, 0x2000
	v_lshl_add_u64 v[196:197], s[62:63], 0, v[136:137]
	s_add_u32 s62, s62, s8
	s_addc_u32 s63, s63, s9
	s_add_i32 s65, s66, s43
	global_load_lds_dwordx4 v[196:197], off
	v_lshl_add_u64 v[200:201], s[62:63], 0, v[132:133]
	s_mov_b32 m0, s65
	v_lshl_add_u64 v[224:225], s[62:63], 0, v[136:137]
	global_load_lds_dwordx4 v[200:201], off
	s_add_i32 m0, s65, 0x2000
	v_lshl_add_u64 v[226:227], s[6:7], 0, v[130:131]
	global_load_lds_dwordx4 v[224:225], off
	s_mov_b32 m0, s45
	v_lshl_add_u64 v[228:229], s[6:7], 0, v[134:135]
	global_load_lds_dwordx4 v[226:227], off
	s_mov_b32 m0, s46
	s_nop 0
	global_load_lds_dwordx4 v[228:229], off
	s_waitcnt vmcnt(8)
	s_waitcnt lgkmcnt(0)
	s_barrier
; #define PG8_STAGE(bufoff, gbase, voff) do { _Pragma("unroll") for (int _i = 0; _i < 2; ++_i) \
;         __builtin_amdgcn_global_load_lds((const unsigned*)((const char*)(gbase) + (voff)[_i]), (PG8_LAS unsigned*)(lds + (bufoff) + ldsw + _i * 8192), 16, 0, 0); } while (0)
; #define PG8_WAIT_V(n) asm volatile("s_waitcnt vmcnt(" #n ")" ::: "memory")
; #define PG8_WAIT_L(n) asm volatile("s_waitcnt lgkmcnt(" #n ")" ::: "memory")
; #define PG8_BAR __builtin_amdgcn_s_barrier()
; #define PG8_SCHED __builtin_amdgcn_sched_barrier(0)
; template <class Epi, class Sched, bool ALIGN_EPI = false, bool SP2 = false, bool F8 = false>
; __device__ __forceinline__ void gemm_phase(PG8_LAS unsigned char* lds, const Gemm g, const Sched& S, const Epi& E, const int tidb  ) {
;     ...
;             PG8_WAIT_V(8); PG8_WAIT_L(0); PG8_BAR; PG8_MMA(1, 0, At, B0); PG8_MMA(1, 1, At, B1); PG8_BAR; PG8_SCHED;
;             PG8_LDB(B0, 1, 0); PG8_LDB(B1, 1, 1); PG8_SCHED; PG8_LDA(At, 1, 0); PG8_STAGE(PG8_SA(0, 1), a2 + hstep, voffA);
;             PG8_WAIT_V(8); PG8_WAIT_L(0); PG8_BAR; PG8_MMA(0, 0, At, B0); PG8_MMA(0, 1, At, B1); PG8_BAR; PG8_SCHED;
	s_setprio 1
	s_waitcnt lgkmcnt(0)
	v_mfma_f32_16x16x32_bf16 v[94:97], v[142:145], v[184:187], v[94:97]
	v_mfma_f32_16x16x32_bf16 v[90:93], v[154:157], v[184:187], v[90:93]
	v_mfma_f32_16x16x32_bf16 v[86:89], v[142:145], v[192:195], v[86:89]
	v_mfma_f32_16x16x32_bf16 v[82:85], v[154:157], v[192:195], v[82:85]
	v_mfma_f32_16x16x32_bf16 v[78:81], v[142:145], v[208:211], v[78:81]
	v_mfma_f32_16x16x32_bf16 v[74:77], v[154:157], v[208:211], v[74:77]
	v_mfma_f32_16x16x32_bf16 v[70:73], v[142:145], v[216:219], v[70:73]
	v_mfma_f32_16x16x32_bf16 v[66:69], v[154:157], v[216:219], v[66:69]
	v_mfma_f32_16x16x32_bf16 v[94:97], v[146:149], v[188:191], v[94:97]
	v_mfma_f32_16x16x32_bf16 v[90:93], v[164:167], v[188:191], v[90:93]
	v_mfma_f32_16x16x32_bf16 v[86:89], v[146:149], v[204:207], v[86:89]
	v_mfma_f32_16x16x32_bf16 v[82:85], v[164:167], v[204:207], v[82:85]
	v_mfma_f32_16x16x32_bf16 v[78:81], v[146:149], v[212:215], v[78:81]
	v_mfma_f32_16x16x32_bf16 v[74:77], v[164:167], v[212:215], v[74:77]
	v_mfma_f32_16x16x32_bf16 v[70:73], v[146:149], v[220:223], v[70:73]
	v_mfma_f32_16x16x32_bf16 v[66:69], v[164:167], v[220:223], v[66:69]
	s_setprio 0
	s_setprio 1
	v_mfma_f32_16x16x32_bf16 v[30:33], v[168:171], v[184:187], v[30:33]
	v_mfma_f32_16x16x32_bf16 v[26:29], v[176:179], v[184:187], v[26:29]
	v_mfma_f32_16x16x32_bf16 v[22:25], v[168:171], v[192:195], v[22:25]
	v_mfma_f32_16x16x32_bf16 v[18:21], v[176:179], v[192:195], v[18:21]
	v_mfma_f32_16x16x32_bf16 v[14:17], v[168:171], v[208:211], v[14:17]
	v_mfma_f32_16x16x32_bf16 v[10:13], v[176:179], v[208:211], v[10:13]
	v_mfma_f32_16x16x32_bf16 v[6:9], v[168:171], v[216:219], v[6:9]
	v_mfma_f32_16x16x32_bf16 v[2:5], v[176:179], v[216:219], v[2:5]
	v_mfma_f32_16x16x32_bf16 v[30:33], v[172:175], v[188:191], v[30:33]
	v_mfma_f32_16x16x32_bf16 v[26:29], v[180:183], v[188:191], v[26:29]
	v_mfma_f32_16x16x32_bf16 v[22:25], v[172:175], v[204:207], v[22:25]
	v_mfma_f32_16x16x32_bf16 v[18:21], v[180:183], v[204:207], v[18:21]
	v_mfma_f32_16x16x32_bf16 v[14:17], v[172:175], v[212:215], v[14:17]
	v_mfma_f32_16x16x32_bf16 v[10:13], v[180:183], v[212:215], v[10:13]
	v_mfma_f32_16x16x32_bf16 v[6:9], v[172:175], v[220:223], v[6:9]
	v_mfma_f32_16x16x32_bf16 v[2:5], v[180:183], v[220:223], v[2:5]
	s_setprio 0
	s_barrier
	s_add_i32 s62, 0, 0x18000
	v_add_u32_e32 v0, s62, v159
	s_add_i32 s63, 0, 0x1c000
	ds_read_b128 v[142:145], v0
	ds_read_b128 v[146:149], v0 offset:1024
	ds_read_b128 v[154:157], v0 offset:2048
	ds_read_b128 v[164:167], v0 offset:3072
	v_add_u32_e32 v0, s63, v159
	ds_read_b128 v[168:171], v0
	ds_read_b128 v[172:175], v0 offset:1024
	ds_read_b128 v[176:179], v0 offset:2048
	ds_read_b128 v[180:183], v0 offset:3072
	s_add_u32 s6, s6, s8
	s_addc_u32 s7, s7, s9
	s_mov_b32 m0, s47
	v_lshl_add_u64 v[230:231], s[6:7], 0, v[130:131]
	ds_read_b128 v[184:187], v160 offset:32768
	ds_read_b128 v[188:191], v160 offset:33792
	ds_read_b128 v[192:195], v160 offset:34816
	ds_read_b128 v[204:207], v160 offset:35840
	ds_read_b128 v[208:211], v160 offset:36864
	ds_read_b128 v[212:215], v160 offset:37888
	ds_read_b128 v[216:219], v160 offset:38912
	ds_read_b128 v[220:223], v160 offset:39936
	global_load_lds_dwordx4 v[230:231], off
	v_lshl_add_u64 v[230:231], s[6:7], 0, v[134:135]
	s_mov_b32 m0, s48
	s_nop 0
	global_load_lds_dwordx4 v[230:231], off
	s_waitcnt vmcnt(8)
	s_waitcnt lgkmcnt(0)
	s_barrier
	s_setprio 1
	s_waitcnt lgkmcnt(0)
	v_mfma_f32_16x16x32_bf16 v[126:129], v[142:145], v[184:187], v[126:129]
	v_mfma_f32_16x16x32_bf16 v[122:125], v[154:157], v[184:187], v[122:125]
	v_mfma_f32_16x16x32_bf16 v[118:121], v[142:145], v[192:195], v[118:121]
	v_mfma_f32_16x16x32_bf16 v[114:117], v[154:157], v[192:195], v[114:117]
	v_mfma_f32_16x16x32_bf16 v[110:113], v[142:145], v[208:211], v[110:113]
	v_mfma_f32_16x16x32_bf16 v[106:109], v[154:157], v[208:211], v[106:109]
	v_mfma_f32_16x16x32_bf16 v[102:105], v[142:145], v[216:219], v[102:105]
	v_mfma_f32_16x16x32_bf16 v[98:101], v[154:157], v[216:219], v[98:101]
	v_mfma_f32_16x16x32_bf16 v[126:129], v[146:149], v[188:191], v[126:129]
	v_mfma_f32_16x16x32_bf16 v[122:125], v[164:167], v[188:191], v[122:125]
	v_mfma_f32_16x16x32_bf16 v[118:121], v[146:149], v[204:207], v[118:121]
	v_mfma_f32_16x16x32_bf16 v[114:117], v[164:167], v[204:207], v[114:117]
	v_mfma_f32_16x16x32_bf16 v[110:113], v[146:149], v[212:215], v[110:113]
	v_mfma_f32_16x16x32_bf16 v[106:109], v[164:167], v[212:215], v[106:109]
	v_mfma_f32_16x16x32_bf16 v[102:105], v[146:149], v[220:223], v[102:105]
	v_mfma_f32_16x16x32_bf16 v[98:101], v[164:167], v[220:223], v[98:101]
	s_setprio 0
	s_setprio 1
	v_mfma_f32_16x16x32_bf16 v[62:65], v[168:171], v[184:187], v[62:65]
	v_mfma_f32_16x16x32_bf16 v[58:61], v[176:179], v[184:187], v[58:61]
	v_mfma_f32_16x16x32_bf16 v[54:57], v[168:171], v[192:195], v[54:57]
	v_mfma_f32_16x16x32_bf16 v[50:53], v[176:179], v[192:195], v[50:53]
	v_mfma_f32_16x16x32_bf16 v[46:49], v[168:171], v[208:211], v[46:49]
	v_mfma_f32_16x16x32_bf16 v[42:45], v[176:179], v[208:211], v[42:45]
	v_mfma_f32_16x16x32_bf16 v[38:41], v[168:171], v[216:219], v[38:41]
	v_mfma_f32_16x16x32_bf16 v[34:37], v[176:179], v[216:219], v[34:37]
	v_mfma_f32_16x16x32_bf16 v[62:65], v[172:175], v[188:191], v[62:65]
	v_mfma_f32_16x16x32_bf16 v[58:61], v[180:183], v[188:191], v[58:61]
	v_mfma_f32_16x16x32_bf16 v[54:57], v[172:175], v[204:207], v[54:57]
	v_mfma_f32_16x16x32_bf16 v[50:53], v[180:183], v[204:207], v[50:53]
	v_mfma_f32_16x16x32_bf16 v[46:49], v[172:175], v[212:215], v[46:49]
	v_mfma_f32_16x16x32_bf16 v[42:45], v[180:183], v[212:215], v[42:45]
	v_mfma_f32_16x16x32_bf16 v[38:41], v[172:175], v[220:223], v[38:41]
	v_mfma_f32_16x16x32_bf16 v[34:37], v[180:183], v[220:223], v[34:37]
	s_setprio 0
	s_barrier
; #define PG8_STAGE(bufoff, gbase, voff) do { _Pragma("unroll") for (int _i = 0; _i < 2; ++_i) \
;         __builtin_amdgcn_global_load_lds((const unsigned*)((const char*)(gbase) + (voff)[_i]), (PG8_LAS unsigned*)(lds + (bufoff) + ldsw + _i * 8192), 16, 0, 0); } while (0)
; #define PG8_WAIT_V(n) asm volatile("s_waitcnt vmcnt(" #n ")" ::: "memory")
; #define PG8_WAIT_L(n) asm volatile("s_waitcnt lgkmcnt(" #n ")" ::: "memory")
; #define PG8_BAR __builtin_amdgcn_s_barrier()
; #define PG8_SCHED __builtin_amdgcn_sched_barrier(0)
; template <class Epi, class Sched, bool ALIGN_EPI = false, bool SP2 = false, bool F8 = false>
; __device__ __forceinline__ void gemm_phase(PG8_LAS unsigned char* lds, const Gemm g, const Sched& S, const Epi& E, const int tidb  ) {
;     ...
;             PG8_LDA(At, 1, 1); PG8_STAGE(PG8_SB(1, 0), b3, voffB); PG8_STAGE(PG8_SB(1, 1), b3 + hstep, voffB); PG8_STAGE(PG8_SA(1, 0), a3, voffA);
;             PG8_WAIT_V(8); PG8_WAIT_L(0); PG8_BAR; PG8_MMA(1, 0, At, B0); PG8_MMA(1, 1, At, B1); PG8_BAR; PG8_SCHED;
	ds_read_b128 v[184:187], v160 offset:49152
	ds_read_b128 v[188:191], v160 offset:50176
	ds_read_b128 v[192:195], v160 offset:51200
	ds_read_b128 v[204:207], v160 offset:52224
	ds_read_b128 v[208:211], v160 offset:53248
	ds_read_b128 v[212:215], v160 offset:54272
	ds_read_b128 v[216:219], v160 offset:55296
	ds_read_b128 v[220:223], v160 offset:56320
	s_add_i32 s6, s62, s43
	v_lshl_add_u64 v[150:151], v[150:151], 0, s[92:93]
	s_mov_b32 m0, s6
	s_nop 0
	global_load_lds_dwordx4 v[150:151], off
	v_lshl_add_u64 v[150:151], v[196:197], 0, s[92:93]
	s_add_i32 m0, s6, 0x2000
	s_add_i32 s6, s63, s43
	global_load_lds_dwordx4 v[150:151], off
	v_lshl_add_u64 v[150:151], v[200:201], 0, s[92:93]
	s_mov_b32 m0, s6
	s_nop 0
	global_load_lds_dwordx4 v[150:151], off
	v_lshl_add_u64 v[150:151], v[224:225], 0, s[92:93]
	s_add_i32 m0, s6, 0x2000
	s_nop 0
	global_load_lds_dwordx4 v[150:151], off
	v_lshl_add_u64 v[150:151], v[226:227], 0, s[92:93]
	s_mov_b32 m0, s49
	s_nop 0
	global_load_lds_dwordx4 v[150:151], off
	v_lshl_add_u64 v[150:151], v[228:229], 0, s[92:93]
	s_mov_b32 m0, s50
	s_nop 0
	global_load_lds_dwordx4 v[150:151], off
	s_waitcnt vmcnt(8)
	s_waitcnt lgkmcnt(0)
	s_barrier
	s_setprio 1
	s_waitcnt lgkmcnt(0)
	v_mfma_f32_16x16x32_bf16 v[94:97], v[142:145], v[184:187], v[94:97]
	v_mfma_f32_16x16x32_bf16 v[90:93], v[154:157], v[184:187], v[90:93]
	v_mfma_f32_16x16x32_bf16 v[86:89], v[142:145], v[192:195], v[86:89]
	v_mfma_f32_16x16x32_bf16 v[82:85], v[154:157], v[192:195], v[82:85]
	v_mfma_f32_16x16x32_bf16 v[78:81], v[142:145], v[208:211], v[78:81]
	v_mfma_f32_16x16x32_bf16 v[74:77], v[154:157], v[208:211], v[74:77]
	v_mfma_f32_16x16x32_bf16 v[70:73], v[142:145], v[216:219], v[70:73]
	v_mfma_f32_16x16x32_bf16 v[66:69], v[154:157], v[216:219], v[66:69]
	v_mfma_f32_16x16x32_bf16 v[94:97], v[146:149], v[188:191], v[94:97]
	v_mfma_f32_16x16x32_bf16 v[90:93], v[164:167], v[188:191], v[90:93]
	v_mfma_f32_16x16x32_bf16 v[86:89], v[146:149], v[204:207], v[86:89]
	v_mfma_f32_16x16x32_bf16 v[82:85], v[164:167], v[204:207], v[82:85]
	v_mfma_f32_16x16x32_bf16 v[78:81], v[146:149], v[212:215], v[78:81]
	v_mfma_f32_16x16x32_bf16 v[74:77], v[164:167], v[212:215], v[74:77]
	v_mfma_f32_16x16x32_bf16 v[70:73], v[146:149], v[220:223], v[70:73]
	v_mfma_f32_16x16x32_bf16 v[66:69], v[164:167], v[220:223], v[66:69]
	s_setprio 0
	s_setprio 1
	v_mfma_f32_16x16x32_bf16 v[30:33], v[168:171], v[184:187], v[30:33]
	v_mfma_f32_16x16x32_bf16 v[26:29], v[176:179], v[184:187], v[26:29]
	v_mfma_f32_16x16x32_bf16 v[22:25], v[168:171], v[192:195], v[22:25]
	v_mfma_f32_16x16x32_bf16 v[18:21], v[176:179], v[192:195], v[18:21]
	v_mfma_f32_16x16x32_bf16 v[14:17], v[168:171], v[208:211], v[14:17]
	v_mfma_f32_16x16x32_bf16 v[10:13], v[176:179], v[208:211], v[10:13]
	v_mfma_f32_16x16x32_bf16 v[6:9], v[168:171], v[216:219], v[6:9]
	v_mfma_f32_16x16x32_bf16 v[2:5], v[176:179], v[216:219], v[2:5]
	v_mfma_f32_16x16x32_bf16 v[30:33], v[172:175], v[188:191], v[30:33]
	v_mfma_f32_16x16x32_bf16 v[26:29], v[180:183], v[188:191], v[26:29]
	v_mfma_f32_16x16x32_bf16 v[22:25], v[172:175], v[204:207], v[22:25]
	v_mfma_f32_16x16x32_bf16 v[18:21], v[180:183], v[204:207], v[18:21]
	s_add_u32 s4, s4, 0x100
	s_addc_u32 s5, s5, 0
	s_add_u32 s28, s28, 0x100
	s_addc_u32 s29, s29, 0
	s_cmp_ge_i32 s61, s51
	s_mov_b32 s6, s61
	v_mfma_f32_16x16x32_bf16 v[14:17], v[172:175], v[212:215], v[14:17]
	v_mfma_f32_16x16x32_bf16 v[10:13], v[180:183], v[212:215], v[10:13]
	v_mfma_f32_16x16x32_bf16 v[6:9], v[172:175], v[220:223], v[6:9]
	v_mfma_f32_16x16x32_bf16 v[2:5], v[180:183], v[220:223], v[2:5]
	s_setprio 0
	s_barrier
	s_cbranch_scc0 .LBB0_465

; #define PG8_STAGE(bufoff, gbase, voff) do { _Pragma("unroll") for (int _i = 0; _i < 2; ++_i) \
;         __builtin_amdgcn_global_load_lds((const unsigned*)((const char*)(gbase) + (voff)[_i]), (PG8_LAS unsigned*)(lds + (bufoff) + ldsw + _i * 8192), 16, 0, 0); } while (0)
; #define PG8_WAIT_V(n) asm volatile("s_waitcnt vmcnt(" #n ")" ::: "memory")
; #define PG8_WAIT_L(n) asm volatile("s_waitcnt lgkmcnt(" #n ")" ::: "memory")
; #define PG8_BAR __builtin_amdgcn_s_barrier()
; #define PG8_SCHED __builtin_amdgcn_sched_barrier(0)
; template <class Epi, class Sched, bool ALIGN_EPI = false, bool SP2 = false, bool F8 = false>
; __device__ __forceinline__ void gemm_phase(PG8_LAS unsigned char* lds, const Gemm g, const Sched& S, const Epi& E, const int tidb  ) {
;     ...
;         for (int t = 0; t < nt; t += 2) {
;             const bool last = (t == nt - 2);
;             if constexpr (Epi::PREFETCH) { if (t == 0) E.prefetch(cur, wid, lane); }
;             const char* a1 = cA + (size_t)(t + 1) * kstep;
;             const char* a2 = last ? nA : cA + (size_t)(t + 2) * kstep; const char* b2 = last ? nB : cB + (size_t)(t + 2) * kstep;
;             const char* a3 = a2 + kstep; const char* b3 = b2 + kstep;
;             if (last && has_next) S.a_ready(nxt);
;             if constexpr (SP2) {
;             PG8_LDB(B0, 0, 0); PG8_LDB(B1, 0, 1); PG8_SCHED; PG8_LDA(At, 0, 0); PG8_STAGE(PG8_SA(1, 1), a1 + hstep, voffA);
;             PG8_WAIT_V(8); PG8_WAIT_L(0); PG8_BAR; PG8_MMA(0, 0, At, B0); PG8_MMA(0, 1, At, B1); PG8_BAR; PG8_SCHED;
;             PG8_LDA(At, 0, 1); PG8_STAGE(PG8_SB(0, 0), b2, voffB); PG8_STAGE(PG8_SB(0, 1), b2 + hstep, voffB); PG8_STAGE(PG8_SA(0, 0), a2, voffA);
;             PG8_WAIT_V(8); PG8_WAIT_L(0); PG8_BAR; PG8_MMA(1, 0, At, B0); PG8_MMA(1, 1, At, B1); PG8_BAR; PG8_SCHED;
.LBB0_943:
	s_add_i32 s65, 0, 0x10000
	v_add_u32_e32 v142, s65, v196
	ds_read_b128 v[130:133], v142
	ds_read_b128 v[134:137], v142 offset:1024
	ds_read_b128 v[138:141], v142 offset:2048
	ds_read_b128 v[142:145], v142 offset:3072
	s_add_i32 s60, s26, 2
	s_add_u32 s61, s24, 0x80
	s_addc_u32 s27, s25, 0
	s_cmp_eq_u32 s45, s26
	s_cselect_b32 s27, s7, s27
	s_cselect_b32 s26, s6, s61
	s_cselect_b32 s63, s23, s59
	s_cselect_b32 s62, s22, s58
	s_add_i32 s61, 0, 0x14000
	v_add_u32_e32 v158, s61, v196
	ds_read_b128 v[146:149], v158
	ds_read_b128 v[150:153], v158 offset:1024
	ds_read_b128 v[154:157], v158 offset:2048
	ds_read_b128 v[158:161], v158 offset:3072
	v_lshl_add_u64 v[198:199], s[24:25], 0, v[210:211]
	s_add_i32 m0, s1, 0xc000
	ds_read_b128 v[164:167], v200
	ds_read_b128 v[168:171], v200 offset:1024
	ds_read_b128 v[172:175], v200 offset:2048
	ds_read_b128 v[176:179], v200 offset:3072
	ds_read_b128 v[180:183], v200 offset:4096
	ds_read_b128 v[184:187], v200 offset:5120
	ds_read_b128 v[188:191], v200 offset:6144
	ds_read_b128 v[192:195], v200 offset:7168
	global_load_lds_dwordx4 v[198:199], off
	v_lshl_add_u64 v[198:199], s[24:25], 0, v[212:213]
	s_add_i32 m0, s1, 0xe000
	s_nop 0
	global_load_lds_dwordx4 v[198:199], off
	s_waitcnt vmcnt(8)
	s_waitcnt lgkmcnt(0)
	s_barrier
	s_setprio 1
	s_waitcnt lgkmcnt(0)
	v_mfma_f32_16x16x32_bf16 v[126:129], v[130:133], v[164:167], v[126:129]
	v_mfma_f32_16x16x32_bf16 v[122:125], v[138:141], v[164:167], v[122:125]
	v_mfma_f32_16x16x32_bf16 v[110:113], v[130:133], v[172:175], v[110:113]
	v_mfma_f32_16x16x32_bf16 v[106:109], v[138:141], v[172:175], v[106:109]
	v_mfma_f32_16x16x32_bf16 v[94:97], v[130:133], v[180:183], v[94:97]
	v_mfma_f32_16x16x32_bf16 v[90:93], v[138:141], v[180:183], v[90:93]
	v_mfma_f32_16x16x32_bf16 v[78:81], v[130:133], v[188:191], v[78:81]
	v_mfma_f32_16x16x32_bf16 v[74:77], v[138:141], v[188:191], v[74:77]
	v_mfma_f32_16x16x32_bf16 v[126:129], v[134:137], v[168:171], v[126:129]
	v_mfma_f32_16x16x32_bf16 v[122:125], v[142:145], v[168:171], v[122:125]
	v_mfma_f32_16x16x32_bf16 v[110:113], v[134:137], v[176:179], v[110:113]
	v_mfma_f32_16x16x32_bf16 v[106:109], v[142:145], v[176:179], v[106:109]
	v_mfma_f32_16x16x32_bf16 v[94:97], v[134:137], v[184:187], v[94:97]
	v_mfma_f32_16x16x32_bf16 v[90:93], v[142:145], v[184:187], v[90:93]
	v_mfma_f32_16x16x32_bf16 v[78:81], v[134:137], v[192:195], v[78:81]
	v_mfma_f32_16x16x32_bf16 v[74:77], v[142:145], v[192:195], v[74:77]
	s_setprio 0
	s_setprio 1
	v_mfma_f32_16x16x32_bf16 v[118:121], v[146:149], v[164:167], v[118:121]
	v_mfma_f32_16x16x32_bf16 v[114:117], v[154:157], v[164:167], v[114:117]
	v_mfma_f32_16x16x32_bf16 v[102:105], v[146:149], v[172:175], v[102:105]
	v_mfma_f32_16x16x32_bf16 v[98:101], v[154:157], v[172:175], v[98:101]
	v_mfma_f32_16x16x32_bf16 v[86:89], v[146:149], v[180:183], v[86:89]
	v_mfma_f32_16x16x32_bf16 v[82:85], v[154:157], v[180:183], v[82:85]
	v_mfma_f32_16x16x32_bf16 v[70:73], v[146:149], v[188:191], v[70:73]
	v_mfma_f32_16x16x32_bf16 v[66:69], v[154:157], v[188:191], v[66:69]
	v_mfma_f32_16x16x32_bf16 v[118:121], v[150:153], v[168:171], v[118:121]
	v_mfma_f32_16x16x32_bf16 v[114:117], v[158:161], v[168:171], v[114:117]
	v_mfma_f32_16x16x32_bf16 v[102:105], v[150:153], v[176:179], v[102:105]
	v_mfma_f32_16x16x32_bf16 v[98:101], v[158:161], v[176:179], v[98:101]
	v_mfma_f32_16x16x32_bf16 v[86:89], v[150:153], v[184:187], v[86:89]
	v_mfma_f32_16x16x32_bf16 v[82:85], v[158:161], v[184:187], v[82:85]
	v_mfma_f32_16x16x32_bf16 v[70:73], v[150:153], v[192:195], v[70:73]
	v_mfma_f32_16x16x32_bf16 v[66:69], v[158:161], v[192:195], v[66:69]
	s_setprio 0
	s_barrier
	ds_read_b128 v[164:167], v200 offset:16384
	ds_read_b128 v[168:171], v200 offset:17408
	ds_read_b128 v[172:175], v200 offset:18432
	ds_read_b128 v[176:179], v200 offset:19456
	ds_read_b128 v[180:183], v200 offset:20480
	ds_read_b128 v[184:187], v200 offset:21504
	ds_read_b128 v[188:191], v200 offset:22528
	ds_read_b128 v[192:195], v200 offset:23552
	s_add_i32 s65, s65, s0
	v_lshl_add_u64 v[198:199], s[62:63], 0, v[0:1]
	s_mov_b32 m0, s65
	s_nop 0
	global_load_lds_dwordx4 v[198:199], off
	s_add_i32 m0, s65, 0x2000
	v_lshl_add_u64 v[214:215], s[62:63], 0, v[208:209]
	s_add_u32 s62, s62, s10
	s_addc_u32 s63, s63, s11
	s_add_i32 s61, s61, s0
	global_load_lds_dwordx4 v[214:215], off
	v_lshl_add_u64 v[216:217], s[62:63], 0, v[0:1]
	s_mov_b32 m0, s61
	v_lshl_add_u64 v[218:219], s[62:63], 0, v[208:209]
	global_load_lds_dwordx4 v[216:217], off
	s_add_i32 m0, s61, 0x2000
	v_lshl_add_u64 v[220:221], s[26:27], 0, v[204:205]
	global_load_lds_dwordx4 v[218:219], off
	s_mov_b32 m0, s1
	v_lshl_add_u64 v[222:223], s[26:27], 0, v[206:207]
	global_load_lds_dwordx4 v[220:221], off
	s_mov_b32 m0, s28
	s_nop 0
	global_load_lds_dwordx4 v[222:223], off
	s_waitcnt vmcnt(8)
	s_waitcnt lgkmcnt(0)
	s_barrier
; #define PG8_STAGE(bufoff, gbase, voff) do { _Pragma("unroll") for (int _i = 0; _i < 2; ++_i) \
;         __builtin_amdgcn_global_load_lds((const unsigned*)((const char*)(gbase) + (voff)[_i]), (PG8_LAS unsigned*)(lds + (bufoff) + ldsw + _i * 8192), 16, 0, 0); } while (0)
; #define PG8_WAIT_V(n) asm volatile("s_waitcnt vmcnt(" #n ")" ::: "memory")
; #define PG8_WAIT_L(n) asm volatile("s_waitcnt lgkmcnt(" #n ")" ::: "memory")
; #define PG8_BAR __builtin_amdgcn_s_barrier()
; #define PG8_SCHED __builtin_amdgcn_sched_barrier(0)
; template <class Epi, class Sched, bool ALIGN_EPI = false, bool SP2 = false, bool F8 = false>
; __device__ __forceinline__ void gemm_phase(PG8_LAS unsigned char* lds, const Gemm g, const Sched& S, const Epi& E, const int tidb  ) {
;     ...
;             PG8_WAIT_V(8); PG8_WAIT_L(0); PG8_BAR; PG8_MMA(1, 0, At, B0); PG8_MMA(1, 1, At, B1); PG8_BAR; PG8_SCHED;
;             PG8_LDB(B0, 1, 0); PG8_LDB(B1, 1, 1); PG8_SCHED; PG8_LDA(At, 1, 0); PG8_STAGE(PG8_SA(0, 1), a2 + hstep, voffA);
;             PG8_WAIT_V(8); PG8_WAIT_L(0); PG8_BAR; PG8_MMA(0, 0, At, B0); PG8_MMA(0, 1, At, B1); PG8_BAR; PG8_SCHED;
	s_setprio 1
	s_waitcnt lgkmcnt(0)
	v_mfma_f32_16x16x32_bf16 v[62:65], v[130:133], v[164:167], v[62:65]
	v_mfma_f32_16x16x32_bf16 v[58:61], v[138:141], v[164:167], v[58:61]
	v_mfma_f32_16x16x32_bf16 v[46:49], v[130:133], v[172:175], v[46:49]
	v_mfma_f32_16x16x32_bf16 v[42:45], v[138:141], v[172:175], v[42:45]
	v_mfma_f32_16x16x32_bf16 v[30:33], v[130:133], v[180:183], v[30:33]
	v_mfma_f32_16x16x32_bf16 v[26:29], v[138:141], v[180:183], v[26:29]
	v_mfma_f32_16x16x32_bf16 v[14:17], v[130:133], v[188:191], v[14:17]
	v_mfma_f32_16x16x32_bf16 v[10:13], v[138:141], v[188:191], v[10:13]
	v_mfma_f32_16x16x32_bf16 v[62:65], v[134:137], v[168:171], v[62:65]
	v_mfma_f32_16x16x32_bf16 v[58:61], v[142:145], v[168:171], v[58:61]
	v_mfma_f32_16x16x32_bf16 v[46:49], v[134:137], v[176:179], v[46:49]
	v_mfma_f32_16x16x32_bf16 v[42:45], v[142:145], v[176:179], v[42:45]
	v_mfma_f32_16x16x32_bf16 v[30:33], v[134:137], v[184:187], v[30:33]
	v_mfma_f32_16x16x32_bf16 v[26:29], v[142:145], v[184:187], v[26:29]
	v_mfma_f32_16x16x32_bf16 v[14:17], v[134:137], v[192:195], v[14:17]
	v_mfma_f32_16x16x32_bf16 v[10:13], v[142:145], v[192:195], v[10:13]
	s_setprio 0
	s_setprio 1
	v_mfma_f32_16x16x32_bf16 v[54:57], v[146:149], v[164:167], v[54:57]
	v_mfma_f32_16x16x32_bf16 v[50:53], v[154:157], v[164:167], v[50:53]
	v_mfma_f32_16x16x32_bf16 v[38:41], v[146:149], v[172:175], v[38:41]
	v_mfma_f32_16x16x32_bf16 v[34:37], v[154:157], v[172:175], v[34:37]
	v_mfma_f32_16x16x32_bf16 v[22:25], v[146:149], v[180:183], v[22:25]
	v_mfma_f32_16x16x32_bf16 v[18:21], v[154:157], v[180:183], v[18:21]
	v_mfma_f32_16x16x32_bf16 v[6:9], v[146:149], v[188:191], v[6:9]
	v_mfma_f32_16x16x32_bf16 v[2:5], v[154:157], v[188:191], v[2:5]
	v_mfma_f32_16x16x32_bf16 v[54:57], v[150:153], v[168:171], v[54:57]
	v_mfma_f32_16x16x32_bf16 v[50:53], v[158:161], v[168:171], v[50:53]
	v_mfma_f32_16x16x32_bf16 v[38:41], v[150:153], v[176:179], v[38:41]
	v_mfma_f32_16x16x32_bf16 v[34:37], v[158:161], v[176:179], v[34:37]
	v_mfma_f32_16x16x32_bf16 v[22:25], v[150:153], v[184:187], v[22:25]
	v_mfma_f32_16x16x32_bf16 v[18:21], v[158:161], v[184:187], v[18:21]
	v_mfma_f32_16x16x32_bf16 v[6:9], v[150:153], v[192:195], v[6:9]
	v_mfma_f32_16x16x32_bf16 v[2:5], v[158:161], v[192:195], v[2:5]
	s_setprio 0
	s_barrier
	s_add_i32 s61, 0, 0x18000
	s_add_i32 s62, 0, 0x1c000
	v_add_u32_e32 v142, s61, v196
	v_add_u32_e32 v158, s62, v196
	ds_read_b128 v[130:133], v142
	ds_read_b128 v[134:137], v142 offset:1024
	ds_read_b128 v[138:141], v142 offset:2048
	ds_read_b128 v[142:145], v142 offset:3072
	ds_read_b128 v[146:149], v158
	ds_read_b128 v[150:153], v158 offset:1024
	ds_read_b128 v[154:157], v158 offset:2048
	ds_read_b128 v[158:161], v158 offset:3072
	s_add_u32 s26, s26, s10
	s_addc_u32 s27, s27, s11
	s_mov_b32 m0, s29
	v_lshl_add_u64 v[224:225], s[26:27], 0, v[204:205]
	ds_read_b128 v[164:167], v200 offset:32768
	ds_read_b128 v[168:171], v200 offset:33792
	ds_read_b128 v[172:175], v200 offset:34816
	ds_read_b128 v[176:179], v200 offset:35840
	ds_read_b128 v[180:183], v200 offset:36864
	ds_read_b128 v[184:187], v200 offset:37888
	ds_read_b128 v[188:191], v200 offset:38912
	ds_read_b128 v[192:195], v200 offset:39936
	global_load_lds_dwordx4 v[224:225], off
	v_lshl_add_u64 v[224:225], s[26:27], 0, v[206:207]
	s_mov_b32 m0, s36
	s_nop 0
	global_load_lds_dwordx4 v[224:225], off
	s_waitcnt vmcnt(8)
	s_waitcnt lgkmcnt(0)
	s_barrier
	s_setprio 1
	s_waitcnt lgkmcnt(0)
	v_mfma_f32_16x16x32_bf16 v[126:129], v[130:133], v[164:167], v[126:129]
	v_mfma_f32_16x16x32_bf16 v[122:125], v[138:141], v[164:167], v[122:125]
	v_mfma_f32_16x16x32_bf16 v[110:113], v[130:133], v[172:175], v[110:113]
	v_mfma_f32_16x16x32_bf16 v[106:109], v[138:141], v[172:175], v[106:109]
	v_mfma_f32_16x16x32_bf16 v[94:97], v[130:133], v[180:183], v[94:97]
	v_mfma_f32_16x16x32_bf16 v[90:93], v[138:141], v[180:183], v[90:93]
	v_mfma_f32_16x16x32_bf16 v[78:81], v[130:133], v[188:191], v[78:81]
	v_mfma_f32_16x16x32_bf16 v[74:77], v[138:141], v[188:191], v[74:77]
	v_mfma_f32_16x16x32_bf16 v[126:129], v[134:137], v[168:171], v[126:129]
	v_mfma_f32_16x16x32_bf16 v[122:125], v[142:145], v[168:171], v[122:125]
	v_mfma_f32_16x16x32_bf16 v[110:113], v[134:137], v[176:179], v[110:113]
	v_mfma_f32_16x16x32_bf16 v[106:109], v[142:145], v[176:179], v[106:109]
	v_mfma_f32_16x16x32_bf16 v[94:97], v[134:137], v[184:187], v[94:97]
	v_mfma_f32_16x16x32_bf16 v[90:93], v[142:145], v[184:187], v[90:93]
	v_mfma_f32_16x16x32_bf16 v[78:81], v[134:137], v[192:195], v[78:81]
	v_mfma_f32_16x16x32_bf16 v[74:77], v[142:145], v[192:195], v[74:77]
	s_setprio 0
	s_setprio 1
	v_mfma_f32_16x16x32_bf16 v[118:121], v[146:149], v[164:167], v[118:121]
	v_mfma_f32_16x16x32_bf16 v[114:117], v[154:157], v[164:167], v[114:117]
	v_mfma_f32_16x16x32_bf16 v[102:105], v[146:149], v[172:175], v[102:105]
	v_mfma_f32_16x16x32_bf16 v[98:101], v[154:157], v[172:175], v[98:101]
	v_mfma_f32_16x16x32_bf16 v[86:89], v[146:149], v[180:183], v[86:89]
	v_mfma_f32_16x16x32_bf16 v[82:85], v[154:157], v[180:183], v[82:85]
	v_mfma_f32_16x16x32_bf16 v[70:73], v[146:149], v[188:191], v[70:73]
	v_mfma_f32_16x16x32_bf16 v[66:69], v[154:157], v[188:191], v[66:69]
	v_mfma_f32_16x16x32_bf16 v[118:121], v[150:153], v[168:171], v[118:121]
	v_mfma_f32_16x16x32_bf16 v[114:117], v[158:161], v[168:171], v[114:117]
	v_mfma_f32_16x16x32_bf16 v[102:105], v[150:153], v[176:179], v[102:105]
	v_mfma_f32_16x16x32_bf16 v[98:101], v[158:161], v[176:179], v[98:101]
	v_mfma_f32_16x16x32_bf16 v[86:89], v[150:153], v[184:187], v[86:89]
	v_mfma_f32_16x16x32_bf16 v[82:85], v[158:161], v[184:187], v[82:85]
	v_mfma_f32_16x16x32_bf16 v[70:73], v[150:153], v[192:195], v[70:73]
	v_mfma_f32_16x16x32_bf16 v[66:69], v[158:161], v[192:195], v[66:69]
	s_setprio 0
	s_barrier
; #define PG8_STAGE(bufoff, gbase, voff) do { _Pragma("unroll") for (int _i = 0; _i < 2; ++_i) \
;         __builtin_amdgcn_global_load_lds((const unsigned*)((const char*)(gbase) + (voff)[_i]), (PG8_LAS unsigned*)(lds + (bufoff) + ldsw + _i * 8192), 16, 0, 0); } while (0)
; #define PG8_WAIT_V(n) asm volatile("s_waitcnt vmcnt(" #n ")" ::: "memory")
; #define PG8_WAIT_L(n) asm volatile("s_waitcnt lgkmcnt(" #n ")" ::: "memory")
; #define PG8_BAR __builtin_amdgcn_s_barrier()
; #define PG8_SCHED __builtin_amdgcn_sched_barrier(0)
; template <class Epi, class Sched, bool ALIGN_EPI = false, bool SP2 = false, bool F8 = false>
; __device__ __forceinline__ void gemm_phase(PG8_LAS unsigned char* lds, const Gemm g, const Sched& S, const Epi& E, const int tidb  ) {
;     ...
;             PG8_LDA(At, 1, 1); PG8_STAGE(PG8_SB(1, 0), b3, voffB); PG8_STAGE(PG8_SB(1, 1), b3 + hstep, voffB); PG8_STAGE(PG8_SA(1, 0), a3, voffA);
;             PG8_WAIT_V(8); PG8_WAIT_L(0); PG8_BAR; PG8_MMA(1, 0, At, B0); PG8_MMA(1, 1, At, B1); PG8_BAR; PG8_SCHED;
	ds_read_b128 v[164:167], v200 offset:49152
	ds_read_b128 v[168:171], v200 offset:50176
	ds_read_b128 v[172:175], v200 offset:51200
	ds_read_b128 v[176:179], v200 offset:52224
	ds_read_b128 v[180:183], v200 offset:53248
	ds_read_b128 v[184:187], v200 offset:54272
	ds_read_b128 v[188:191], v200 offset:55296
	ds_read_b128 v[192:195], v200 offset:56320
	s_add_i32 s26, s61, s0
	v_lshl_add_u64 v[198:199], v[198:199], 0, s[92:93]
	s_mov_b32 m0, s26
	s_nop 0
	global_load_lds_dwordx4 v[198:199], off
	v_lshl_add_u64 v[198:199], v[214:215], 0, s[92:93]
	s_add_i32 m0, s26, 0x2000
	s_add_i32 s26, s62, s0
	global_load_lds_dwordx4 v[198:199], off
	v_lshl_add_u64 v[198:199], v[216:217], 0, s[92:93]
	s_mov_b32 m0, s26
	s_nop 0
	global_load_lds_dwordx4 v[198:199], off
	v_lshl_add_u64 v[198:199], v[218:219], 0, s[92:93]
	s_add_i32 m0, s26, 0x2000
	s_nop 0
	global_load_lds_dwordx4 v[198:199], off
	v_lshl_add_u64 v[198:199], v[220:221], 0, s[92:93]
	s_mov_b32 m0, s37
	s_nop 0
	global_load_lds_dwordx4 v[198:199], off
	v_lshl_add_u64 v[198:199], v[222:223], 0, s[92:93]
	s_mov_b32 m0, s41
	s_nop 0
	global_load_lds_dwordx4 v[198:199], off
	s_waitcnt vmcnt(8)
	s_waitcnt lgkmcnt(0)
	s_barrier
	s_setprio 1
	s_waitcnt lgkmcnt(0)
	v_mfma_f32_16x16x32_bf16 v[62:65], v[130:133], v[164:167], v[62:65]
	v_mfma_f32_16x16x32_bf16 v[58:61], v[138:141], v[164:167], v[58:61]
	v_mfma_f32_16x16x32_bf16 v[46:49], v[130:133], v[172:175], v[46:49]
	v_mfma_f32_16x16x32_bf16 v[42:45], v[138:141], v[172:175], v[42:45]
	v_mfma_f32_16x16x32_bf16 v[30:33], v[130:133], v[180:183], v[30:33]
	v_mfma_f32_16x16x32_bf16 v[26:29], v[138:141], v[180:183], v[26:29]
	v_mfma_f32_16x16x32_bf16 v[14:17], v[130:133], v[188:191], v[14:17]
	v_mfma_f32_16x16x32_bf16 v[10:13], v[138:141], v[188:191], v[10:13]
	v_mfma_f32_16x16x32_bf16 v[62:65], v[134:137], v[168:171], v[62:65]
	v_mfma_f32_16x16x32_bf16 v[58:61], v[142:145], v[168:171], v[58:61]
	v_mfma_f32_16x16x32_bf16 v[46:49], v[134:137], v[176:179], v[46:49]
	v_mfma_f32_16x16x32_bf16 v[42:45], v[142:145], v[176:179], v[42:45]
	v_mfma_f32_16x16x32_bf16 v[30:33], v[134:137], v[184:187], v[30:33]
	v_mfma_f32_16x16x32_bf16 v[26:29], v[142:145], v[184:187], v[26:29]
	v_mfma_f32_16x16x32_bf16 v[14:17], v[134:137], v[192:195], v[14:17]
	v_mfma_f32_16x16x32_bf16 v[10:13], v[142:145], v[192:195], v[10:13]
	s_setprio 0
	s_setprio 1
	v_mfma_f32_16x16x32_bf16 v[54:57], v[146:149], v[164:167], v[54:57]
	v_mfma_f32_16x16x32_bf16 v[50:53], v[154:157], v[164:167], v[50:53]
	v_mfma_f32_16x16x32_bf16 v[38:41], v[146:149], v[172:175], v[38:41]
	v_mfma_f32_16x16x32_bf16 v[34:37], v[154:157], v[172:175], v[34:37]
	v_mfma_f32_16x16x32_bf16 v[22:25], v[146:149], v[180:183], v[22:25]
	v_mfma_f32_16x16x32_bf16 v[18:21], v[154:157], v[180:183], v[18:21]
	v_mfma_f32_16x16x32_bf16 v[6:9], v[146:149], v[188:191], v[6:9]
	v_mfma_f32_16x16x32_bf16 v[2:5], v[154:157], v[188:191], v[2:5]
	v_mfma_f32_16x16x32_bf16 v[54:57], v[150:153], v[168:171], v[54:57]
	v_mfma_f32_16x16x32_bf16 v[50:53], v[158:161], v[168:171], v[50:53]
	v_mfma_f32_16x16x32_bf16 v[38:41], v[150:153], v[176:179], v[38:41]
	v_mfma_f32_16x16x32_bf16 v[34:37], v[158:161], v[176:179], v[34:37]
	s_add_u32 s24, s24, 0x100
	s_addc_u32 s25, s25, 0
	s_add_u32 s58, s58, 0x100
	s_addc_u32 s59, s59, 0
	s_cmp_ge_i32 s60, s43
	s_mov_b32 s26, s60
	v_mfma_f32_16x16x32_bf16 v[22:25], v[150:153], v[184:187], v[22:25]
	v_mfma_f32_16x16x32_bf16 v[18:21], v[158:161], v[184:187], v[18:21]
	v_mfma_f32_16x16x32_bf16 v[6:9], v[150:153], v[192:195], v[6:9]
	v_mfma_f32_16x16x32_bf16 v[2:5], v[158:161], v[192:195], v[2:5]
	s_setprio 0
	s_barrier
	s_cbranch_scc0 .LBB0_943

; #define PG8_STAGE(bufoff, gbase, voff) do { _Pragma("unroll") for (int _i = 0; _i < 2; ++_i) \
;         __builtin_amdgcn_global_load_lds((const unsigned*)((const char*)(gbase) + (voff)[_i]), (PG8_LAS unsigned*)(lds + (bufoff) + ldsw + _i * 8192), 16, 0, 0); } while (0)
; #define PG8_WAIT_V(n) asm volatile("s_waitcnt vmcnt(" #n ")" ::: "memory")
; #define PG8_WAIT_L(n) asm volatile("s_waitcnt lgkmcnt(" #n ")" ::: "memory")
; #define PG8_BAR __builtin_amdgcn_s_barrier()
; #define PG8_SCHED __builtin_amdgcn_sched_barrier(0)
; template <class Epi, class Sched, bool ALIGN_EPI = false, bool SP2 = false, bool F8 = false>
; __device__ __forceinline__ void gemm_phase(PG8_LAS unsigned char* lds, const Gemm g, const Sched& S, const Epi& E, const int tidb  ) {
;     ...
;         for (int t = 0; t < nt; t += 2) {
;             const bool last = (t == nt - 2);
;             if constexpr (Epi::PREFETCH) { if (t == 0) E.prefetch(cur, wid, lane); }
;             const char* a1 = cA + (size_t)(t + 1) * kstep;
;             const char* a2 = last ? nA : cA + (size_t)(t + 2) * kstep; const char* b2 = last ? nB : cB + (size_t)(t + 2) * kstep;
;             const char* a3 = a2 + kstep; const char* b3 = b2 + kstep;
;             if (last && has_next) S.a_ready(nxt);
;             if constexpr (SP2) {
;             PG8_LDB(B0, 0, 0); PG8_LDB(B1, 0, 1); PG8_SCHED; PG8_LDA(At, 0, 0); PG8_STAGE(PG8_SA(1, 1), a1 + hstep, voffA);
;             PG8_WAIT_V(8); PG8_WAIT_L(0); PG8_BAR; PG8_MMA(0, 0, At, B0); PG8_MMA(0, 1, At, B1); PG8_BAR; PG8_SCHED;
;             PG8_LDA(At, 0, 1); PG8_STAGE(PG8_SB(0, 0), b2, voffB); PG8_STAGE(PG8_SB(0, 1), b2 + hstep, voffB); PG8_STAGE(PG8_SA(0, 0), a2, voffA);
;             PG8_WAIT_V(8); PG8_WAIT_L(0); PG8_BAR; PG8_MMA(1, 0, At, B0); PG8_MMA(1, 1, At, B1); PG8_BAR; PG8_SCHED;
.LBB0_993:
	s_add_i32 s63, 0, 0x10000
	v_add_u32_e32 v2, s63, v200
	ds_read_b128 v[18:21], v2
	ds_read_b128 v[22:25], v2 offset:1024
	ds_read_b128 v[26:29], v2 offset:2048
	ds_read_b128 v[30:33], v2 offset:3072
	s_add_i32 s62, s26, 2
	s_add_u32 s28, s24, 0x80
	s_addc_u32 s27, s25, 0
	s_cmp_eq_u32 s47, s26
	s_cselect_b32 s27, s7, s27
	s_cselect_b32 s26, s6, s28
	s_cselect_b32 s29, s23, s61
	s_cselect_b32 s28, s22, s60
	s_add_i32 s65, 0, 0x14000
	v_add_u32_e32 v14, s65, v200
	ds_read_b128 v[2:5], v14
	ds_read_b128 v[6:9], v14 offset:1024
	ds_read_b128 v[10:13], v14 offset:2048
	ds_read_b128 v[14:17], v14 offset:3072
	v_lshl_add_u64 v[198:199], s[24:25], 0, v[210:211]
	s_add_i32 m0, s1, 0xc000
	ds_read_b128 v[164:167], v196
	ds_read_b128 v[168:171], v196 offset:1024
	ds_read_b128 v[172:175], v196 offset:2048
	ds_read_b128 v[176:179], v196 offset:3072
	ds_read_b128 v[180:183], v196 offset:4096
	ds_read_b128 v[184:187], v196 offset:5120
	ds_read_b128 v[188:191], v196 offset:6144
	ds_read_b128 v[192:195], v196 offset:7168
	global_load_lds_dwordx4 v[198:199], off
	v_lshl_add_u64 v[198:199], s[24:25], 0, v[212:213]
	s_add_i32 m0, s1, 0xe000
	s_nop 0
	global_load_lds_dwordx4 v[198:199], off
	s_waitcnt vmcnt(8)
	s_waitcnt lgkmcnt(0)
	s_barrier
	s_setprio 1
	s_waitcnt lgkmcnt(0)
	v_mfma_scale_f32_16x16x128_f8f6f4 v[158:161], v[18:25], v[164:171], v[158:161], v246, v247 op_sel_hi:[0,0,0]
	v_mfma_scale_f32_16x16x128_f8f6f4 v[154:157], v[26:33], v[164:171], v[154:157], v246, v247 op_sel_hi:[0,0,0]
	v_mfma_scale_f32_16x16x128_f8f6f4 v[142:145], v[18:25], v[172:179], v[142:145], v246, v247 op_sel_hi:[0,0,0]
	v_mfma_scale_f32_16x16x128_f8f6f4 v[138:141], v[26:33], v[172:179], v[138:141], v246, v247 op_sel_hi:[0,0,0]
	v_mfma_scale_f32_16x16x128_f8f6f4 v[126:129], v[18:25], v[180:187], v[126:129], v246, v247 op_sel_hi:[0,0,0]
	v_mfma_scale_f32_16x16x128_f8f6f4 v[122:125], v[26:33], v[180:187], v[122:125], v246, v247 op_sel_hi:[0,0,0]
	v_mfma_scale_f32_16x16x128_f8f6f4 v[110:113], v[18:25], v[188:195], v[110:113], v246, v247 op_sel_hi:[0,0,0]
	v_mfma_scale_f32_16x16x128_f8f6f4 v[106:109], v[26:33], v[188:195], v[106:109], v246, v247 op_sel_hi:[0,0,0]
	s_setprio 0
	s_setprio 1
	v_mfma_scale_f32_16x16x128_f8f6f4 v[150:153], v[2:9], v[164:171], v[150:153], v246, v247 op_sel_hi:[0,0,0]
	v_mfma_scale_f32_16x16x128_f8f6f4 v[146:149], v[10:17], v[164:171], v[146:149], v246, v247 op_sel_hi:[0,0,0]
	v_mfma_scale_f32_16x16x128_f8f6f4 v[134:137], v[2:9], v[172:179], v[134:137], v246, v247 op_sel_hi:[0,0,0]
	v_mfma_scale_f32_16x16x128_f8f6f4 v[130:133], v[10:17], v[172:179], v[130:133], v246, v247 op_sel_hi:[0,0,0]
	v_mfma_scale_f32_16x16x128_f8f6f4 v[118:121], v[2:9], v[180:187], v[118:121], v246, v247 op_sel_hi:[0,0,0]
	v_mfma_scale_f32_16x16x128_f8f6f4 v[114:117], v[10:17], v[180:187], v[114:117], v246, v247 op_sel_hi:[0,0,0]
	v_mfma_scale_f32_16x16x128_f8f6f4 v[102:105], v[2:9], v[188:195], v[102:105], v246, v247 op_sel_hi:[0,0,0]
	v_mfma_scale_f32_16x16x128_f8f6f4 v[98:101], v[10:17], v[188:195], v[98:101], v246, v247 op_sel_hi:[0,0,0]
	s_setprio 0
	s_barrier
	ds_read_b128 v[176:179], v196 offset:16384
	ds_read_b128 v[180:183], v196 offset:17408
	ds_read_b128 v[184:187], v196 offset:18432
	ds_read_b128 v[188:191], v196 offset:19456
	ds_read_b128 v[214:217], v196 offset:20480
	ds_read_b128 v[218:221], v196 offset:21504
	ds_read_b128 v[222:225], v196 offset:22528
	ds_read_b128 v[226:229], v196 offset:23552
	s_add_i32 s63, s63, s0
	v_lshl_add_u64 v[164:165], s[28:29], 0, v[0:1]
	s_mov_b32 m0, s63
	s_nop 0
	global_load_lds_dwordx4 v[164:165], off
	s_add_i32 m0, s63, 0x2000
	v_lshl_add_u64 v[166:167], s[28:29], 0, v[208:209]
	s_add_u32 s28, s28, s10
	s_addc_u32 s29, s29, s11
	s_add_i32 s63, s65, s0
	global_load_lds_dwordx4 v[166:167], off
	v_lshl_add_u64 v[168:169], s[28:29], 0, v[0:1]
	s_mov_b32 m0, s63
	v_lshl_add_u64 v[170:171], s[28:29], 0, v[208:209]
	global_load_lds_dwordx4 v[168:169], off
	s_add_i32 m0, s63, 0x2000
	v_lshl_add_u64 v[172:173], s[26:27], 0, v[204:205]
	global_load_lds_dwordx4 v[170:171], off
	s_mov_b32 m0, s1
	v_lshl_add_u64 v[174:175], s[26:27], 0, v[206:207]
	global_load_lds_dwordx4 v[172:173], off
	s_mov_b32 m0, s36
	s_nop 0
	global_load_lds_dwordx4 v[174:175], off
	s_waitcnt vmcnt(8)
	s_waitcnt lgkmcnt(0)
	s_barrier
	s_setprio 1
	s_waitcnt lgkmcnt(0)
	v_mfma_scale_f32_16x16x128_f8f6f4 v[94:97], v[18:25], v[176:183], v[94:97], v246, v247 op_sel_hi:[0,0,0]
	v_mfma_scale_f32_16x16x128_f8f6f4 v[90:93], v[26:33], v[176:183], v[90:93], v246, v247 op_sel_hi:[0,0,0]
	v_mfma_scale_f32_16x16x128_f8f6f4 v[78:81], v[18:25], v[184:191], v[78:81], v246, v247 op_sel_hi:[0,0,0]
	v_mfma_scale_f32_16x16x128_f8f6f4 v[74:77], v[26:33], v[184:191], v[74:77], v246, v247 op_sel_hi:[0,0,0]
	v_mfma_scale_f32_16x16x128_f8f6f4 v[62:65], v[18:25], v[214:221], v[62:65], v246, v247 op_sel_hi:[0,0,0]
	v_mfma_scale_f32_16x16x128_f8f6f4 v[58:61], v[26:33], v[214:221], v[58:61], v246, v247 op_sel_hi:[0,0,0]
	v_mfma_scale_f32_16x16x128_f8f6f4 v[46:49], v[18:25], v[222:229], v[46:49], v246, v247 op_sel_hi:[0,0,0]
	v_mfma_scale_f32_16x16x128_f8f6f4 v[42:45], v[26:33], v[222:229], v[42:45], v246, v247 op_sel_hi:[0,0,0]
	s_setprio 0
	s_setprio 1
	v_mfma_scale_f32_16x16x128_f8f6f4 v[86:89], v[2:9], v[176:183], v[86:89], v246, v247 op_sel_hi:[0,0,0]
	v_mfma_scale_f32_16x16x128_f8f6f4 v[82:85], v[10:17], v[176:183], v[82:85], v246, v247 op_sel_hi:[0,0,0]
	v_mfma_scale_f32_16x16x128_f8f6f4 v[70:73], v[2:9], v[184:191], v[70:73], v246, v247 op_sel_hi:[0,0,0]
	v_mfma_scale_f32_16x16x128_f8f6f4 v[66:69], v[10:17], v[184:191], v[66:69], v246, v247 op_sel_hi:[0,0,0]
	v_mfma_scale_f32_16x16x128_f8f6f4 v[54:57], v[2:9], v[214:221], v[54:57], v246, v247 op_sel_hi:[0,0,0]
	v_mfma_scale_f32_16x16x128_f8f6f4 v[50:53], v[10:17], v[214:221], v[50:53], v246, v247 op_sel_hi:[0,0,0]
	v_mfma_scale_f32_16x16x128_f8f6f4 v[38:41], v[2:9], v[222:229], v[38:41], v246, v247 op_sel_hi:[0,0,0]
	v_mfma_scale_f32_16x16x128_f8f6f4 v[34:37], v[10:17], v[222:229], v[34:37], v246, v247 op_sel_hi:[0,0,0]
	s_setprio 0
	s_barrier
; #define PG8_STAGE(bufoff, gbase, voff) do { _Pragma("unroll") for (int _i = 0; _i < 2; ++_i) \
;         __builtin_amdgcn_global_load_lds((const unsigned*)((const char*)(gbase) + (voff)[_i]), (PG8_LAS unsigned*)(lds + (bufoff) + ldsw + _i * 8192), 16, 0, 0); } while (0)
; #define PG8_WAIT_V(n) asm volatile("s_waitcnt vmcnt(" #n ")" ::: "memory")
; #define PG8_WAIT_L(n) asm volatile("s_waitcnt lgkmcnt(" #n ")" ::: "memory")
; #define PG8_BAR __builtin_amdgcn_s_barrier()
; #define PG8_SCHED __builtin_amdgcn_sched_barrier(0)
; template <class Epi, class Sched, bool ALIGN_EPI = false, bool SP2 = false, bool F8 = false>
; __device__ __forceinline__ void gemm_phase(PG8_LAS unsigned char* lds, const Gemm g, const Sched& S, const Epi& E, const int tidb  ) {
;     ...
;             PG8_LDB(B0, 1, 0); PG8_LDB(B1, 1, 1); PG8_SCHED; PG8_LDA(At, 1, 0); PG8_STAGE(PG8_SA(0, 1), a2 + hstep, voffA);
;             PG8_WAIT_V(8); PG8_WAIT_L(0); PG8_BAR; PG8_MMA(0, 0, At, B0); PG8_MMA(0, 1, At, B1); PG8_BAR; PG8_SCHED;
;             PG8_LDA(At, 1, 1); PG8_STAGE(PG8_SB(1, 0), b3, voffB); PG8_STAGE(PG8_SB(1, 1), b3 + hstep, voffB); PG8_STAGE(PG8_SA(1, 0), a3, voffA);
;             PG8_WAIT_V(8); PG8_WAIT_L(0); PG8_BAR; PG8_MMA(1, 0, At, B0); PG8_MMA(1, 1, At, B1); PG8_BAR; PG8_SCHED;
	s_add_i32 s28, 0, 0x18000
	s_add_i32 s29, 0, 0x1c000
	v_add_u32_e32 v14, s28, v200
	v_add_u32_e32 v30, s29, v200
	ds_read_b128 v[2:5], v14
	ds_read_b128 v[6:9], v14 offset:1024
	ds_read_b128 v[10:13], v14 offset:2048
	ds_read_b128 v[14:17], v14 offset:3072
	ds_read_b128 v[18:21], v30
	ds_read_b128 v[22:25], v30 offset:1024
	ds_read_b128 v[26:29], v30 offset:2048
	ds_read_b128 v[30:33], v30 offset:3072
	s_add_u32 s26, s26, s10
	s_addc_u32 s27, s27, s11
	s_mov_b32 m0, s37
	v_lshl_add_u64 v[192:193], s[26:27], 0, v[204:205]
	ds_read_b128 v[176:179], v196 offset:32768
	ds_read_b128 v[180:183], v196 offset:33792
	ds_read_b128 v[184:187], v196 offset:34816
	ds_read_b128 v[188:191], v196 offset:35840
	ds_read_b128 v[214:217], v196 offset:36864
	ds_read_b128 v[218:221], v196 offset:37888
	ds_read_b128 v[222:225], v196 offset:38912
	ds_read_b128 v[226:229], v196 offset:39936
	global_load_lds_dwordx4 v[192:193], off
	v_lshl_add_u64 v[192:193], s[26:27], 0, v[206:207]
	s_mov_b32 m0, s41
	s_nop 0
	global_load_lds_dwordx4 v[192:193], off
	s_waitcnt vmcnt(8)
	s_waitcnt lgkmcnt(0)
	s_barrier
	s_setprio 1
	s_waitcnt lgkmcnt(0)
	v_mfma_scale_f32_16x16x128_f8f6f4 v[158:161], v[2:9], v[176:183], v[158:161], v246, v247 op_sel_hi:[0,0,0]
	v_mfma_scale_f32_16x16x128_f8f6f4 v[154:157], v[10:17], v[176:183], v[154:157], v246, v247 op_sel_hi:[0,0,0]
	v_mfma_scale_f32_16x16x128_f8f6f4 v[142:145], v[2:9], v[184:191], v[142:145], v246, v247 op_sel_hi:[0,0,0]
	v_mfma_scale_f32_16x16x128_f8f6f4 v[138:141], v[10:17], v[184:191], v[138:141], v246, v247 op_sel_hi:[0,0,0]
	v_mfma_scale_f32_16x16x128_f8f6f4 v[126:129], v[2:9], v[214:221], v[126:129], v246, v247 op_sel_hi:[0,0,0]
	v_mfma_scale_f32_16x16x128_f8f6f4 v[122:125], v[10:17], v[214:221], v[122:125], v246, v247 op_sel_hi:[0,0,0]
	v_mfma_scale_f32_16x16x128_f8f6f4 v[110:113], v[2:9], v[222:229], v[110:113], v246, v247 op_sel_hi:[0,0,0]
	v_mfma_scale_f32_16x16x128_f8f6f4 v[106:109], v[10:17], v[222:229], v[106:109], v246, v247 op_sel_hi:[0,0,0]
	s_setprio 0
	s_setprio 1
	v_mfma_scale_f32_16x16x128_f8f6f4 v[150:153], v[18:25], v[176:183], v[150:153], v246, v247 op_sel_hi:[0,0,0]
	v_mfma_scale_f32_16x16x128_f8f6f4 v[146:149], v[26:33], v[176:183], v[146:149], v246, v247 op_sel_hi:[0,0,0]
	v_mfma_scale_f32_16x16x128_f8f6f4 v[134:137], v[18:25], v[184:191], v[134:137], v246, v247 op_sel_hi:[0,0,0]
	v_mfma_scale_f32_16x16x128_f8f6f4 v[130:133], v[26:33], v[184:191], v[130:133], v246, v247 op_sel_hi:[0,0,0]
	v_mfma_scale_f32_16x16x128_f8f6f4 v[118:121], v[18:25], v[214:221], v[118:121], v246, v247 op_sel_hi:[0,0,0]
	v_mfma_scale_f32_16x16x128_f8f6f4 v[114:117], v[26:33], v[214:221], v[114:117], v246, v247 op_sel_hi:[0,0,0]
	v_mfma_scale_f32_16x16x128_f8f6f4 v[102:105], v[18:25], v[222:229], v[102:105], v246, v247 op_sel_hi:[0,0,0]
	v_mfma_scale_f32_16x16x128_f8f6f4 v[98:101], v[26:33], v[222:229], v[98:101], v246, v247 op_sel_hi:[0,0,0]
	s_setprio 0
	s_barrier
	ds_read_b128 v[176:179], v196 offset:49152
	ds_read_b128 v[180:183], v196 offset:50176
	ds_read_b128 v[184:187], v196 offset:51200
	ds_read_b128 v[188:191], v196 offset:52224
	ds_read_b128 v[214:217], v196 offset:53248
	ds_read_b128 v[218:221], v196 offset:54272
	ds_read_b128 v[222:225], v196 offset:55296
	ds_read_b128 v[226:229], v196 offset:56320
	s_add_i32 s26, s28, s0
	v_lshl_add_u64 v[164:165], v[164:165], 0, s[92:93]
	s_mov_b32 m0, s26
	s_nop 0
	global_load_lds_dwordx4 v[164:165], off
	v_lshl_add_u64 v[164:165], v[166:167], 0, s[92:93]
	s_add_i32 m0, s26, 0x2000
	s_add_i32 s26, s29, s0
	global_load_lds_dwordx4 v[164:165], off
	v_lshl_add_u64 v[164:165], v[168:169], 0, s[92:93]
	s_mov_b32 m0, s26
	s_nop 0
	global_load_lds_dwordx4 v[164:165], off
	v_lshl_add_u64 v[164:165], v[170:171], 0, s[92:93]
	s_add_i32 m0, s26, 0x2000
	s_nop 0
	global_load_lds_dwordx4 v[164:165], off
	v_lshl_add_u64 v[164:165], v[172:173], 0, s[92:93]
	s_mov_b32 m0, s43
	s_nop 0
	global_load_lds_dwordx4 v[164:165], off
	v_lshl_add_u64 v[164:165], v[174:175], 0, s[92:93]
	s_mov_b32 m0, s45
	s_nop 0
	global_load_lds_dwordx4 v[164:165], off
	s_waitcnt vmcnt(8)
	s_waitcnt lgkmcnt(0)
	s_barrier
	s_setprio 1
	s_waitcnt lgkmcnt(0)
	v_mfma_scale_f32_16x16x128_f8f6f4 v[94:97], v[2:9], v[176:183], v[94:97], v246, v247 op_sel_hi:[0,0,0]
	v_mfma_scale_f32_16x16x128_f8f6f4 v[90:93], v[10:17], v[176:183], v[90:93], v246, v247 op_sel_hi:[0,0,0]
	v_mfma_scale_f32_16x16x128_f8f6f4 v[78:81], v[2:9], v[184:191], v[78:81], v246, v247 op_sel_hi:[0,0,0]
	v_mfma_scale_f32_16x16x128_f8f6f4 v[74:77], v[10:17], v[184:191], v[74:77], v246, v247 op_sel_hi:[0,0,0]
	v_mfma_scale_f32_16x16x128_f8f6f4 v[62:65], v[2:9], v[214:221], v[62:65], v246, v247 op_sel_hi:[0,0,0]
	v_mfma_scale_f32_16x16x128_f8f6f4 v[58:61], v[10:17], v[214:221], v[58:61], v246, v247 op_sel_hi:[0,0,0]
	v_mfma_scale_f32_16x16x128_f8f6f4 v[46:49], v[2:9], v[222:229], v[46:49], v246, v247 op_sel_hi:[0,0,0]
	v_mfma_scale_f32_16x16x128_f8f6f4 v[42:45], v[10:17], v[222:229], v[42:45], v246, v247 op_sel_hi:[0,0,0]
	s_setprio 0
	s_setprio 1
	v_mfma_scale_f32_16x16x128_f8f6f4 v[86:89], v[18:25], v[176:183], v[86:89], v246, v247 op_sel_hi:[0,0,0]
	v_mfma_scale_f32_16x16x128_f8f6f4 v[82:85], v[26:33], v[176:183], v[82:85], v246, v247 op_sel_hi:[0,0,0]
	v_mfma_scale_f32_16x16x128_f8f6f4 v[70:73], v[18:25], v[184:191], v[70:73], v246, v247 op_sel_hi:[0,0,0]
	v_mfma_scale_f32_16x16x128_f8f6f4 v[66:69], v[26:33], v[184:191], v[66:69], v246, v247 op_sel_hi:[0,0,0]
	s_add_u32 s24, s24, 0x100
	s_addc_u32 s25, s25, 0
	s_add_u32 s60, s60, 0x100
	s_addc_u32 s61, s61, 0
	s_cmp_ge_i32 s62, s46
	s_mov_b32 s26, s62
	v_mfma_scale_f32_16x16x128_f8f6f4 v[54:57], v[18:25], v[214:221], v[54:57], v246, v247 op_sel_hi:[0,0,0]
	v_mfma_scale_f32_16x16x128_f8f6f4 v[50:53], v[26:33], v[214:221], v[50:53], v246, v247 op_sel_hi:[0,0,0]
	v_mfma_scale_f32_16x16x128_f8f6f4 v[38:41], v[18:25], v[222:229], v[38:41], v246, v247 op_sel_hi:[0,0,0]
	v_mfma_scale_f32_16x16x128_f8f6f4 v[34:37], v[26:33], v[222:229], v[34:37], v246, v247 op_sel_hi:[0,0,0]
	s_setprio 0
	s_barrier
	s_cbranch_scc0 .LBB0_993

; #define PG8_STAGE(bufoff, gbase, voff) do { _Pragma("unroll") for (int _i = 0; _i < 2; ++_i) \
;         __builtin_amdgcn_global_load_lds((const unsigned*)((const char*)(gbase) + (voff)[_i]), (PG8_LAS unsigned*)(lds + (bufoff) + ldsw + _i * 8192), 16, 0, 0); } while (0)
; #define PG8_WAIT_V(n) asm volatile("s_waitcnt vmcnt(" #n ")" ::: "memory")
; #define PG8_WAIT_L(n) asm volatile("s_waitcnt lgkmcnt(" #n ")" ::: "memory")
; #define PG8_BAR __builtin_amdgcn_s_barrier()
; #define PG8_SCHED __builtin_amdgcn_sched_barrier(0)
; template <class Epi, class Sched, bool ALIGN_EPI = false, bool SP2 = false, bool F8 = false>
; __device__ __forceinline__ void gemm_phase(PG8_LAS unsigned char* lds, const Gemm g, const Sched& S, const Epi& E, const int tidb  ) {
;     ...
;         for (int t = 0; t < nt; t += 2) {
;             const bool last = (t == nt - 2);
;             if constexpr (Epi::PREFETCH) { if (t == 0) E.prefetch(cur, wid, lane); }
;             const char* a1 = cA + (size_t)(t + 1) * kstep;
;             const char* a2 = last ? nA : cA + (size_t)(t + 2) * kstep; const char* b2 = last ? nB : cB + (size_t)(t + 2) * kstep;
;             const char* a3 = a2 + kstep; const char* b3 = b2 + kstep;
;             if (last && has_next) S.a_ready(nxt);
;             if constexpr (SP2) {
;             PG8_LDB(B0, 0, 0); PG8_LDB(B1, 0, 1); PG8_SCHED; PG8_LDA(At, 0, 0); PG8_STAGE(PG8_SA(1, 1), a1 + hstep, voffA);
;             PG8_WAIT_V(8); PG8_WAIT_L(0); PG8_BAR; PG8_MMA(0, 0, At, B0); PG8_MMA(0, 1, At, B1); PG8_BAR; PG8_SCHED;
;             PG8_LDA(At, 0, 1); PG8_STAGE(PG8_SB(0, 0), b2, voffB); PG8_STAGE(PG8_SB(0, 1), b2 + hstep, voffB); PG8_STAGE(PG8_SA(0, 0), a2, voffA);
;             PG8_WAIT_V(8); PG8_WAIT_L(0); PG8_BAR; PG8_MMA(1, 0, At, B0); PG8_MMA(1, 1, At, B1); PG8_BAR; PG8_SCHED;
.LBB0_1042:
	s_add_i32 s63, 0, 0x10000
	v_add_u32_e32 v2, s63, v192
	ds_read_b128 v[18:21], v2
	ds_read_b128 v[22:25], v2 offset:1024
	ds_read_b128 v[26:29], v2 offset:2048
	ds_read_b128 v[30:33], v2 offset:3072
	s_add_i32 s62, s26, 2
	s_add_u32 s28, s24, 0x80
	s_addc_u32 s27, s25, 0
	s_cmp_eq_u32 s47, s26
	s_cselect_b32 s27, s7, s27
	s_cselect_b32 s26, s6, s28
	s_cselect_b32 s29, s9, s61
	s_cselect_b32 s28, s8, s60
	s_add_i32 s65, 0, 0x14000
	v_add_u32_e32 v14, s65, v192
	ds_read_b128 v[2:5], v14
	ds_read_b128 v[6:9], v14 offset:1024
	ds_read_b128 v[10:13], v14 offset:2048
	ds_read_b128 v[14:17], v14 offset:3072
	v_lshl_add_u64 v[190:191], s[24:25], 0, v[170:171]
	s_add_i32 m0, s1, 0xc000
	ds_read_b128 v[174:177], v194
	ds_read_b128 v[178:181], v194 offset:1024
	ds_read_b128 v[182:185], v194 offset:2048
	ds_read_b128 v[186:189], v194 offset:3072
	ds_read_b128 v[204:207], v194 offset:4096
	ds_read_b128 v[208:211], v194 offset:5120
	ds_read_b128 v[212:215], v194 offset:6144
	ds_read_b128 v[216:219], v194 offset:7168
	global_load_lds_dwordx4 v[190:191], off
	v_lshl_add_u64 v[190:191], s[24:25], 0, v[172:173]
	s_add_i32 m0, s1, 0xe000
	s_nop 0
	global_load_lds_dwordx4 v[190:191], off
	s_waitcnt vmcnt(8)
	s_waitcnt lgkmcnt(0)
	s_barrier
	s_setprio 1
	s_waitcnt lgkmcnt(0)
	v_mfma_scale_f32_16x16x128_f8f6f4 v[158:161], v[18:25], v[174:181], v[158:161], v246, v247 op_sel_hi:[0,0,0]
	v_mfma_scale_f32_16x16x128_f8f6f4 v[154:157], v[26:33], v[174:181], v[154:157], v246, v247 op_sel_hi:[0,0,0]
	v_mfma_scale_f32_16x16x128_f8f6f4 v[142:145], v[18:25], v[182:189], v[142:145], v246, v247 op_sel_hi:[0,0,0]
	v_mfma_scale_f32_16x16x128_f8f6f4 v[138:141], v[26:33], v[182:189], v[138:141], v246, v247 op_sel_hi:[0,0,0]
	v_mfma_scale_f32_16x16x128_f8f6f4 v[126:129], v[18:25], v[204:211], v[126:129], v246, v247 op_sel_hi:[0,0,0]
	v_mfma_scale_f32_16x16x128_f8f6f4 v[122:125], v[26:33], v[204:211], v[122:125], v246, v247 op_sel_hi:[0,0,0]
	v_mfma_scale_f32_16x16x128_f8f6f4 v[110:113], v[18:25], v[212:219], v[110:113], v246, v247 op_sel_hi:[0,0,0]
	v_mfma_scale_f32_16x16x128_f8f6f4 v[106:109], v[26:33], v[212:219], v[106:109], v246, v247 op_sel_hi:[0,0,0]
	s_setprio 0
	s_setprio 1
	v_mfma_scale_f32_16x16x128_f8f6f4 v[150:153], v[2:9], v[174:181], v[150:153], v246, v247 op_sel_hi:[0,0,0]
	v_mfma_scale_f32_16x16x128_f8f6f4 v[146:149], v[10:17], v[174:181], v[146:149], v246, v247 op_sel_hi:[0,0,0]
	v_mfma_scale_f32_16x16x128_f8f6f4 v[134:137], v[2:9], v[182:189], v[134:137], v246, v247 op_sel_hi:[0,0,0]
	v_mfma_scale_f32_16x16x128_f8f6f4 v[130:133], v[10:17], v[182:189], v[130:133], v246, v247 op_sel_hi:[0,0,0]
	v_mfma_scale_f32_16x16x128_f8f6f4 v[118:121], v[2:9], v[204:211], v[118:121], v246, v247 op_sel_hi:[0,0,0]
	v_mfma_scale_f32_16x16x128_f8f6f4 v[114:117], v[10:17], v[204:211], v[114:117], v246, v247 op_sel_hi:[0,0,0]
	v_mfma_scale_f32_16x16x128_f8f6f4 v[102:105], v[2:9], v[212:219], v[102:105], v246, v247 op_sel_hi:[0,0,0]
	v_mfma_scale_f32_16x16x128_f8f6f4 v[98:101], v[10:17], v[212:219], v[98:101], v246, v247 op_sel_hi:[0,0,0]
	s_setprio 0
	s_barrier
	ds_read_b128 v[204:207], v194 offset:16384
	ds_read_b128 v[208:211], v194 offset:17408
	ds_read_b128 v[212:215], v194 offset:18432
	ds_read_b128 v[216:219], v194 offset:19456
	ds_read_b128 v[220:223], v194 offset:20480
	ds_read_b128 v[224:227], v194 offset:21504
	ds_read_b128 v[228:231], v194 offset:22528
	ds_read_b128 v[232:235], v194 offset:23552
	s_add_i32 s63, s63, s0
	v_lshl_add_u64 v[174:175], s[28:29], 0, v[0:1]
	s_mov_b32 m0, s63
	s_nop 0
	global_load_lds_dwordx4 v[174:175], off
	s_add_i32 m0, s63, 0x2000
	v_lshl_add_u64 v[176:177], s[28:29], 0, v[168:169]
	s_add_u32 s28, s28, s10
	s_addc_u32 s29, s29, s11
	s_add_i32 s63, s65, s0
	global_load_lds_dwordx4 v[176:177], off
	v_lshl_add_u64 v[178:179], s[28:29], 0, v[0:1]
	s_mov_b32 m0, s63
	v_lshl_add_u64 v[180:181], s[28:29], 0, v[168:169]
	global_load_lds_dwordx4 v[178:179], off
	s_add_i32 m0, s63, 0x2000
	v_lshl_add_u64 v[182:183], s[26:27], 0, v[164:165]
	global_load_lds_dwordx4 v[180:181], off
	s_mov_b32 m0, s1
	v_lshl_add_u64 v[184:185], s[26:27], 0, v[166:167]
	global_load_lds_dwordx4 v[182:183], off
	s_mov_b32 m0, s36
	s_nop 0
	global_load_lds_dwordx4 v[184:185], off
	s_waitcnt vmcnt(8)
	s_waitcnt lgkmcnt(0)
	s_barrier
	s_setprio 1
	s_waitcnt lgkmcnt(0)
	v_mfma_scale_f32_16x16x128_f8f6f4 v[94:97], v[18:25], v[204:211], v[94:97], v246, v247 op_sel_hi:[0,0,0]
	v_mfma_scale_f32_16x16x128_f8f6f4 v[90:93], v[26:33], v[204:211], v[90:93], v246, v247 op_sel_hi:[0,0,0]
	v_mfma_scale_f32_16x16x128_f8f6f4 v[78:81], v[18:25], v[212:219], v[78:81], v246, v247 op_sel_hi:[0,0,0]
	v_mfma_scale_f32_16x16x128_f8f6f4 v[74:77], v[26:33], v[212:219], v[74:77], v246, v247 op_sel_hi:[0,0,0]
	v_mfma_scale_f32_16x16x128_f8f6f4 v[62:65], v[18:25], v[220:227], v[62:65], v246, v247 op_sel_hi:[0,0,0]
	v_mfma_scale_f32_16x16x128_f8f6f4 v[58:61], v[26:33], v[220:227], v[58:61], v246, v247 op_sel_hi:[0,0,0]
	v_mfma_scale_f32_16x16x128_f8f6f4 v[46:49], v[18:25], v[228:235], v[46:49], v246, v247 op_sel_hi:[0,0,0]
	v_mfma_scale_f32_16x16x128_f8f6f4 v[42:45], v[26:33], v[228:235], v[42:45], v246, v247 op_sel_hi:[0,0,0]
	s_setprio 0
	s_setprio 1
	v_mfma_scale_f32_16x16x128_f8f6f4 v[86:89], v[2:9], v[204:211], v[86:89], v246, v247 op_sel_hi:[0,0,0]
	v_mfma_scale_f32_16x16x128_f8f6f4 v[82:85], v[10:17], v[204:211], v[82:85], v246, v247 op_sel_hi:[0,0,0]
	v_mfma_scale_f32_16x16x128_f8f6f4 v[70:73], v[2:9], v[212:219], v[70:73], v246, v247 op_sel_hi:[0,0,0]
	v_mfma_scale_f32_16x16x128_f8f6f4 v[66:69], v[10:17], v[212:219], v[66:69], v246, v247 op_sel_hi:[0,0,0]
	v_mfma_scale_f32_16x16x128_f8f6f4 v[54:57], v[2:9], v[220:227], v[54:57], v246, v247 op_sel_hi:[0,0,0]
	v_mfma_scale_f32_16x16x128_f8f6f4 v[50:53], v[10:17], v[220:227], v[50:53], v246, v247 op_sel_hi:[0,0,0]
	v_mfma_scale_f32_16x16x128_f8f6f4 v[38:41], v[2:9], v[228:235], v[38:41], v246, v247 op_sel_hi:[0,0,0]
	v_mfma_scale_f32_16x16x128_f8f6f4 v[34:37], v[10:17], v[228:235], v[34:37], v246, v247 op_sel_hi:[0,0,0]
	s_setprio 0
	s_barrier
; #define PG8_STAGE(bufoff, gbase, voff) do { _Pragma("unroll") for (int _i = 0; _i < 2; ++_i) \
;         __builtin_amdgcn_global_load_lds((const unsigned*)((const char*)(gbase) + (voff)[_i]), (PG8_LAS unsigned*)(lds + (bufoff) + ldsw + _i * 8192), 16, 0, 0); } while (0)
; #define PG8_WAIT_V(n) asm volatile("s_waitcnt vmcnt(" #n ")" ::: "memory")
; #define PG8_WAIT_L(n) asm volatile("s_waitcnt lgkmcnt(" #n ")" ::: "memory")
; #define PG8_BAR __builtin_amdgcn_s_barrier()
; #define PG8_SCHED __builtin_amdgcn_sched_barrier(0)
; template <class Epi, class Sched, bool ALIGN_EPI = false, bool SP2 = false, bool F8 = false>
; __device__ __forceinline__ void gemm_phase(PG8_LAS unsigned char* lds, const Gemm g, const Sched& S, const Epi& E, const int tidb  ) {
;     ...
;             PG8_LDB(B0, 1, 0); PG8_LDB(B1, 1, 1); PG8_SCHED; PG8_LDA(At, 1, 0); PG8_STAGE(PG8_SA(0, 1), a2 + hstep, voffA);
;             PG8_WAIT_V(8); PG8_WAIT_L(0); PG8_BAR; PG8_MMA(0, 0, At, B0); PG8_MMA(0, 1, At, B1); PG8_BAR; PG8_SCHED;
;             PG8_LDA(At, 1, 1); PG8_STAGE(PG8_SB(1, 0), b3, voffB); PG8_STAGE(PG8_SB(1, 1), b3 + hstep, voffB); PG8_STAGE(PG8_SA(1, 0), a3, voffA);
;             PG8_WAIT_V(8); PG8_WAIT_L(0); PG8_BAR; PG8_MMA(1, 0, At, B0); PG8_MMA(1, 1, At, B1); PG8_BAR; PG8_SCHED;
	s_add_i32 s28, 0, 0x18000
	s_add_i32 s29, 0, 0x1c000
	v_add_u32_e32 v14, s28, v192
	v_add_u32_e32 v30, s29, v192
	ds_read_b128 v[2:5], v14
	ds_read_b128 v[6:9], v14 offset:1024
	ds_read_b128 v[10:13], v14 offset:2048
	ds_read_b128 v[14:17], v14 offset:3072
	ds_read_b128 v[18:21], v30
	ds_read_b128 v[22:25], v30 offset:1024
	ds_read_b128 v[26:29], v30 offset:2048
	ds_read_b128 v[30:33], v30 offset:3072
	s_add_u32 s26, s26, s10
	s_addc_u32 s27, s27, s11
	s_mov_b32 m0, s37
	v_lshl_add_u64 v[186:187], s[26:27], 0, v[164:165]
	ds_read_b128 v[204:207], v194 offset:32768
	ds_read_b128 v[208:211], v194 offset:33792
	ds_read_b128 v[212:215], v194 offset:34816
	ds_read_b128 v[216:219], v194 offset:35840
	ds_read_b128 v[220:223], v194 offset:36864
	ds_read_b128 v[224:227], v194 offset:37888
	ds_read_b128 v[228:231], v194 offset:38912
	ds_read_b128 v[232:235], v194 offset:39936
	global_load_lds_dwordx4 v[186:187], off
	v_lshl_add_u64 v[186:187], s[26:27], 0, v[166:167]
	s_mov_b32 m0, s41
	s_nop 0
	global_load_lds_dwordx4 v[186:187], off
	s_waitcnt vmcnt(8)
	s_waitcnt lgkmcnt(0)
	s_barrier
	s_setprio 1
	s_waitcnt lgkmcnt(0)
	v_mfma_scale_f32_16x16x128_f8f6f4 v[158:161], v[2:9], v[204:211], v[158:161], v246, v247 op_sel_hi:[0,0,0]
	v_mfma_scale_f32_16x16x128_f8f6f4 v[154:157], v[10:17], v[204:211], v[154:157], v246, v247 op_sel_hi:[0,0,0]
	v_mfma_scale_f32_16x16x128_f8f6f4 v[142:145], v[2:9], v[212:219], v[142:145], v246, v247 op_sel_hi:[0,0,0]
	v_mfma_scale_f32_16x16x128_f8f6f4 v[138:141], v[10:17], v[212:219], v[138:141], v246, v247 op_sel_hi:[0,0,0]
	v_mfma_scale_f32_16x16x128_f8f6f4 v[126:129], v[2:9], v[220:227], v[126:129], v246, v247 op_sel_hi:[0,0,0]
	v_mfma_scale_f32_16x16x128_f8f6f4 v[122:125], v[10:17], v[220:227], v[122:125], v246, v247 op_sel_hi:[0,0,0]
	v_mfma_scale_f32_16x16x128_f8f6f4 v[110:113], v[2:9], v[228:235], v[110:113], v246, v247 op_sel_hi:[0,0,0]
	v_mfma_scale_f32_16x16x128_f8f6f4 v[106:109], v[10:17], v[228:235], v[106:109], v246, v247 op_sel_hi:[0,0,0]
	s_setprio 0
	s_setprio 1
	v_mfma_scale_f32_16x16x128_f8f6f4 v[150:153], v[18:25], v[204:211], v[150:153], v246, v247 op_sel_hi:[0,0,0]
	v_mfma_scale_f32_16x16x128_f8f6f4 v[146:149], v[26:33], v[204:211], v[146:149], v246, v247 op_sel_hi:[0,0,0]
	v_mfma_scale_f32_16x16x128_f8f6f4 v[134:137], v[18:25], v[212:219], v[134:137], v246, v247 op_sel_hi:[0,0,0]
	v_mfma_scale_f32_16x16x128_f8f6f4 v[130:133], v[26:33], v[212:219], v[130:133], v246, v247 op_sel_hi:[0,0,0]
	v_mfma_scale_f32_16x16x128_f8f6f4 v[118:121], v[18:25], v[220:227], v[118:121], v246, v247 op_sel_hi:[0,0,0]
	v_mfma_scale_f32_16x16x128_f8f6f4 v[114:117], v[26:33], v[220:227], v[114:117], v246, v247 op_sel_hi:[0,0,0]
	v_mfma_scale_f32_16x16x128_f8f6f4 v[102:105], v[18:25], v[228:235], v[102:105], v246, v247 op_sel_hi:[0,0,0]
	v_mfma_scale_f32_16x16x128_f8f6f4 v[98:101], v[26:33], v[228:235], v[98:101], v246, v247 op_sel_hi:[0,0,0]
	s_setprio 0
	s_barrier
	ds_read_b128 v[204:207], v194 offset:49152
	ds_read_b128 v[208:211], v194 offset:50176
	ds_read_b128 v[212:215], v194 offset:51200
	ds_read_b128 v[216:219], v194 offset:52224
	ds_read_b128 v[220:223], v194 offset:53248
	ds_read_b128 v[224:227], v194 offset:54272
	ds_read_b128 v[228:231], v194 offset:55296
	ds_read_b128 v[232:235], v194 offset:56320
	s_add_i32 s26, s28, s0
	v_lshl_add_u64 v[174:175], v[174:175], 0, s[92:93]
	s_mov_b32 m0, s26
	s_nop 0
	global_load_lds_dwordx4 v[174:175], off
	v_lshl_add_u64 v[174:175], v[176:177], 0, s[92:93]
	s_add_i32 m0, s26, 0x2000
	s_add_i32 s26, s29, s0
	global_load_lds_dwordx4 v[174:175], off
	v_lshl_add_u64 v[174:175], v[178:179], 0, s[92:93]
	s_mov_b32 m0, s26
	s_nop 0
	global_load_lds_dwordx4 v[174:175], off
	v_lshl_add_u64 v[174:175], v[180:181], 0, s[92:93]
	s_add_i32 m0, s26, 0x2000
	s_nop 0
	global_load_lds_dwordx4 v[174:175], off
	v_lshl_add_u64 v[174:175], v[182:183], 0, s[92:93]
	s_mov_b32 m0, s43
	s_nop 0
	global_load_lds_dwordx4 v[174:175], off
	v_lshl_add_u64 v[174:175], v[184:185], 0, s[92:93]
	s_mov_b32 m0, s45
	s_nop 0
	global_load_lds_dwordx4 v[174:175], off
	s_waitcnt vmcnt(8)
	s_waitcnt lgkmcnt(0)
	s_barrier
	s_setprio 1
	s_waitcnt lgkmcnt(0)
	v_mfma_scale_f32_16x16x128_f8f6f4 v[94:97], v[2:9], v[204:211], v[94:97], v246, v247 op_sel_hi:[0,0,0]
	v_mfma_scale_f32_16x16x128_f8f6f4 v[90:93], v[10:17], v[204:211], v[90:93], v246, v247 op_sel_hi:[0,0,0]
	v_mfma_scale_f32_16x16x128_f8f6f4 v[78:81], v[2:9], v[212:219], v[78:81], v246, v247 op_sel_hi:[0,0,0]
	v_mfma_scale_f32_16x16x128_f8f6f4 v[74:77], v[10:17], v[212:219], v[74:77], v246, v247 op_sel_hi:[0,0,0]
	v_mfma_scale_f32_16x16x128_f8f6f4 v[62:65], v[2:9], v[220:227], v[62:65], v246, v247 op_sel_hi:[0,0,0]
	v_mfma_scale_f32_16x16x128_f8f6f4 v[58:61], v[10:17], v[220:227], v[58:61], v246, v247 op_sel_hi:[0,0,0]
	v_mfma_scale_f32_16x16x128_f8f6f4 v[46:49], v[2:9], v[228:235], v[46:49], v246, v247 op_sel_hi:[0,0,0]
	v_mfma_scale_f32_16x16x128_f8f6f4 v[42:45], v[10:17], v[228:235], v[42:45], v246, v247 op_sel_hi:[0,0,0]
	s_setprio 0
	s_setprio 1
	v_mfma_scale_f32_16x16x128_f8f6f4 v[86:89], v[18:25], v[204:211], v[86:89], v246, v247 op_sel_hi:[0,0,0]
	v_mfma_scale_f32_16x16x128_f8f6f4 v[82:85], v[26:33], v[204:211], v[82:85], v246, v247 op_sel_hi:[0,0,0]
	v_mfma_scale_f32_16x16x128_f8f6f4 v[70:73], v[18:25], v[212:219], v[70:73], v246, v247 op_sel_hi:[0,0,0]
	v_mfma_scale_f32_16x16x128_f8f6f4 v[66:69], v[26:33], v[212:219], v[66:69], v246, v247 op_sel_hi:[0,0,0]
	s_add_u32 s24, s24, 0x100
	s_addc_u32 s25, s25, 0
	s_add_u32 s60, s60, 0x100
	s_addc_u32 s61, s61, 0
	s_cmp_ge_i32 s62, s46
	s_mov_b32 s26, s62
	v_mfma_scale_f32_16x16x128_f8f6f4 v[54:57], v[18:25], v[220:227], v[54:57], v246, v247 op_sel_hi:[0,0,0]
	v_mfma_scale_f32_16x16x128_f8f6f4 v[50:53], v[26:33], v[220:227], v[50:53], v246, v247 op_sel_hi:[0,0,0]
	v_mfma_scale_f32_16x16x128_f8f6f4 v[38:41], v[18:25], v[228:235], v[38:41], v246, v247 op_sel_hi:[0,0,0]
	v_mfma_scale_f32_16x16x128_f8f6f4 v[34:37], v[26:33], v[228:235], v[34:37], v246, v247 op_sel_hi:[0,0,0]
	s_setprio 0
	s_barrier
	s_cbranch_scc0 .LBB0_1042

; #define PG8_STAGE(bufoff, gbase, voff) do { _Pragma("unroll") for (int _i = 0; _i < 2; ++_i) \
;         __builtin_amdgcn_global_load_lds((const unsigned*)((const char*)(gbase) + (voff)[_i]), (PG8_LAS unsigned*)(lds + (bufoff) + ldsw + _i * 8192), 16, 0, 0); } while (0)
; #define PG8_WAIT_V(n) asm volatile("s_waitcnt vmcnt(" #n ")" ::: "memory")
; #define PG8_WAIT_L(n) asm volatile("s_waitcnt lgkmcnt(" #n ")" ::: "memory")
; #define PG8_BAR __builtin_amdgcn_s_barrier()
; #define PG8_SCHED __builtin_amdgcn_sched_barrier(0)
; template <class Epi, class Sched, bool ALIGN_EPI = false, bool SP2 = false, bool F8 = false>
; __device__ __forceinline__ void gemm_phase(PG8_LAS unsigned char* lds, const Gemm g, const Sched& S, const Epi& E, const int tidb  ) {
;     ...
;         for (int t = 0; t < nt; t += 2) {
;             const bool last = (t == nt - 2);
;             if constexpr (Epi::PREFETCH) { if (t == 0) E.prefetch(cur, wid, lane); }
;             const char* a1 = cA + (size_t)(t + 1) * kstep;
;             const char* a2 = last ? nA : cA + (size_t)(t + 2) * kstep; const char* b2 = last ? nB : cB + (size_t)(t + 2) * kstep;
;             const char* a3 = a2 + kstep; const char* b3 = b2 + kstep;
;             if (last && has_next) S.a_ready(nxt);
;             if constexpr (SP2) {
;             PG8_LDB(B0, 0, 0); PG8_LDB(B1, 0, 1); PG8_SCHED; PG8_LDA(At, 0, 0); PG8_STAGE(PG8_SA(1, 1), a1 + hstep, voffA);
;             PG8_WAIT_V(8); PG8_WAIT_L(0); PG8_BAR; PG8_MMA(0, 0, At, B0); PG8_MMA(0, 1, At, B1); PG8_BAR; PG8_SCHED;
;             PG8_LDA(At, 0, 1); PG8_STAGE(PG8_SB(0, 0), b2, voffB); PG8_STAGE(PG8_SB(0, 1), b2 + hstep, voffB); PG8_STAGE(PG8_SA(0, 0), a2, voffA);
;             PG8_WAIT_V(8); PG8_WAIT_L(0); PG8_BAR; PG8_MMA(1, 0, At, B0); PG8_MMA(1, 1, At, B1); PG8_BAR; PG8_SCHED;
.LBB0_1371:
	s_add_i32 s66, 0, 0x10000
	v_add_u32_e32 v0, s66, v192
	ds_read_b128 v[18:21], v0
	ds_read_b128 v[22:25], v0 offset:1024
	ds_read_b128 v[26:29], v0 offset:2048
	ds_read_b128 v[30:33], v0 offset:3072
	s_add_i32 s65, s24, 2
	s_add_u32 s67, s22, 0x80
	s_addc_u32 s25, s23, 0
	s_cmp_eq_u32 s57, s24
	s_cselect_b32 s25, s5, s25
	s_cselect_b32 s24, s4, s67
	s_cselect_b64 vcc, -1, 0
	s_add_i32 s67, 0, 0x14000
	v_add_u32_e32 v0, s67, v192
	ds_read_b128 v[2:5], v0
	ds_read_b128 v[6:9], v0 offset:1024
	ds_read_b128 v[10:13], v0 offset:2048
	ds_read_b128 v[14:17], v0 offset:3072
	v_cndmask_b32_e32 v189, v179, v177, vcc
	v_cndmask_b32_e32 v188, v178, v176, vcc
	v_lshl_add_u64 v[190:191], s[22:23], 0, v[172:173]
	s_add_i32 m0, s50, 0xc000
	ds_read_b128 v[180:183], v194
	ds_read_b128 v[184:187], v194 offset:1024
	ds_read_b128 v[204:207], v194 offset:2048
	ds_read_b128 v[208:211], v194 offset:3072
	ds_read_b128 v[212:215], v194 offset:4096
	ds_read_b128 v[216:219], v194 offset:5120
	ds_read_b128 v[220:223], v194 offset:6144
	ds_read_b128 v[224:227], v194 offset:7168
	global_load_lds_dwordx4 v[190:191], off
	v_lshl_add_u64 v[190:191], s[22:23], 0, v[174:175]
	s_add_i32 m0, s50, 0xe000
	s_nop 0
	global_load_lds_dwordx4 v[190:191], off
	s_waitcnt vmcnt(8)
	s_waitcnt lgkmcnt(0)
	s_barrier
	s_setprio 1
	s_waitcnt lgkmcnt(0)
	v_mfma_scale_f32_16x16x128_f8f6f4 v[154:157], v[18:25], v[180:187], v[154:157], v246, v253 op_sel_hi:[0,0,0]
	v_mfma_scale_f32_16x16x128_f8f6f4 v[150:153], v[26:33], v[180:187], v[150:153], v246, v253 op_sel_hi:[0,0,0]
	v_mfma_scale_f32_16x16x128_f8f6f4 v[142:145], v[18:25], v[204:211], v[142:145], v246, v253 op_sel_hi:[0,0,0]
	v_mfma_scale_f32_16x16x128_f8f6f4 v[134:137], v[26:33], v[204:211], v[134:137], v246, v253 op_sel_hi:[0,0,0]
	v_mfma_scale_f32_16x16x128_f8f6f4 v[126:129], v[18:25], v[212:219], v[126:129], v246, v253 op_sel_hi:[0,0,0]
	v_mfma_scale_f32_16x16x128_f8f6f4 v[118:121], v[26:33], v[212:219], v[118:121], v246, v253 op_sel_hi:[0,0,0]
	v_mfma_scale_f32_16x16x128_f8f6f4 v[110:113], v[18:25], v[220:227], v[110:113], v246, v253 op_sel_hi:[0,0,0]
	v_mfma_scale_f32_16x16x128_f8f6f4 v[102:105], v[26:33], v[220:227], v[102:105], v246, v253 op_sel_hi:[0,0,0]
	s_setprio 0
	s_setprio 1
	v_mfma_scale_f32_16x16x128_f8f6f4 v[158:161], v[2:9], v[180:187], v[158:161], v246, v253 op_sel_hi:[0,0,0]
	v_mfma_scale_f32_16x16x128_f8f6f4 v[146:149], v[10:17], v[180:187], v[146:149], v246, v253 op_sel_hi:[0,0,0]
	v_mfma_scale_f32_16x16x128_f8f6f4 v[138:141], v[2:9], v[204:211], v[138:141], v246, v253 op_sel_hi:[0,0,0]
	v_mfma_scale_f32_16x16x128_f8f6f4 v[130:133], v[10:17], v[204:211], v[130:133], v246, v253 op_sel_hi:[0,0,0]
	v_mfma_scale_f32_16x16x128_f8f6f4 v[122:125], v[2:9], v[212:219], v[122:125], v246, v253 op_sel_hi:[0,0,0]
	v_mfma_scale_f32_16x16x128_f8f6f4 v[114:117], v[10:17], v[212:219], v[114:117], v246, v253 op_sel_hi:[0,0,0]
	v_mfma_scale_f32_16x16x128_f8f6f4 v[106:109], v[2:9], v[220:227], v[106:109], v246, v253 op_sel_hi:[0,0,0]
	v_mfma_scale_f32_16x16x128_f8f6f4 v[98:101], v[10:17], v[220:227], v[98:101], v246, v253 op_sel_hi:[0,0,0]
	s_setprio 0
	s_barrier
	ds_read_b128 v[204:207], v194 offset:16384
	ds_read_b128 v[208:211], v194 offset:17408
	ds_read_b128 v[212:215], v194 offset:18432
	ds_read_b128 v[216:219], v194 offset:19456
	ds_read_b128 v[220:223], v194 offset:20480
	ds_read_b128 v[224:227], v194 offset:21504
	ds_read_b128 v[228:231], v194 offset:22528
	ds_read_b128 v[232:235], v194 offset:23552
	s_add_i32 s66, s66, s49
	v_lshl_add_u64 v[180:181], v[188:189], 0, v[166:167]
	s_mov_b32 m0, s66
	s_nop 0
	global_load_lds_dwordx4 v[180:181], off
	v_lshl_add_u64 v[182:183], v[188:189], 0, v[170:171]
	s_add_i32 m0, s66, 0x2000
	v_lshl_add_u64 v[186:187], v[188:189], 0, s[10:11]
	s_add_i32 s66, s67, s49
	global_load_lds_dwordx4 v[182:183], off
	v_lshl_add_u64 v[184:185], v[186:187], 0, v[166:167]
	s_mov_b32 m0, s66
	v_lshl_add_u64 v[186:187], v[186:187], 0, v[170:171]
	global_load_lds_dwordx4 v[184:185], off
	s_add_i32 m0, s66, 0x2000
	v_lshl_add_u64 v[188:189], s[24:25], 0, v[164:165]
	global_load_lds_dwordx4 v[186:187], off
	s_mov_b32 m0, s50
	v_lshl_add_u64 v[190:191], s[24:25], 0, v[168:169]
	global_load_lds_dwordx4 v[188:189], off
	s_mov_b32 m0, s51
	s_nop 0
	global_load_lds_dwordx4 v[190:191], off
	s_waitcnt vmcnt(8)
	s_waitcnt lgkmcnt(0)
	s_barrier
	s_setprio 1
	s_waitcnt lgkmcnt(0)
	v_mfma_scale_f32_16x16x128_f8f6f4 v[94:97], v[18:25], v[204:211], v[94:97], v246, v253 op_sel_hi:[0,0,0]
	v_mfma_scale_f32_16x16x128_f8f6f4 v[86:89], v[26:33], v[204:211], v[86:89], v246, v253 op_sel_hi:[0,0,0]
	v_mfma_scale_f32_16x16x128_f8f6f4 v[78:81], v[18:25], v[212:219], v[78:81], v246, v253 op_sel_hi:[0,0,0]
	v_mfma_scale_f32_16x16x128_f8f6f4 v[70:73], v[26:33], v[212:219], v[70:73], v246, v253 op_sel_hi:[0,0,0]
	v_mfma_scale_f32_16x16x128_f8f6f4 v[62:65], v[18:25], v[220:227], v[62:65], v246, v253 op_sel_hi:[0,0,0]
	v_mfma_scale_f32_16x16x128_f8f6f4 v[54:57], v[26:33], v[220:227], v[54:57], v246, v253 op_sel_hi:[0,0,0]
	v_mfma_scale_f32_16x16x128_f8f6f4 v[46:49], v[18:25], v[228:235], v[46:49], v246, v253 op_sel_hi:[0,0,0]
	v_mfma_scale_f32_16x16x128_f8f6f4 v[38:41], v[26:33], v[228:235], v[38:41], v246, v253 op_sel_hi:[0,0,0]
	s_setprio 0
	s_setprio 1
	v_mfma_scale_f32_16x16x128_f8f6f4 v[90:93], v[2:9], v[204:211], v[90:93], v246, v253 op_sel_hi:[0,0,0]
	v_mfma_scale_f32_16x16x128_f8f6f4 v[82:85], v[10:17], v[204:211], v[82:85], v246, v253 op_sel_hi:[0,0,0]
	v_mfma_scale_f32_16x16x128_f8f6f4 v[74:77], v[2:9], v[212:219], v[74:77], v246, v253 op_sel_hi:[0,0,0]
	v_mfma_scale_f32_16x16x128_f8f6f4 v[66:69], v[10:17], v[212:219], v[66:69], v246, v253 op_sel_hi:[0,0,0]
	v_mfma_scale_f32_16x16x128_f8f6f4 v[58:61], v[2:9], v[220:227], v[58:61], v246, v253 op_sel_hi:[0,0,0]
	v_mfma_scale_f32_16x16x128_f8f6f4 v[50:53], v[10:17], v[220:227], v[50:53], v246, v253 op_sel_hi:[0,0,0]
	v_mfma_scale_f32_16x16x128_f8f6f4 v[42:45], v[2:9], v[228:235], v[42:45], v246, v253 op_sel_hi:[0,0,0]
	v_mfma_scale_f32_16x16x128_f8f6f4 v[34:37], v[10:17], v[228:235], v[34:37], v246, v253 op_sel_hi:[0,0,0]
	s_setprio 0
	s_barrier
; #define PG8_STAGE(bufoff, gbase, voff) do { _Pragma("unroll") for (int _i = 0; _i < 2; ++_i) \
;         __builtin_amdgcn_global_load_lds((const unsigned*)((const char*)(gbase) + (voff)[_i]), (PG8_LAS unsigned*)(lds + (bufoff) + ldsw + _i * 8192), 16, 0, 0); } while (0)
; #define PG8_WAIT_V(n) asm volatile("s_waitcnt vmcnt(" #n ")" ::: "memory")
; #define PG8_WAIT_L(n) asm volatile("s_waitcnt lgkmcnt(" #n ")" ::: "memory")
; #define PG8_BAR __builtin_amdgcn_s_barrier()
; #define PG8_SCHED __builtin_amdgcn_sched_barrier(0)
; template <class Epi, class Sched, bool ALIGN_EPI = false, bool SP2 = false, bool F8 = false>
; __device__ __forceinline__ void gemm_phase(PG8_LAS unsigned char* lds, const Gemm g, const Sched& S, const Epi& E, const int tidb  ) {
;     ...
;             PG8_LDB(B0, 1, 0); PG8_LDB(B1, 1, 1); PG8_SCHED; PG8_LDA(At, 1, 0); PG8_STAGE(PG8_SA(0, 1), a2 + hstep, voffA);
;             PG8_WAIT_V(8); PG8_WAIT_L(0); PG8_BAR; PG8_MMA(0, 0, At, B0); PG8_MMA(0, 1, At, B1); PG8_BAR; PG8_SCHED;
;             PG8_LDA(At, 1, 1); PG8_STAGE(PG8_SB(1, 0), b3, voffB); PG8_STAGE(PG8_SB(1, 1), b3 + hstep, voffB); PG8_STAGE(PG8_SA(1, 0), a3, voffA);
;             PG8_WAIT_V(8); PG8_WAIT_L(0); PG8_BAR; PG8_MMA(1, 0, At, B0); PG8_MMA(1, 1, At, B1); PG8_BAR; PG8_SCHED;
	s_add_i32 s66, 0, 0x18000
	v_add_u32_e32 v0, s66, v192
	s_add_i32 s67, 0, 0x1c000
	ds_read_b128 v[2:5], v0
	ds_read_b128 v[6:9], v0 offset:1024
	ds_read_b128 v[10:13], v0 offset:2048
	ds_read_b128 v[14:17], v0 offset:3072
	v_add_u32_e32 v0, s67, v192
	ds_read_b128 v[18:21], v0
	ds_read_b128 v[22:25], v0 offset:1024
	ds_read_b128 v[26:29], v0 offset:2048
	ds_read_b128 v[30:33], v0 offset:3072
	s_add_u32 s24, s24, s10
	s_addc_u32 s25, s25, s11
	s_mov_b32 m0, s52
	v_lshl_add_u64 v[196:197], s[24:25], 0, v[164:165]
	ds_read_b128 v[204:207], v194 offset:32768
	ds_read_b128 v[208:211], v194 offset:33792
	ds_read_b128 v[212:215], v194 offset:34816
	ds_read_b128 v[216:219], v194 offset:35840
	ds_read_b128 v[220:223], v194 offset:36864
	ds_read_b128 v[224:227], v194 offset:37888
	ds_read_b128 v[228:231], v194 offset:38912
	ds_read_b128 v[232:235], v194 offset:39936
	global_load_lds_dwordx4 v[196:197], off
	v_lshl_add_u64 v[196:197], s[24:25], 0, v[168:169]
	s_mov_b32 m0, s53
	s_nop 0
	global_load_lds_dwordx4 v[196:197], off
	s_waitcnt vmcnt(8)
	s_waitcnt lgkmcnt(0)
	s_barrier
	s_setprio 1
	s_waitcnt lgkmcnt(0)
	v_mfma_scale_f32_16x16x128_f8f6f4 v[154:157], v[2:9], v[204:211], v[154:157], v246, v253 op_sel_hi:[0,0,0]
	v_mfma_scale_f32_16x16x128_f8f6f4 v[150:153], v[10:17], v[204:211], v[150:153], v246, v253 op_sel_hi:[0,0,0]
	v_mfma_scale_f32_16x16x128_f8f6f4 v[142:145], v[2:9], v[212:219], v[142:145], v246, v253 op_sel_hi:[0,0,0]
	v_mfma_scale_f32_16x16x128_f8f6f4 v[134:137], v[10:17], v[212:219], v[134:137], v246, v253 op_sel_hi:[0,0,0]
	v_mfma_scale_f32_16x16x128_f8f6f4 v[126:129], v[2:9], v[220:227], v[126:129], v246, v253 op_sel_hi:[0,0,0]
	v_mfma_scale_f32_16x16x128_f8f6f4 v[118:121], v[10:17], v[220:227], v[118:121], v246, v253 op_sel_hi:[0,0,0]
	v_mfma_scale_f32_16x16x128_f8f6f4 v[110:113], v[2:9], v[228:235], v[110:113], v246, v253 op_sel_hi:[0,0,0]
	v_mfma_scale_f32_16x16x128_f8f6f4 v[102:105], v[10:17], v[228:235], v[102:105], v246, v253 op_sel_hi:[0,0,0]
	s_setprio 0
	s_setprio 1
	v_mfma_scale_f32_16x16x128_f8f6f4 v[158:161], v[18:25], v[204:211], v[158:161], v246, v253 op_sel_hi:[0,0,0]
	v_mfma_scale_f32_16x16x128_f8f6f4 v[146:149], v[26:33], v[204:211], v[146:149], v246, v253 op_sel_hi:[0,0,0]
	v_mfma_scale_f32_16x16x128_f8f6f4 v[138:141], v[18:25], v[212:219], v[138:141], v246, v253 op_sel_hi:[0,0,0]
	v_mfma_scale_f32_16x16x128_f8f6f4 v[130:133], v[26:33], v[212:219], v[130:133], v246, v253 op_sel_hi:[0,0,0]
	v_mfma_scale_f32_16x16x128_f8f6f4 v[122:125], v[18:25], v[220:227], v[122:125], v246, v253 op_sel_hi:[0,0,0]
	v_mfma_scale_f32_16x16x128_f8f6f4 v[114:117], v[26:33], v[220:227], v[114:117], v246, v253 op_sel_hi:[0,0,0]
	v_mfma_scale_f32_16x16x128_f8f6f4 v[106:109], v[18:25], v[228:235], v[106:109], v246, v253 op_sel_hi:[0,0,0]
	v_mfma_scale_f32_16x16x128_f8f6f4 v[98:101], v[26:33], v[228:235], v[98:101], v246, v253 op_sel_hi:[0,0,0]
	s_setprio 0
	s_barrier
	ds_read_b128 v[204:207], v194 offset:49152
	ds_read_b128 v[208:211], v194 offset:50176
	ds_read_b128 v[212:215], v194 offset:51200
	ds_read_b128 v[216:219], v194 offset:52224
	ds_read_b128 v[220:223], v194 offset:53248
	ds_read_b128 v[224:227], v194 offset:54272
	ds_read_b128 v[228:231], v194 offset:55296
	ds_read_b128 v[232:235], v194 offset:56320
	s_add_i32 s24, s66, s49
	v_lshl_add_u64 v[180:181], v[180:181], 0, s[92:93]
	s_mov_b32 m0, s24
	s_nop 0
	global_load_lds_dwordx4 v[180:181], off
	v_lshl_add_u64 v[180:181], v[182:183], 0, s[92:93]
	s_add_i32 m0, s24, 0x2000
	s_add_i32 s24, s67, s49
	global_load_lds_dwordx4 v[180:181], off
	v_lshl_add_u64 v[180:181], v[184:185], 0, s[92:93]
	s_mov_b32 m0, s24
	s_nop 0
	global_load_lds_dwordx4 v[180:181], off
	v_lshl_add_u64 v[180:181], v[186:187], 0, s[92:93]
	s_add_i32 m0, s24, 0x2000
	s_nop 0
	global_load_lds_dwordx4 v[180:181], off
	v_lshl_add_u64 v[180:181], v[188:189], 0, s[92:93]
	s_mov_b32 m0, s54
	s_nop 0
	global_load_lds_dwordx4 v[180:181], off
	v_lshl_add_u64 v[180:181], v[190:191], 0, s[92:93]
	s_mov_b32 m0, s55
	s_nop 0
	global_load_lds_dwordx4 v[180:181], off
	s_waitcnt vmcnt(8)
	s_waitcnt lgkmcnt(0)
	s_barrier
	s_setprio 1
	s_waitcnt lgkmcnt(0)
	v_mfma_scale_f32_16x16x128_f8f6f4 v[94:97], v[2:9], v[204:211], v[94:97], v246, v253 op_sel_hi:[0,0,0]
	v_mfma_scale_f32_16x16x128_f8f6f4 v[86:89], v[10:17], v[204:211], v[86:89], v246, v253 op_sel_hi:[0,0,0]
	v_mfma_scale_f32_16x16x128_f8f6f4 v[78:81], v[2:9], v[212:219], v[78:81], v246, v253 op_sel_hi:[0,0,0]
	v_mfma_scale_f32_16x16x128_f8f6f4 v[70:73], v[10:17], v[212:219], v[70:73], v246, v253 op_sel_hi:[0,0,0]
	v_mfma_scale_f32_16x16x128_f8f6f4 v[62:65], v[2:9], v[220:227], v[62:65], v246, v253 op_sel_hi:[0,0,0]
	v_mfma_scale_f32_16x16x128_f8f6f4 v[54:57], v[10:17], v[220:227], v[54:57], v246, v253 op_sel_hi:[0,0,0]
	v_mfma_scale_f32_16x16x128_f8f6f4 v[46:49], v[2:9], v[228:235], v[46:49], v246, v253 op_sel_hi:[0,0,0]
	v_mfma_scale_f32_16x16x128_f8f6f4 v[38:41], v[10:17], v[228:235], v[38:41], v246, v253 op_sel_hi:[0,0,0]
	s_setprio 0
	s_setprio 1
	v_mfma_scale_f32_16x16x128_f8f6f4 v[90:93], v[18:25], v[204:211], v[90:93], v246, v253 op_sel_hi:[0,0,0]
	v_mfma_scale_f32_16x16x128_f8f6f4 v[82:85], v[26:33], v[204:211], v[82:85], v246, v253 op_sel_hi:[0,0,0]
	v_mfma_scale_f32_16x16x128_f8f6f4 v[74:77], v[18:25], v[212:219], v[74:77], v246, v253 op_sel_hi:[0,0,0]
	v_mfma_scale_f32_16x16x128_f8f6f4 v[66:69], v[26:33], v[212:219], v[66:69], v246, v253 op_sel_hi:[0,0,0]
	s_add_u32 s22, s22, 0x100
	s_addc_u32 s23, s23, 0
	v_lshl_add_u64 v[178:179], v[178:179], 0, s[84:85]
	s_cmp_ge_i32 s65, s56
	s_mov_b32 s24, s65
	v_mfma_scale_f32_16x16x128_f8f6f4 v[58:61], v[18:25], v[220:227], v[58:61], v246, v253 op_sel_hi:[0,0,0]
	v_mfma_scale_f32_16x16x128_f8f6f4 v[50:53], v[26:33], v[220:227], v[50:53], v246, v253 op_sel_hi:[0,0,0]
	v_mfma_scale_f32_16x16x128_f8f6f4 v[42:45], v[18:25], v[228:235], v[42:45], v246, v253 op_sel_hi:[0,0,0]
	v_mfma_scale_f32_16x16x128_f8f6f4 v[34:37], v[26:33], v[228:235], v[34:37], v246, v253 op_sel_hi:[0,0,0]
	s_setprio 0
	s_barrier
	s_cbranch_scc0 .LBB0_1371
	s_movk_i32 s67, 0x300

; #define PG8_STAGE(bufoff, gbase, voff) do { _Pragma("unroll") for (int _i = 0; _i < 2; ++_i) \
;         __builtin_amdgcn_global_load_lds((const unsigned*)((const char*)(gbase) + (voff)[_i]), (PG8_LAS unsigned*)(lds + (bufoff) + ldsw + _i * 8192), 16, 0, 0); } while (0)
; #define PG8_WAIT_V(n) asm volatile("s_waitcnt vmcnt(" #n ")" ::: "memory")
; #define PG8_WAIT_L(n) asm volatile("s_waitcnt lgkmcnt(" #n ")" ::: "memory")
; #define PG8_BAR __builtin_amdgcn_s_barrier()
; #define PG8_SCHED __builtin_amdgcn_sched_barrier(0)
; template <class Epi, class Sched, bool ALIGN_EPI = false, bool SP2 = false, bool F8 = false>
; __device__ __forceinline__ void gemm_phase(PG8_LAS unsigned char* lds, const Gemm g, const Sched& S, const Epi& E, const int tidb  ) {
;     ...
;             const char* a1 = cA + (size_t)(t + 1) * kstep;
;             const char* a2 = last ? nA : cA + (size_t)(t + 2) * kstep; const char* b2 = last ? nB : cB + (size_t)(t + 2) * kstep;
;             const char* a3 = a2 + kstep; const char* b3 = b2 + kstep;
;             if (last && has_next) S.a_ready(nxt);
;             if constexpr (SP2) {
;             PG8_LDB(B0, 0, 0); PG8_LDB(B1, 0, 1); PG8_SCHED; PG8_LDA(At, 0, 0); PG8_STAGE(PG8_SA(1, 1), a1 + hstep, voffA);
;             PG8_WAIT_V(8); PG8_WAIT_L(0); PG8_BAR; PG8_MMA(0, 0, At, B0); PG8_MMA(0, 1, At, B1); PG8_BAR; PG8_SCHED;
;             PG8_LDA(At, 0, 1); PG8_STAGE(PG8_SB(0, 0), b2, voffB); PG8_STAGE(PG8_SB(0, 1), b2 + hstep, voffB); PG8_STAGE(PG8_SA(0, 0), a2, voffA);
;             PG8_WAIT_V(8); PG8_WAIT_L(0); PG8_BAR; PG8_MMA(1, 0, At, B0); PG8_MMA(1, 1, At, B1); PG8_BAR; PG8_SCHED;
.LBB0_1452:
	ds_read_b128 v[6:9], v175 offset:3072
	ds_read_b128 v[2:5], v175 offset:2048
	ds_read_b128 v[182:185], v175 offset:1024
	ds_read_b128 v[178:181], v175
	ds_read_b128 v[190:193], v0 offset:3072
	ds_read_b128 v[186:189], v0 offset:2048
	ds_read_b128 v[208:211], v0 offset:1024
	ds_read_b128 v[204:207], v0
	s_add_u32 s54, s52, 0x80
	s_addc_u32 s55, s53, 0
	s_cmp_eq_u32 s66, s72
	s_cselect_b64 vcc, -1, 0
	s_cselect_b32 s55, s7, s55
	s_cselect_b32 s54, s6, s54
	v_cndmask_b32_e32 v161, v155, v153, vcc
	v_cndmask_b32_e32 v160, v154, v152, vcc
	s_mov_b32 m0, s35
	v_lshl_add_u64 v[156:157], s[52:53], 0, v[148:149]
	ds_read_b128 v[212:215], v174
	ds_read_b128 v[216:219], v174 offset:1024
	ds_read_b128 v[220:223], v174 offset:2048
	ds_read_b128 v[224:227], v174 offset:3072
	ds_read_b128 v[228:231], v174 offset:4096
	ds_read_b128 v[232:235], v174 offset:5120
	ds_read_b128 v[236:239], v174 offset:6144
	ds_read_b128 v[240:243], v174 offset:7168
	global_load_lds_dwordx4 v[156:157], off
	v_lshl_add_u64 v[156:157], s[52:53], 0, v[150:151]
	s_mov_b32 m0, s56
	s_nop 0
	global_load_lds_dwordx4 v[156:157], off
	s_waitcnt vmcnt(8)
	s_waitcnt lgkmcnt(0)
	s_barrier
	s_setprio 1
	s_waitcnt lgkmcnt(0)
	v_mfma_scale_f32_16x16x128_f8f6f4 v[134:137], v[204:211], v[212:219], v[134:137], v246, v247 op_sel_hi:[0,0,0]
	v_mfma_scale_f32_16x16x128_f8f6f4 v[130:133], v[186:193], v[212:219], v[130:133], v246, v247 op_sel_hi:[0,0,0]
	v_mfma_scale_f32_16x16x128_f8f6f4 v[118:121], v[204:211], v[220:227], v[118:121], v246, v247 op_sel_hi:[0,0,0]
	v_mfma_scale_f32_16x16x128_f8f6f4 v[114:117], v[186:193], v[220:227], v[114:117], v246, v247 op_sel_hi:[0,0,0]
	v_mfma_scale_f32_16x16x128_f8f6f4 v[102:105], v[204:211], v[228:235], v[102:105], v246, v247 op_sel_hi:[0,0,0]
	v_mfma_scale_f32_16x16x128_f8f6f4 v[98:101], v[186:193], v[228:235], v[98:101], v246, v247 op_sel_hi:[0,0,0]
	v_mfma_scale_f32_16x16x128_f8f6f4 v[86:89], v[204:211], v[236:243], v[86:89], v246, v247 op_sel_hi:[0,0,0]
	v_mfma_scale_f32_16x16x128_f8f6f4 v[82:85], v[186:193], v[236:243], v[82:85], v246, v247 op_sel_hi:[0,0,0]
	s_setprio 0
	s_setprio 1
	v_mfma_scale_f32_16x16x128_f8f6f4 v[126:129], v[178:185], v[212:219], v[126:129], v246, v247 op_sel_hi:[0,0,0]
	v_mfma_scale_f32_16x16x128_f8f6f4 v[122:125], v[2:9], v[212:219], v[122:125], v246, v247 op_sel_hi:[0,0,0]
	v_mfma_scale_f32_16x16x128_f8f6f4 v[110:113], v[178:185], v[220:227], v[110:113], v246, v247 op_sel_hi:[0,0,0]
	v_mfma_scale_f32_16x16x128_f8f6f4 v[106:109], v[2:9], v[220:227], v[106:109], v246, v247 op_sel_hi:[0,0,0]
	v_mfma_scale_f32_16x16x128_f8f6f4 v[94:97], v[178:185], v[228:235], v[94:97], v246, v247 op_sel_hi:[0,0,0]
	v_mfma_scale_f32_16x16x128_f8f6f4 v[90:93], v[2:9], v[228:235], v[90:93], v246, v247 op_sel_hi:[0,0,0]
	v_mfma_scale_f32_16x16x128_f8f6f4 v[78:81], v[178:185], v[236:243], v[78:81], v246, v247 op_sel_hi:[0,0,0]
	v_mfma_scale_f32_16x16x128_f8f6f4 v[70:73], v[2:9], v[236:243], v[70:73], v246, v247 op_sel_hi:[0,0,0]
	s_setprio 0
	s_barrier
	ds_read_b128 v[212:215], v174 offset:16384
	ds_read_b128 v[216:219], v174 offset:17408
	ds_read_b128 v[220:223], v174 offset:18432
	ds_read_b128 v[224:227], v174 offset:19456
	ds_read_b128 v[228:231], v174 offset:20480
	ds_read_b128 v[232:235], v174 offset:21504
	ds_read_b128 v[236:239], v174 offset:22528
	ds_read_b128 v[240:243], v174 offset:23552
	s_mov_b32 m0, s57
	v_lshl_add_u64 v[156:157], v[160:161], 0, v[140:141]
	global_load_lds_dwordx4 v[156:157], off
	v_lshl_add_u64 v[158:159], v[160:161], 0, v[144:145]
	s_mov_b32 m0, s68
	v_lshl_add_u64 v[164:165], v[160:161], 0, s[16:17]
	global_load_lds_dwordx4 v[158:159], off
	v_lshl_add_u64 v[160:161], v[164:165], 0, v[140:141]
	s_mov_b32 m0, s70
	v_lshl_add_u64 v[164:165], v[164:165], 0, v[144:145]
	global_load_lds_dwordx4 v[160:161], off
	s_mov_b32 m0, s71
	v_lshl_add_u64 v[166:167], s[54:55], 0, v[138:139]
	global_load_lds_dwordx4 v[164:165], off
	s_mov_b32 m0, s59
	v_lshl_add_u64 v[168:169], s[54:55], 0, v[142:143]
	global_load_lds_dwordx4 v[166:167], off
	s_mov_b32 m0, s60
	s_nop 0
	global_load_lds_dwordx4 v[168:169], off
	s_waitcnt vmcnt(8)
	s_waitcnt lgkmcnt(0)
	s_barrier
	s_setprio 1
	s_waitcnt lgkmcnt(0)
	v_mfma_scale_f32_16x16x128_f8f6f4 v[74:77], v[204:211], v[212:219], v[74:77], v246, v247 op_sel_hi:[0,0,0]
	v_mfma_scale_f32_16x16x128_f8f6f4 v[66:69], v[186:193], v[212:219], v[66:69], v246, v247 op_sel_hi:[0,0,0]
	v_mfma_scale_f32_16x16x128_f8f6f4 v[54:57], v[204:211], v[220:227], v[54:57], v246, v247 op_sel_hi:[0,0,0]
	v_mfma_scale_f32_16x16x128_f8f6f4 v[50:53], v[186:193], v[220:227], v[50:53], v246, v247 op_sel_hi:[0,0,0]
	v_mfma_scale_f32_16x16x128_f8f6f4 v[38:41], v[204:211], v[228:235], v[38:41], v246, v247 op_sel_hi:[0,0,0]
	v_mfma_scale_f32_16x16x128_f8f6f4 v[34:37], v[186:193], v[228:235], v[34:37], v246, v247 op_sel_hi:[0,0,0]
	v_mfma_scale_f32_16x16x128_f8f6f4 v[22:25], v[204:211], v[236:243], v[22:25], v246, v247 op_sel_hi:[0,0,0]
	v_mfma_scale_f32_16x16x128_f8f6f4 v[18:21], v[186:193], v[236:243], v[18:21], v246, v247 op_sel_hi:[0,0,0]
	s_setprio 0
	s_setprio 1
	v_mfma_scale_f32_16x16x128_f8f6f4 v[62:65], v[178:185], v[212:219], v[62:65], v246, v247 op_sel_hi:[0,0,0]
	v_mfma_scale_f32_16x16x128_f8f6f4 v[58:61], v[2:9], v[212:219], v[58:61], v246, v247 op_sel_hi:[0,0,0]
	v_mfma_scale_f32_16x16x128_f8f6f4 v[46:49], v[178:185], v[220:227], v[46:49], v246, v247 op_sel_hi:[0,0,0]
	v_mfma_scale_f32_16x16x128_f8f6f4 v[42:45], v[2:9], v[220:227], v[42:45], v246, v247 op_sel_hi:[0,0,0]
	v_mfma_scale_f32_16x16x128_f8f6f4 v[30:33], v[178:185], v[228:235], v[30:33], v246, v247 op_sel_hi:[0,0,0]
	v_mfma_scale_f32_16x16x128_f8f6f4 v[26:29], v[2:9], v[228:235], v[26:29], v246, v247 op_sel_hi:[0,0,0]
	v_mfma_scale_f32_16x16x128_f8f6f4 v[14:17], v[178:185], v[236:243], v[14:17], v246, v247 op_sel_hi:[0,0,0]
	v_mfma_scale_f32_16x16x128_f8f6f4 v[10:13], v[2:9], v[236:243], v[10:13], v246, v247 op_sel_hi:[0,0,0]
	s_setprio 0
	s_barrier
; #define PG8_STAGE(bufoff, gbase, voff) do { _Pragma("unroll") for (int _i = 0; _i < 2; ++_i) \
;         __builtin_amdgcn_global_load_lds((const unsigned*)((const char*)(gbase) + (voff)[_i]), (PG8_LAS unsigned*)(lds + (bufoff) + ldsw + _i * 8192), 16, 0, 0); } while (0)
; #define PG8_WAIT_V(n) asm volatile("s_waitcnt vmcnt(" #n ")" ::: "memory")
; #define PG8_WAIT_L(n) asm volatile("s_waitcnt lgkmcnt(" #n ")" ::: "memory")
; #define PG8_BAR __builtin_amdgcn_s_barrier()
; #define PG8_SCHED __builtin_amdgcn_sched_barrier(0)
; template <class Epi, class Sched, bool ALIGN_EPI = false, bool SP2 = false, bool F8 = false>
; __device__ __forceinline__ void gemm_phase(PG8_LAS unsigned char* lds, const Gemm g, const Sched& S, const Epi& E, const int tidb  ) {
;     ...
;             PG8_LDB(B0, 1, 0); PG8_LDB(B1, 1, 1); PG8_SCHED; PG8_LDA(At, 1, 0); PG8_STAGE(PG8_SA(0, 1), a2 + hstep, voffA);
;             PG8_WAIT_V(8); PG8_WAIT_L(0); PG8_BAR; PG8_MMA(0, 0, At, B0); PG8_MMA(0, 1, At, B1); PG8_BAR; PG8_SCHED;
;             PG8_LDA(At, 1, 1); PG8_STAGE(PG8_SB(1, 0), b3, voffB); PG8_STAGE(PG8_SB(1, 1), b3 + hstep, voffB); PG8_STAGE(PG8_SA(1, 0), a3, voffA);
;             PG8_WAIT_V(8); PG8_WAIT_L(0); PG8_BAR; PG8_MMA(1, 0, At, B0); PG8_MMA(1, 1, At, B1); PG8_BAR; PG8_SCHED;
	ds_read_b128 v[178:181], v176
	ds_read_b128 v[182:185], v176 offset:1024
	ds_read_b128 v[186:189], v176 offset:2048
	ds_read_b128 v[190:193], v176 offset:3072
	ds_read_b128 v[2:5], v177
	ds_read_b128 v[6:9], v177 offset:1024
	ds_read_b128 v[204:207], v177 offset:2048
	ds_read_b128 v[208:211], v177 offset:3072
	s_add_u32 s54, s54, s16
	s_addc_u32 s55, s55, s17
	s_mov_b32 m0, s61
	v_lshl_add_u64 v[194:195], s[54:55], 0, v[138:139]
	ds_read_b128 v[212:215], v174 offset:32768
	ds_read_b128 v[216:219], v174 offset:33792
	ds_read_b128 v[220:223], v174 offset:34816
	ds_read_b128 v[224:227], v174 offset:35840
	ds_read_b128 v[228:231], v174 offset:36864
	ds_read_b128 v[232:235], v174 offset:37888
	ds_read_b128 v[236:239], v174 offset:38912
	ds_read_b128 v[240:243], v174 offset:39936
	global_load_lds_dwordx4 v[194:195], off
	v_lshl_add_u64 v[194:195], s[54:55], 0, v[142:143]
	s_mov_b32 m0, s62
	s_nop 0
	global_load_lds_dwordx4 v[194:195], off
	s_waitcnt vmcnt(8)
	s_waitcnt lgkmcnt(0)
	s_barrier
	s_setprio 1
	s_waitcnt lgkmcnt(0)
	v_mfma_scale_f32_16x16x128_f8f6f4 v[134:137], v[178:185], v[212:219], v[134:137], v246, v247 op_sel_hi:[0,0,0]
	v_mfma_scale_f32_16x16x128_f8f6f4 v[130:133], v[186:193], v[212:219], v[130:133], v246, v247 op_sel_hi:[0,0,0]
	v_mfma_scale_f32_16x16x128_f8f6f4 v[118:121], v[178:185], v[220:227], v[118:121], v246, v247 op_sel_hi:[0,0,0]
	v_mfma_scale_f32_16x16x128_f8f6f4 v[114:117], v[186:193], v[220:227], v[114:117], v246, v247 op_sel_hi:[0,0,0]
	v_mfma_scale_f32_16x16x128_f8f6f4 v[102:105], v[178:185], v[228:235], v[102:105], v246, v247 op_sel_hi:[0,0,0]
	v_mfma_scale_f32_16x16x128_f8f6f4 v[98:101], v[186:193], v[228:235], v[98:101], v246, v247 op_sel_hi:[0,0,0]
	v_mfma_scale_f32_16x16x128_f8f6f4 v[86:89], v[178:185], v[236:243], v[86:89], v246, v247 op_sel_hi:[0,0,0]
	v_mfma_scale_f32_16x16x128_f8f6f4 v[82:85], v[186:193], v[236:243], v[82:85], v246, v247 op_sel_hi:[0,0,0]
	s_setprio 0
	s_setprio 1
	v_mfma_scale_f32_16x16x128_f8f6f4 v[126:129], v[2:9], v[212:219], v[126:129], v246, v247 op_sel_hi:[0,0,0]
	v_mfma_scale_f32_16x16x128_f8f6f4 v[122:125], v[204:211], v[212:219], v[122:125], v246, v247 op_sel_hi:[0,0,0]
	v_mfma_scale_f32_16x16x128_f8f6f4 v[110:113], v[2:9], v[220:227], v[110:113], v246, v247 op_sel_hi:[0,0,0]
	v_mfma_scale_f32_16x16x128_f8f6f4 v[106:109], v[204:211], v[220:227], v[106:109], v246, v247 op_sel_hi:[0,0,0]
	v_mfma_scale_f32_16x16x128_f8f6f4 v[94:97], v[2:9], v[228:235], v[94:97], v246, v247 op_sel_hi:[0,0,0]
	v_mfma_scale_f32_16x16x128_f8f6f4 v[90:93], v[204:211], v[228:235], v[90:93], v246, v247 op_sel_hi:[0,0,0]
	v_mfma_scale_f32_16x16x128_f8f6f4 v[78:81], v[2:9], v[236:243], v[78:81], v246, v247 op_sel_hi:[0,0,0]
	v_mfma_scale_f32_16x16x128_f8f6f4 v[70:73], v[204:211], v[236:243], v[70:73], v246, v247 op_sel_hi:[0,0,0]
	s_setprio 0
	s_barrier
	ds_read_b128 v[212:215], v174 offset:49152
	ds_read_b128 v[216:219], v174 offset:50176
	ds_read_b128 v[220:223], v174 offset:51200
	ds_read_b128 v[224:227], v174 offset:52224
	ds_read_b128 v[228:231], v174 offset:53248
	ds_read_b128 v[232:235], v174 offset:54272
	ds_read_b128 v[236:239], v174 offset:55296
	ds_read_b128 v[240:243], v174 offset:56320
	s_mov_b32 m0, s91
	v_lshl_add_u64 v[156:157], v[156:157], 0, s[92:93]
	global_load_lds_dwordx4 v[156:157], off
	v_lshl_add_u64 v[156:157], v[158:159], 0, s[92:93]
	s_mov_b32 m0, s94
	s_nop 0
	global_load_lds_dwordx4 v[156:157], off
	v_lshl_add_u64 v[156:157], v[160:161], 0, s[92:93]
	s_mov_b32 m0, s95
	s_nop 0
	global_load_lds_dwordx4 v[156:157], off
	v_lshl_add_u64 v[156:157], v[164:165], 0, s[92:93]
	s_mov_b32 m0, s97
	s_nop 0
	global_load_lds_dwordx4 v[156:157], off
	v_lshl_add_u64 v[156:157], v[166:167], 0, s[92:93]
	s_mov_b32 m0, s63
	s_nop 0
	global_load_lds_dwordx4 v[156:157], off
	v_lshl_add_u64 v[156:157], v[168:169], 0, s[92:93]
	s_mov_b32 m0, s65
	s_nop 0
	global_load_lds_dwordx4 v[156:157], off
	s_waitcnt vmcnt(8)
	s_waitcnt lgkmcnt(0)
	s_barrier
	s_setprio 1
	s_waitcnt lgkmcnt(0)
	v_mfma_scale_f32_16x16x128_f8f6f4 v[74:77], v[178:185], v[212:219], v[74:77], v246, v247 op_sel_hi:[0,0,0]
	v_mfma_scale_f32_16x16x128_f8f6f4 v[66:69], v[186:193], v[212:219], v[66:69], v246, v247 op_sel_hi:[0,0,0]
	v_mfma_scale_f32_16x16x128_f8f6f4 v[54:57], v[178:185], v[220:227], v[54:57], v246, v247 op_sel_hi:[0,0,0]
	v_mfma_scale_f32_16x16x128_f8f6f4 v[50:53], v[186:193], v[220:227], v[50:53], v246, v247 op_sel_hi:[0,0,0]
	v_mfma_scale_f32_16x16x128_f8f6f4 v[38:41], v[178:185], v[228:235], v[38:41], v246, v247 op_sel_hi:[0,0,0]
	v_mfma_scale_f32_16x16x128_f8f6f4 v[34:37], v[186:193], v[228:235], v[34:37], v246, v247 op_sel_hi:[0,0,0]
	v_mfma_scale_f32_16x16x128_f8f6f4 v[22:25], v[178:185], v[236:243], v[22:25], v246, v247 op_sel_hi:[0,0,0]
	v_mfma_scale_f32_16x16x128_f8f6f4 v[18:21], v[186:193], v[236:243], v[18:21], v246, v247 op_sel_hi:[0,0,0]
	s_setprio 0
	s_setprio 1
	v_mfma_scale_f32_16x16x128_f8f6f4 v[62:65], v[2:9], v[212:219], v[62:65], v246, v247 op_sel_hi:[0,0,0]
	v_mfma_scale_f32_16x16x128_f8f6f4 v[58:61], v[204:211], v[212:219], v[58:61], v246, v247 op_sel_hi:[0,0,0]
	v_mfma_scale_f32_16x16x128_f8f6f4 v[46:49], v[2:9], v[220:227], v[46:49], v246, v247 op_sel_hi:[0,0,0]
	v_mfma_scale_f32_16x16x128_f8f6f4 v[42:45], v[204:211], v[220:227], v[42:45], v246, v247 op_sel_hi:[0,0,0]
	s_add_i32 s54, s72, 2
	s_add_u32 s52, s52, 0x100
	s_addc_u32 s53, s53, 0
	v_lshl_add_u64 v[154:155], v[154:155], 0, s[10:11]
	s_cmp_ge_i32 s72, s66
	s_mov_b32 s72, s54
	v_mfma_scale_f32_16x16x128_f8f6f4 v[30:33], v[2:9], v[228:235], v[30:33], v246, v247 op_sel_hi:[0,0,0]
	v_mfma_scale_f32_16x16x128_f8f6f4 v[26:29], v[204:211], v[228:235], v[26:29], v246, v247 op_sel_hi:[0,0,0]
	v_mfma_scale_f32_16x16x128_f8f6f4 v[14:17], v[2:9], v[236:243], v[14:17], v246, v247 op_sel_hi:[0,0,0]
	v_mfma_scale_f32_16x16x128_f8f6f4 v[10:13], v[204:211], v[236:243], v[10:13], v246, v247 op_sel_hi:[0,0,0]
	s_setprio 0
	s_barrier
	s_cbranch_scc0 .LBB0_1452

; #define PG8_STAGE(bufoff, gbase, voff) do { _Pragma("unroll") for (int _i = 0; _i < 2; ++_i) \
;         __builtin_amdgcn_global_load_lds((const unsigned*)((const char*)(gbase) + (voff)[_i]), (PG8_LAS unsigned*)(lds + (bufoff) + ldsw + _i * 8192), 16, 0, 0); } while (0)
; #define PG8_WAIT_V(n) asm volatile("s_waitcnt vmcnt(" #n ")" ::: "memory")
; #define PG8_WAIT_L(n) asm volatile("s_waitcnt lgkmcnt(" #n ")" ::: "memory")
; #define PG8_BAR __builtin_amdgcn_s_barrier()
; #define PG8_SCHED __builtin_amdgcn_sched_barrier(0)
; template <class Epi, class Sched, bool ALIGN_EPI = false, bool SP2 = false, bool F8 = false>
; __device__ __forceinline__ void gemm_phase(PG8_LAS unsigned char* lds, const Gemm g, const Sched& S, const Epi& E, const int tidb  ) {
;     ...
;             const char* a1 = cA + (size_t)(t + 1) * kstep;
;             const char* a2 = last ? nA : cA + (size_t)(t + 2) * kstep; const char* b2 = last ? nB : cB + (size_t)(t + 2) * kstep;
;             const char* a3 = a2 + kstep; const char* b3 = b2 + kstep;
;             if (last && has_next) S.a_ready(nxt);
;             if constexpr (SP2) {
;             PG8_LDB(B0, 0, 0); PG8_LDB(B1, 0, 1); PG8_SCHED; PG8_LDA(At, 0, 0); PG8_STAGE(PG8_SA(1, 1), a1 + hstep, voffA);
;             PG8_WAIT_V(8); PG8_WAIT_L(0); PG8_BAR; PG8_MMA(0, 0, At, B0); PG8_MMA(0, 1, At, B1); PG8_BAR; PG8_SCHED;
;             PG8_LDA(At, 0, 1); PG8_STAGE(PG8_SB(0, 0), b2, voffB); PG8_STAGE(PG8_SB(0, 1), b2 + hstep, voffB); PG8_STAGE(PG8_SA(0, 0), a2, voffA);
;             PG8_WAIT_V(8); PG8_WAIT_L(0); PG8_BAR; PG8_MMA(1, 0, At, B0); PG8_MMA(1, 1, At, B1); PG8_BAR; PG8_SCHED;
.LBB0_1705:
	s_add_i32 s65, 0, 0x10000
	v_add_u32_e32 v148, s65, v151
	ds_read_b128 v[140:143], v148
	ds_read_b128 v[144:147], v148 offset:1024
	ds_read_b128 v[158:161], v148 offset:2048
	ds_read_b128 v[164:167], v148 offset:3072
	s_add_i32 s60, s28, 2
	s_add_u32 s61, s26, 0x80
	s_addc_u32 s29, s27, 0
	s_cmp_eq_u32 s51, s28
	s_cselect_b32 s29, s5, s29
	s_cselect_b32 s28, s4, s61
	s_cselect_b32 s63, s25, s59
	s_cselect_b32 s62, s24, s58
	s_add_i32 s61, 0, 0x14000
	v_add_u32_e32 v148, s61, v151
	ds_read_b128 v[168:171], v148
	ds_read_b128 v[172:175], v148 offset:1024
	ds_read_b128 v[176:179], v148 offset:2048
	ds_read_b128 v[180:183], v148 offset:3072
	v_lshl_add_u64 v[148:149], s[26:27], 0, v[136:137]
	s_add_i32 m0, s41, 0xc000
	ds_read_b128 v[184:187], v156
	ds_read_b128 v[188:191], v156 offset:1024
	ds_read_b128 v[192:195], v156 offset:2048
	ds_read_b128 v[204:207], v156 offset:3072
	ds_read_b128 v[208:211], v156 offset:4096
	ds_read_b128 v[212:215], v156 offset:5120
	ds_read_b128 v[216:219], v156 offset:6144
	ds_read_b128 v[220:223], v156 offset:7168
	global_load_lds_dwordx4 v[148:149], off
	v_lshl_add_u64 v[148:149], s[26:27], 0, v[138:139]
	s_add_i32 m0, s41, 0xe000
	s_nop 0
	global_load_lds_dwordx4 v[148:149], off
	s_waitcnt vmcnt(8)
	s_waitcnt lgkmcnt(0)
	s_barrier
	s_setprio 1
	s_waitcnt lgkmcnt(0)
	v_mfma_f32_16x16x32_bf16 v[122:125], v[140:143], v[184:187], v[122:125]
	v_mfma_f32_16x16x32_bf16 v[118:121], v[158:161], v[184:187], v[118:121]
	v_mfma_f32_16x16x32_bf16 v[110:113], v[140:143], v[192:195], v[110:113]
	v_mfma_f32_16x16x32_bf16 v[102:105], v[158:161], v[192:195], v[102:105]
	v_mfma_f32_16x16x32_bf16 v[94:97], v[140:143], v[208:211], v[94:97]
	v_mfma_f32_16x16x32_bf16 v[86:89], v[158:161], v[208:211], v[86:89]
	v_mfma_f32_16x16x32_bf16 v[78:81], v[140:143], v[216:219], v[78:81]
	v_mfma_f32_16x16x32_bf16 v[70:73], v[158:161], v[216:219], v[70:73]
	v_mfma_f32_16x16x32_bf16 v[122:125], v[144:147], v[188:191], v[122:125]
	v_mfma_f32_16x16x32_bf16 v[118:121], v[164:167], v[188:191], v[118:121]
	v_mfma_f32_16x16x32_bf16 v[110:113], v[144:147], v[204:207], v[110:113]
	v_mfma_f32_16x16x32_bf16 v[102:105], v[164:167], v[204:207], v[102:105]
	v_mfma_f32_16x16x32_bf16 v[94:97], v[144:147], v[212:215], v[94:97]
	v_mfma_f32_16x16x32_bf16 v[86:89], v[164:167], v[212:215], v[86:89]
	v_mfma_f32_16x16x32_bf16 v[78:81], v[144:147], v[220:223], v[78:81]
	v_mfma_f32_16x16x32_bf16 v[70:73], v[164:167], v[220:223], v[70:73]
	s_setprio 0
	s_setprio 1
	v_mfma_f32_16x16x32_bf16 v[126:129], v[168:171], v[184:187], v[126:129]
	v_mfma_f32_16x16x32_bf16 v[114:117], v[176:179], v[184:187], v[114:117]
	v_mfma_f32_16x16x32_bf16 v[106:109], v[168:171], v[192:195], v[106:109]
	v_mfma_f32_16x16x32_bf16 v[98:101], v[176:179], v[192:195], v[98:101]
	v_mfma_f32_16x16x32_bf16 v[90:93], v[168:171], v[208:211], v[90:93]
	v_mfma_f32_16x16x32_bf16 v[82:85], v[176:179], v[208:211], v[82:85]
	v_mfma_f32_16x16x32_bf16 v[74:77], v[168:171], v[216:219], v[74:77]
	v_mfma_f32_16x16x32_bf16 v[66:69], v[176:179], v[216:219], v[66:69]
	v_mfma_f32_16x16x32_bf16 v[126:129], v[172:175], v[188:191], v[126:129]
	v_mfma_f32_16x16x32_bf16 v[114:117], v[180:183], v[188:191], v[114:117]
	v_mfma_f32_16x16x32_bf16 v[106:109], v[172:175], v[204:207], v[106:109]
	v_mfma_f32_16x16x32_bf16 v[98:101], v[180:183], v[204:207], v[98:101]
	v_mfma_f32_16x16x32_bf16 v[90:93], v[172:175], v[212:215], v[90:93]
	v_mfma_f32_16x16x32_bf16 v[82:85], v[180:183], v[212:215], v[82:85]
	v_mfma_f32_16x16x32_bf16 v[74:77], v[172:175], v[220:223], v[74:77]
	v_mfma_f32_16x16x32_bf16 v[66:69], v[180:183], v[220:223], v[66:69]
	s_setprio 0
	s_barrier
	ds_read_b128 v[184:187], v156 offset:16384
	ds_read_b128 v[188:191], v156 offset:17408
	ds_read_b128 v[192:195], v156 offset:18432
	ds_read_b128 v[204:207], v156 offset:19456
	ds_read_b128 v[208:211], v156 offset:20480
	ds_read_b128 v[212:215], v156 offset:21504
	ds_read_b128 v[216:219], v156 offset:22528
	ds_read_b128 v[220:223], v156 offset:23552
	s_add_i32 s65, s65, s0
	v_lshl_add_u64 v[148:149], s[62:63], 0, v[0:1]
	s_mov_b32 m0, s65
	s_nop 0
	global_load_lds_dwordx4 v[148:149], off
	s_add_i32 m0, s65, 0x2000
	v_lshl_add_u64 v[196:197], s[62:63], 0, v[130:131]
	s_add_u32 s62, s62, s6
	s_addc_u32 s63, s63, s7
	s_add_i32 s61, s61, s0
	global_load_lds_dwordx4 v[196:197], off
	v_lshl_add_u64 v[198:199], s[62:63], 0, v[0:1]
	s_mov_b32 m0, s61
	v_lshl_add_u64 v[200:201], s[62:63], 0, v[130:131]
	global_load_lds_dwordx4 v[198:199], off
	s_add_i32 m0, s61, 0x2000
	v_lshl_add_u64 v[224:225], s[28:29], 0, v[134:135]
	global_load_lds_dwordx4 v[200:201], off
	s_mov_b32 m0, s41
	v_lshl_add_u64 v[226:227], s[28:29], 0, v[132:133]
	global_load_lds_dwordx4 v[224:225], off
	s_mov_b32 m0, s43
	s_nop 0
	global_load_lds_dwordx4 v[226:227], off
	s_waitcnt vmcnt(8)
	s_waitcnt lgkmcnt(0)
	s_barrier
; #define PG8_STAGE(bufoff, gbase, voff) do { _Pragma("unroll") for (int _i = 0; _i < 2; ++_i) \
;         __builtin_amdgcn_global_load_lds((const unsigned*)((const char*)(gbase) + (voff)[_i]), (PG8_LAS unsigned*)(lds + (bufoff) + ldsw + _i * 8192), 16, 0, 0); } while (0)
; #define PG8_WAIT_V(n) asm volatile("s_waitcnt vmcnt(" #n ")" ::: "memory")
; #define PG8_WAIT_L(n) asm volatile("s_waitcnt lgkmcnt(" #n ")" ::: "memory")
; #define PG8_BAR __builtin_amdgcn_s_barrier()
; #define PG8_SCHED __builtin_amdgcn_sched_barrier(0)
; template <class Epi, class Sched, bool ALIGN_EPI = false, bool SP2 = false, bool F8 = false>
; __device__ __forceinline__ void gemm_phase(PG8_LAS unsigned char* lds, const Gemm g, const Sched& S, const Epi& E, const int tidb  ) {
;     ...
;             PG8_WAIT_V(8); PG8_WAIT_L(0); PG8_BAR; PG8_MMA(1, 0, At, B0); PG8_MMA(1, 1, At, B1); PG8_BAR; PG8_SCHED;
;             PG8_LDB(B0, 1, 0); PG8_LDB(B1, 1, 1); PG8_SCHED; PG8_LDA(At, 1, 0); PG8_STAGE(PG8_SA(0, 1), a2 + hstep, voffA);
;             PG8_WAIT_V(8); PG8_WAIT_L(0); PG8_BAR; PG8_MMA(0, 0, At, B0); PG8_MMA(0, 1, At, B1); PG8_BAR; PG8_SCHED;
	s_setprio 1
	s_waitcnt lgkmcnt(0)
	v_mfma_f32_16x16x32_bf16 v[62:65], v[140:143], v[184:187], v[62:65]
	v_mfma_f32_16x16x32_bf16 v[54:57], v[158:161], v[184:187], v[54:57]
	v_mfma_f32_16x16x32_bf16 v[46:49], v[140:143], v[192:195], v[46:49]
	v_mfma_f32_16x16x32_bf16 v[38:41], v[158:161], v[192:195], v[38:41]
	v_mfma_f32_16x16x32_bf16 v[30:33], v[140:143], v[208:211], v[30:33]
	v_mfma_f32_16x16x32_bf16 v[22:25], v[158:161], v[208:211], v[22:25]
	v_mfma_f32_16x16x32_bf16 v[14:17], v[140:143], v[216:219], v[14:17]
	v_mfma_f32_16x16x32_bf16 v[6:9], v[158:161], v[216:219], v[6:9]
	v_mfma_f32_16x16x32_bf16 v[62:65], v[144:147], v[188:191], v[62:65]
	v_mfma_f32_16x16x32_bf16 v[54:57], v[164:167], v[188:191], v[54:57]
	v_mfma_f32_16x16x32_bf16 v[46:49], v[144:147], v[204:207], v[46:49]
	v_mfma_f32_16x16x32_bf16 v[38:41], v[164:167], v[204:207], v[38:41]
	v_mfma_f32_16x16x32_bf16 v[30:33], v[144:147], v[212:215], v[30:33]
	v_mfma_f32_16x16x32_bf16 v[22:25], v[164:167], v[212:215], v[22:25]
	v_mfma_f32_16x16x32_bf16 v[14:17], v[144:147], v[220:223], v[14:17]
	v_mfma_f32_16x16x32_bf16 v[6:9], v[164:167], v[220:223], v[6:9]
	s_setprio 0
	s_setprio 1
	v_mfma_f32_16x16x32_bf16 v[58:61], v[168:171], v[184:187], v[58:61]
	v_mfma_f32_16x16x32_bf16 v[50:53], v[176:179], v[184:187], v[50:53]
	v_mfma_f32_16x16x32_bf16 v[42:45], v[168:171], v[192:195], v[42:45]
	v_mfma_f32_16x16x32_bf16 v[34:37], v[176:179], v[192:195], v[34:37]
	v_mfma_f32_16x16x32_bf16 v[26:29], v[168:171], v[208:211], v[26:29]
	v_mfma_f32_16x16x32_bf16 v[18:21], v[176:179], v[208:211], v[18:21]
	v_mfma_f32_16x16x32_bf16 v[10:13], v[168:171], v[216:219], v[10:13]
	v_mfma_f32_16x16x32_bf16 v[2:5], v[176:179], v[216:219], v[2:5]
	v_mfma_f32_16x16x32_bf16 v[58:61], v[172:175], v[188:191], v[58:61]
	v_mfma_f32_16x16x32_bf16 v[50:53], v[180:183], v[188:191], v[50:53]
	v_mfma_f32_16x16x32_bf16 v[42:45], v[172:175], v[204:207], v[42:45]
	v_mfma_f32_16x16x32_bf16 v[34:37], v[180:183], v[204:207], v[34:37]
	v_mfma_f32_16x16x32_bf16 v[26:29], v[172:175], v[212:215], v[26:29]
	v_mfma_f32_16x16x32_bf16 v[18:21], v[180:183], v[212:215], v[18:21]
	v_mfma_f32_16x16x32_bf16 v[10:13], v[172:175], v[220:223], v[10:13]
	v_mfma_f32_16x16x32_bf16 v[2:5], v[180:183], v[220:223], v[2:5]
	s_setprio 0
	s_barrier
	s_add_i32 s61, 0, 0x18000
	v_add_u32_e32 v157, s61, v151
	s_add_i32 s62, 0, 0x1c000
	ds_read_b128 v[140:143], v157
	ds_read_b128 v[144:147], v157 offset:1024
	ds_read_b128 v[158:161], v157 offset:2048
	ds_read_b128 v[164:167], v157 offset:3072
	v_add_u32_e32 v157, s62, v151
	ds_read_b128 v[168:171], v157
	ds_read_b128 v[172:175], v157 offset:1024
	ds_read_b128 v[176:179], v157 offset:2048
	ds_read_b128 v[180:183], v157 offset:3072
	s_add_u32 s28, s28, s6
	s_addc_u32 s29, s29, s7
	s_mov_b32 m0, s45
	v_lshl_add_u64 v[228:229], s[28:29], 0, v[134:135]
	ds_read_b128 v[184:187], v156 offset:32768
	ds_read_b128 v[188:191], v156 offset:33792
	ds_read_b128 v[192:195], v156 offset:34816
	ds_read_b128 v[204:207], v156 offset:35840
	ds_read_b128 v[208:211], v156 offset:36864
	ds_read_b128 v[212:215], v156 offset:37888
	ds_read_b128 v[216:219], v156 offset:38912
	ds_read_b128 v[220:223], v156 offset:39936
	global_load_lds_dwordx4 v[228:229], off
	v_lshl_add_u64 v[228:229], s[28:29], 0, v[132:133]
	s_mov_b32 m0, s46
	s_nop 0
	global_load_lds_dwordx4 v[228:229], off
	s_waitcnt vmcnt(8)
	s_waitcnt lgkmcnt(0)
	s_barrier
	s_setprio 1
	s_waitcnt lgkmcnt(0)
	v_mfma_f32_16x16x32_bf16 v[122:125], v[140:143], v[184:187], v[122:125]
	v_mfma_f32_16x16x32_bf16 v[118:121], v[158:161], v[184:187], v[118:121]
	v_mfma_f32_16x16x32_bf16 v[110:113], v[140:143], v[192:195], v[110:113]
	v_mfma_f32_16x16x32_bf16 v[102:105], v[158:161], v[192:195], v[102:105]
	v_mfma_f32_16x16x32_bf16 v[94:97], v[140:143], v[208:211], v[94:97]
	v_mfma_f32_16x16x32_bf16 v[86:89], v[158:161], v[208:211], v[86:89]
	v_mfma_f32_16x16x32_bf16 v[78:81], v[140:143], v[216:219], v[78:81]
	v_mfma_f32_16x16x32_bf16 v[70:73], v[158:161], v[216:219], v[70:73]
	v_mfma_f32_16x16x32_bf16 v[122:125], v[144:147], v[188:191], v[122:125]
	v_mfma_f32_16x16x32_bf16 v[118:121], v[164:167], v[188:191], v[118:121]
	v_mfma_f32_16x16x32_bf16 v[110:113], v[144:147], v[204:207], v[110:113]
	v_mfma_f32_16x16x32_bf16 v[102:105], v[164:167], v[204:207], v[102:105]
	v_mfma_f32_16x16x32_bf16 v[94:97], v[144:147], v[212:215], v[94:97]
	v_mfma_f32_16x16x32_bf16 v[86:89], v[164:167], v[212:215], v[86:89]
	v_mfma_f32_16x16x32_bf16 v[78:81], v[144:147], v[220:223], v[78:81]
	v_mfma_f32_16x16x32_bf16 v[70:73], v[164:167], v[220:223], v[70:73]
	s_setprio 0
	s_setprio 1
	v_mfma_f32_16x16x32_bf16 v[126:129], v[168:171], v[184:187], v[126:129]
	v_mfma_f32_16x16x32_bf16 v[114:117], v[176:179], v[184:187], v[114:117]
	v_mfma_f32_16x16x32_bf16 v[106:109], v[168:171], v[192:195], v[106:109]
	v_mfma_f32_16x16x32_bf16 v[98:101], v[176:179], v[192:195], v[98:101]
	v_mfma_f32_16x16x32_bf16 v[90:93], v[168:171], v[208:211], v[90:93]
	v_mfma_f32_16x16x32_bf16 v[82:85], v[176:179], v[208:211], v[82:85]
	v_mfma_f32_16x16x32_bf16 v[74:77], v[168:171], v[216:219], v[74:77]
	v_mfma_f32_16x16x32_bf16 v[66:69], v[176:179], v[216:219], v[66:69]
	v_mfma_f32_16x16x32_bf16 v[126:129], v[172:175], v[188:191], v[126:129]
	v_mfma_f32_16x16x32_bf16 v[114:117], v[180:183], v[188:191], v[114:117]
	v_mfma_f32_16x16x32_bf16 v[106:109], v[172:175], v[204:207], v[106:109]
	v_mfma_f32_16x16x32_bf16 v[98:101], v[180:183], v[204:207], v[98:101]
	v_mfma_f32_16x16x32_bf16 v[90:93], v[172:175], v[212:215], v[90:93]
	v_mfma_f32_16x16x32_bf16 v[82:85], v[180:183], v[212:215], v[82:85]
	v_mfma_f32_16x16x32_bf16 v[74:77], v[172:175], v[220:223], v[74:77]
	v_mfma_f32_16x16x32_bf16 v[66:69], v[180:183], v[220:223], v[66:69]
	s_setprio 0
	s_barrier
; #define PG8_STAGE(bufoff, gbase, voff) do { _Pragma("unroll") for (int _i = 0; _i < 2; ++_i) \
;         __builtin_amdgcn_global_load_lds((const unsigned*)((const char*)(gbase) + (voff)[_i]), (PG8_LAS unsigned*)(lds + (bufoff) + ldsw + _i * 8192), 16, 0, 0); } while (0)
; #define PG8_WAIT_V(n) asm volatile("s_waitcnt vmcnt(" #n ")" ::: "memory")
; #define PG8_WAIT_L(n) asm volatile("s_waitcnt lgkmcnt(" #n ")" ::: "memory")
; #define PG8_BAR __builtin_amdgcn_s_barrier()
; #define PG8_SCHED __builtin_amdgcn_sched_barrier(0)
; template <class Epi, class Sched, bool ALIGN_EPI = false, bool SP2 = false, bool F8 = false>
; __device__ __forceinline__ void gemm_phase(PG8_LAS unsigned char* lds, const Gemm g, const Sched& S, const Epi& E, const int tidb  ) {
;     ...
;         for (int t = 0; t < nt; t += 2) {
;             const bool last = (t == nt - 2);
;             if constexpr (Epi::PREFETCH) { if (t == 0) E.prefetch(cur, wid, lane); }
;             const char* a1 = cA + (size_t)(t + 1) * kstep;
;             const char* a2 = last ? nA : cA + (size_t)(t + 2) * kstep; const char* b2 = last ? nB : cB + (size_t)(t + 2) * kstep;
;     ...
;             PG8_LDA(At, 1, 1); PG8_STAGE(PG8_SB(1, 0), b3, voffB); PG8_STAGE(PG8_SB(1, 1), b3 + hstep, voffB); PG8_STAGE(PG8_SA(1, 0), a3, voffA);
;             PG8_WAIT_V(8); PG8_WAIT_L(0); PG8_BAR; PG8_MMA(1, 0, At, B0); PG8_MMA(1, 1, At, B1); PG8_BAR; PG8_SCHED;
	ds_read_b128 v[184:187], v156 offset:49152
	ds_read_b128 v[188:191], v156 offset:50176
	ds_read_b128 v[192:195], v156 offset:51200
	ds_read_b128 v[204:207], v156 offset:52224
	ds_read_b128 v[208:211], v156 offset:53248
	ds_read_b128 v[212:215], v156 offset:54272
	ds_read_b128 v[216:219], v156 offset:55296
	ds_read_b128 v[220:223], v156 offset:56320
	s_add_i32 s28, s61, s0
	v_lshl_add_u64 v[148:149], v[148:149], 0, s[92:93]
	s_mov_b32 m0, s28
	s_nop 0
	global_load_lds_dwordx4 v[148:149], off
	v_lshl_add_u64 v[148:149], v[196:197], 0, s[92:93]
	s_add_i32 m0, s28, 0x2000
	s_add_i32 s28, s62, s0
	global_load_lds_dwordx4 v[148:149], off
	v_lshl_add_u64 v[148:149], v[198:199], 0, s[92:93]
	s_mov_b32 m0, s28
	s_nop 0
	global_load_lds_dwordx4 v[148:149], off
	v_lshl_add_u64 v[148:149], v[200:201], 0, s[92:93]
	s_add_i32 m0, s28, 0x2000
	s_nop 0
	global_load_lds_dwordx4 v[148:149], off
	v_lshl_add_u64 v[148:149], v[224:225], 0, s[92:93]
	s_mov_b32 m0, s47
	s_nop 0
	global_load_lds_dwordx4 v[148:149], off
	v_lshl_add_u64 v[148:149], v[226:227], 0, s[92:93]
	s_mov_b32 m0, s48
	s_nop 0
	global_load_lds_dwordx4 v[148:149], off
	s_waitcnt vmcnt(8)
	s_waitcnt lgkmcnt(0)
	s_barrier
	s_setprio 1
	s_waitcnt lgkmcnt(0)
	v_mfma_f32_16x16x32_bf16 v[62:65], v[140:143], v[184:187], v[62:65]
	v_mfma_f32_16x16x32_bf16 v[54:57], v[158:161], v[184:187], v[54:57]
	v_mfma_f32_16x16x32_bf16 v[46:49], v[140:143], v[192:195], v[46:49]
	v_mfma_f32_16x16x32_bf16 v[38:41], v[158:161], v[192:195], v[38:41]
	v_mfma_f32_16x16x32_bf16 v[30:33], v[140:143], v[208:211], v[30:33]
	v_mfma_f32_16x16x32_bf16 v[22:25], v[158:161], v[208:211], v[22:25]
	v_mfma_f32_16x16x32_bf16 v[14:17], v[140:143], v[216:219], v[14:17]
	v_mfma_f32_16x16x32_bf16 v[6:9], v[158:161], v[216:219], v[6:9]
	v_mfma_f32_16x16x32_bf16 v[62:65], v[144:147], v[188:191], v[62:65]
	v_mfma_f32_16x16x32_bf16 v[54:57], v[164:167], v[188:191], v[54:57]
	v_mfma_f32_16x16x32_bf16 v[46:49], v[144:147], v[204:207], v[46:49]
	v_mfma_f32_16x16x32_bf16 v[38:41], v[164:167], v[204:207], v[38:41]
	v_mfma_f32_16x16x32_bf16 v[30:33], v[144:147], v[212:215], v[30:33]
	v_mfma_f32_16x16x32_bf16 v[22:25], v[164:167], v[212:215], v[22:25]
	v_mfma_f32_16x16x32_bf16 v[14:17], v[144:147], v[220:223], v[14:17]
	v_mfma_f32_16x16x32_bf16 v[6:9], v[164:167], v[220:223], v[6:9]
	s_setprio 0
	s_setprio 1
	v_mfma_f32_16x16x32_bf16 v[58:61], v[168:171], v[184:187], v[58:61]
	v_mfma_f32_16x16x32_bf16 v[50:53], v[176:179], v[184:187], v[50:53]
	v_mfma_f32_16x16x32_bf16 v[42:45], v[168:171], v[192:195], v[42:45]
	v_mfma_f32_16x16x32_bf16 v[34:37], v[176:179], v[192:195], v[34:37]
	v_mfma_f32_16x16x32_bf16 v[26:29], v[168:171], v[208:211], v[26:29]
	v_mfma_f32_16x16x32_bf16 v[18:21], v[176:179], v[208:211], v[18:21]
	v_mfma_f32_16x16x32_bf16 v[10:13], v[168:171], v[216:219], v[10:13]
	v_mfma_f32_16x16x32_bf16 v[2:5], v[176:179], v[216:219], v[2:5]
	v_mfma_f32_16x16x32_bf16 v[58:61], v[172:175], v[188:191], v[58:61]
	v_mfma_f32_16x16x32_bf16 v[50:53], v[180:183], v[188:191], v[50:53]
	v_mfma_f32_16x16x32_bf16 v[42:45], v[172:175], v[204:207], v[42:45]
	v_mfma_f32_16x16x32_bf16 v[34:37], v[180:183], v[204:207], v[34:37]
	s_add_u32 s26, s26, 0x100
	s_addc_u32 s27, s27, 0
	s_add_u32 s58, s58, 0x100
	s_addc_u32 s59, s59, 0
	s_cmp_ge_i32 s60, s49
	s_mov_b32 s28, s60
	v_mfma_f32_16x16x32_bf16 v[26:29], v[172:175], v[212:215], v[26:29]
	v_mfma_f32_16x16x32_bf16 v[18:21], v[180:183], v[212:215], v[18:21]
	v_mfma_f32_16x16x32_bf16 v[10:13], v[172:175], v[220:223], v[10:13]
	v_mfma_f32_16x16x32_bf16 v[2:5], v[180:183], v[220:223], v[2:5]
	s_setprio 0
	s_barrier
	s_cbranch_scc0 .LBB0_1705

; #define PG8_STAGE(bufoff, gbase, voff) do { _Pragma("unroll") for (int _i = 0; _i < 2; ++_i) \
;         __builtin_amdgcn_global_load_lds((const unsigned*)((const char*)(gbase) + (voff)[_i]), (PG8_LAS unsigned*)(lds + (bufoff) + ldsw + _i * 8192), 16, 0, 0); } while (0)
; #define PG8_WAIT_V(n) asm volatile("s_waitcnt vmcnt(" #n ")" ::: "memory")
; #define PG8_WAIT_L(n) asm volatile("s_waitcnt lgkmcnt(" #n ")" ::: "memory")
; #define PG8_BAR __builtin_amdgcn_s_barrier()
; #define PG8_SCHED __builtin_amdgcn_sched_barrier(0)
; template <class Epi, class Sched, bool ALIGN_EPI = false, bool SP2 = false, bool F8 = false>
; __device__ __forceinline__ void gemm_phase(PG8_LAS unsigned char* lds, const Gemm g, const Sched& S, const Epi& E, const int tidb  ) {
;     ...
;             const char* a1 = cA + (size_t)(t + 1) * kstep;
;             const char* a2 = last ? nA : cA + (size_t)(t + 2) * kstep; const char* b2 = last ? nB : cB + (size_t)(t + 2) * kstep;
;             const char* a3 = a2 + kstep; const char* b3 = b2 + kstep;
;             if (last && has_next) S.a_ready(nxt);
;             if constexpr (SP2) {
;             PG8_LDB(B0, 0, 0); PG8_LDB(B1, 0, 1); PG8_SCHED; PG8_LDA(At, 0, 0); PG8_STAGE(PG8_SA(1, 1), a1 + hstep, voffA);
;             PG8_WAIT_V(8); PG8_WAIT_L(0); PG8_BAR; PG8_MMA(0, 0, At, B0); PG8_MMA(0, 1, At, B1); PG8_BAR; PG8_SCHED;
;             PG8_LDA(At, 0, 1); PG8_STAGE(PG8_SB(0, 0), b2, voffB); PG8_STAGE(PG8_SB(0, 1), b2 + hstep, voffB); PG8_STAGE(PG8_SA(0, 0), a2, voffA);
;             PG8_WAIT_V(8); PG8_WAIT_L(0); PG8_BAR; PG8_MMA(1, 0, At, B0); PG8_MMA(1, 1, At, B1); PG8_BAR; PG8_SCHED;
.LBB0_1728:
	s_add_i32 s61, 0, 0x10000
	v_add_u32_e32 v2, s61, v186
	ds_read_b128 v[18:21], v2
	ds_read_b128 v[22:25], v2 offset:1024
	ds_read_b128 v[26:29], v2 offset:2048
	ds_read_b128 v[30:33], v2 offset:3072
	s_add_i32 s60, s26, 2
	s_add_u32 s28, s24, 0x80
	s_addc_u32 s27, s25, 0
	s_cmp_eq_u32 s51, s26
	s_cselect_b32 s27, s5, s27
	s_cselect_b32 s26, s4, s28
	s_cselect_b32 s29, s23, s59
	s_cselect_b32 s28, s22, s58
	s_add_i32 s62, 0, 0x14000
	v_add_u32_e32 v14, s62, v186
	ds_read_b128 v[2:5], v14
	ds_read_b128 v[6:9], v14 offset:1024
	ds_read_b128 v[10:13], v14 offset:2048
	ds_read_b128 v[14:17], v14 offset:3072
	v_lshl_add_u64 v[182:183], s[24:25], 0, v[170:171]
	s_add_i32 m0, s41, 0xc000
	ds_read_b128 v[174:177], v191
	ds_read_b128 v[178:181], v191 offset:1024
	ds_read_b128 v[204:207], v191 offset:2048
	ds_read_b128 v[208:211], v191 offset:3072
	ds_read_b128 v[212:215], v191 offset:4096
	ds_read_b128 v[216:219], v191 offset:5120
	ds_read_b128 v[220:223], v191 offset:6144
	ds_read_b128 v[224:227], v191 offset:7168
	global_load_lds_dwordx4 v[182:183], off
	v_lshl_add_u64 v[182:183], s[24:25], 0, v[172:173]
	s_add_i32 m0, s41, 0xe000
	s_nop 0
	global_load_lds_dwordx4 v[182:183], off
	s_waitcnt vmcnt(8)
	s_waitcnt lgkmcnt(0)
	s_barrier
	s_setprio 1
	s_waitcnt lgkmcnt(0)
	v_mfma_scale_f32_16x16x128_f8f6f4 v[154:157], v[18:25], v[174:181], v[154:157], v246, v247 op_sel_hi:[0,0,0]
	v_mfma_scale_f32_16x16x128_f8f6f4 v[150:153], v[26:33], v[174:181], v[150:153], v246, v247 op_sel_hi:[0,0,0]
	v_mfma_scale_f32_16x16x128_f8f6f4 v[142:145], v[18:25], v[204:211], v[142:145], v246, v247 op_sel_hi:[0,0,0]
	v_mfma_scale_f32_16x16x128_f8f6f4 v[134:137], v[26:33], v[204:211], v[134:137], v246, v247 op_sel_hi:[0,0,0]
	v_mfma_scale_f32_16x16x128_f8f6f4 v[126:129], v[18:25], v[212:219], v[126:129], v246, v247 op_sel_hi:[0,0,0]
	v_mfma_scale_f32_16x16x128_f8f6f4 v[118:121], v[26:33], v[212:219], v[118:121], v246, v247 op_sel_hi:[0,0,0]
	v_mfma_scale_f32_16x16x128_f8f6f4 v[110:113], v[18:25], v[220:227], v[110:113], v246, v247 op_sel_hi:[0,0,0]
	v_mfma_scale_f32_16x16x128_f8f6f4 v[102:105], v[26:33], v[220:227], v[102:105], v246, v247 op_sel_hi:[0,0,0]
	s_setprio 0
	s_setprio 1
	v_mfma_scale_f32_16x16x128_f8f6f4 v[158:161], v[2:9], v[174:181], v[158:161], v246, v247 op_sel_hi:[0,0,0]
	v_mfma_scale_f32_16x16x128_f8f6f4 v[146:149], v[10:17], v[174:181], v[146:149], v246, v247 op_sel_hi:[0,0,0]
	v_mfma_scale_f32_16x16x128_f8f6f4 v[138:141], v[2:9], v[204:211], v[138:141], v246, v247 op_sel_hi:[0,0,0]
	v_mfma_scale_f32_16x16x128_f8f6f4 v[130:133], v[10:17], v[204:211], v[130:133], v246, v247 op_sel_hi:[0,0,0]
	v_mfma_scale_f32_16x16x128_f8f6f4 v[122:125], v[2:9], v[212:219], v[122:125], v246, v247 op_sel_hi:[0,0,0]
	v_mfma_scale_f32_16x16x128_f8f6f4 v[114:117], v[10:17], v[212:219], v[114:117], v246, v247 op_sel_hi:[0,0,0]
	v_mfma_scale_f32_16x16x128_f8f6f4 v[106:109], v[2:9], v[220:227], v[106:109], v246, v247 op_sel_hi:[0,0,0]
	v_mfma_scale_f32_16x16x128_f8f6f4 v[98:101], v[10:17], v[220:227], v[98:101], v246, v247 op_sel_hi:[0,0,0]
	s_setprio 0
	s_barrier
	ds_read_b128 v[204:207], v191 offset:16384
	ds_read_b128 v[208:211], v191 offset:17408
	ds_read_b128 v[212:215], v191 offset:18432
	ds_read_b128 v[216:219], v191 offset:19456
	ds_read_b128 v[220:223], v191 offset:20480
	ds_read_b128 v[224:227], v191 offset:21504
	ds_read_b128 v[228:231], v191 offset:22528
	ds_read_b128 v[232:235], v191 offset:23552
	s_add_i32 s61, s61, s36
	v_lshl_add_u64 v[174:175], s[28:29], 0, v[0:1]
	s_mov_b32 m0, s61
	s_nop 0
	global_load_lds_dwordx4 v[174:175], off
	s_add_i32 m0, s61, 0x2000
	v_lshl_add_u64 v[176:177], s[28:29], 0, v[164:165]
	s_add_u32 s28, s28, s6
	s_addc_u32 s29, s29, s7
	s_add_i32 s61, s62, s36
	global_load_lds_dwordx4 v[176:177], off
	v_lshl_add_u64 v[178:179], s[28:29], 0, v[0:1]
	s_mov_b32 m0, s61
	v_lshl_add_u64 v[180:181], s[28:29], 0, v[164:165]
	global_load_lds_dwordx4 v[178:179], off
	s_add_i32 m0, s61, 0x2000
	v_lshl_add_u64 v[182:183], s[26:27], 0, v[168:169]
	global_load_lds_dwordx4 v[180:181], off
	s_mov_b32 m0, s41
	v_lshl_add_u64 v[184:185], s[26:27], 0, v[166:167]
	global_load_lds_dwordx4 v[182:183], off
	s_mov_b32 m0, s43
	s_nop 0
	global_load_lds_dwordx4 v[184:185], off
	s_waitcnt vmcnt(8)
	s_waitcnt lgkmcnt(0)
	s_barrier
	s_setprio 1
	s_waitcnt lgkmcnt(0)
	v_mfma_scale_f32_16x16x128_f8f6f4 v[94:97], v[18:25], v[204:211], v[94:97], v246, v247 op_sel_hi:[0,0,0]
	v_mfma_scale_f32_16x16x128_f8f6f4 v[86:89], v[26:33], v[204:211], v[86:89], v246, v247 op_sel_hi:[0,0,0]
	v_mfma_scale_f32_16x16x128_f8f6f4 v[78:81], v[18:25], v[212:219], v[78:81], v246, v247 op_sel_hi:[0,0,0]
	v_mfma_scale_f32_16x16x128_f8f6f4 v[70:73], v[26:33], v[212:219], v[70:73], v246, v247 op_sel_hi:[0,0,0]
	v_mfma_scale_f32_16x16x128_f8f6f4 v[62:65], v[18:25], v[220:227], v[62:65], v246, v247 op_sel_hi:[0,0,0]
	v_mfma_scale_f32_16x16x128_f8f6f4 v[54:57], v[26:33], v[220:227], v[54:57], v246, v247 op_sel_hi:[0,0,0]
	v_mfma_scale_f32_16x16x128_f8f6f4 v[46:49], v[18:25], v[228:235], v[46:49], v246, v247 op_sel_hi:[0,0,0]
	v_mfma_scale_f32_16x16x128_f8f6f4 v[38:41], v[26:33], v[228:235], v[38:41], v246, v247 op_sel_hi:[0,0,0]
	s_setprio 0
	s_setprio 1
	v_mfma_scale_f32_16x16x128_f8f6f4 v[90:93], v[2:9], v[204:211], v[90:93], v246, v247 op_sel_hi:[0,0,0]
	v_mfma_scale_f32_16x16x128_f8f6f4 v[82:85], v[10:17], v[204:211], v[82:85], v246, v247 op_sel_hi:[0,0,0]
	v_mfma_scale_f32_16x16x128_f8f6f4 v[74:77], v[2:9], v[212:219], v[74:77], v246, v247 op_sel_hi:[0,0,0]
	v_mfma_scale_f32_16x16x128_f8f6f4 v[66:69], v[10:17], v[212:219], v[66:69], v246, v247 op_sel_hi:[0,0,0]
	v_mfma_scale_f32_16x16x128_f8f6f4 v[58:61], v[2:9], v[220:227], v[58:61], v246, v247 op_sel_hi:[0,0,0]
	v_mfma_scale_f32_16x16x128_f8f6f4 v[50:53], v[10:17], v[220:227], v[50:53], v246, v247 op_sel_hi:[0,0,0]
	v_mfma_scale_f32_16x16x128_f8f6f4 v[42:45], v[2:9], v[228:235], v[42:45], v246, v247 op_sel_hi:[0,0,0]
	v_mfma_scale_f32_16x16x128_f8f6f4 v[34:37], v[10:17], v[228:235], v[34:37], v246, v247 op_sel_hi:[0,0,0]
	s_setprio 0
	s_barrier
; #define PG8_STAGE(bufoff, gbase, voff) do { _Pragma("unroll") for (int _i = 0; _i < 2; ++_i) \
;         __builtin_amdgcn_global_load_lds((const unsigned*)((const char*)(gbase) + (voff)[_i]), (PG8_LAS unsigned*)(lds + (bufoff) + ldsw + _i * 8192), 16, 0, 0); } while (0)
; #define PG8_WAIT_V(n) asm volatile("s_waitcnt vmcnt(" #n ")" ::: "memory")
; #define PG8_WAIT_L(n) asm volatile("s_waitcnt lgkmcnt(" #n ")" ::: "memory")
; #define PG8_BAR __builtin_amdgcn_s_barrier()
; #define PG8_SCHED __builtin_amdgcn_sched_barrier(0)
; template <class Epi, class Sched, bool ALIGN_EPI = false, bool SP2 = false, bool F8 = false>
; __device__ __forceinline__ void gemm_phase(PG8_LAS unsigned char* lds, const Gemm g, const Sched& S, const Epi& E, const int tidb  ) {
;     ...
;             PG8_LDB(B0, 1, 0); PG8_LDB(B1, 1, 1); PG8_SCHED; PG8_LDA(At, 1, 0); PG8_STAGE(PG8_SA(0, 1), a2 + hstep, voffA);
;             PG8_WAIT_V(8); PG8_WAIT_L(0); PG8_BAR; PG8_MMA(0, 0, At, B0); PG8_MMA(0, 1, At, B1); PG8_BAR; PG8_SCHED;
;             PG8_LDA(At, 1, 1); PG8_STAGE(PG8_SB(1, 0), b3, voffB); PG8_STAGE(PG8_SB(1, 1), b3 + hstep, voffB); PG8_STAGE(PG8_SA(1, 0), a3, voffA);
;             PG8_WAIT_V(8); PG8_WAIT_L(0); PG8_BAR; PG8_MMA(1, 0, At, B0); PG8_MMA(1, 1, At, B1); PG8_BAR; PG8_SCHED;
	s_add_i32 s28, 0, 0x18000
	s_add_i32 s29, 0, 0x1c000
	v_add_u32_e32 v14, s28, v186
	v_add_u32_e32 v30, s29, v186
	ds_read_b128 v[2:5], v14
	ds_read_b128 v[6:9], v14 offset:1024
	ds_read_b128 v[10:13], v14 offset:2048
	ds_read_b128 v[14:17], v14 offset:3072
	ds_read_b128 v[18:21], v30
	ds_read_b128 v[22:25], v30 offset:1024
	ds_read_b128 v[26:29], v30 offset:2048
	ds_read_b128 v[30:33], v30 offset:3072
	s_add_u32 s26, s26, s6
	s_addc_u32 s27, s27, s7
	s_mov_b32 m0, s45
	v_lshl_add_u64 v[192:193], s[26:27], 0, v[168:169]
	ds_read_b128 v[204:207], v191 offset:32768
	ds_read_b128 v[208:211], v191 offset:33792
	ds_read_b128 v[212:215], v191 offset:34816
	ds_read_b128 v[216:219], v191 offset:35840
	ds_read_b128 v[220:223], v191 offset:36864
	ds_read_b128 v[224:227], v191 offset:37888
	ds_read_b128 v[228:231], v191 offset:38912
	ds_read_b128 v[232:235], v191 offset:39936
	global_load_lds_dwordx4 v[192:193], off
	v_lshl_add_u64 v[192:193], s[26:27], 0, v[166:167]
	s_mov_b32 m0, s46
	s_nop 0
	global_load_lds_dwordx4 v[192:193], off
	s_waitcnt vmcnt(8)
	s_waitcnt lgkmcnt(0)
	s_barrier
	s_setprio 1
	s_waitcnt lgkmcnt(0)
	v_mfma_scale_f32_16x16x128_f8f6f4 v[154:157], v[2:9], v[204:211], v[154:157], v246, v247 op_sel_hi:[0,0,0]
	v_mfma_scale_f32_16x16x128_f8f6f4 v[150:153], v[10:17], v[204:211], v[150:153], v246, v247 op_sel_hi:[0,0,0]
	v_mfma_scale_f32_16x16x128_f8f6f4 v[142:145], v[2:9], v[212:219], v[142:145], v246, v247 op_sel_hi:[0,0,0]
	v_mfma_scale_f32_16x16x128_f8f6f4 v[134:137], v[10:17], v[212:219], v[134:137], v246, v247 op_sel_hi:[0,0,0]
	v_mfma_scale_f32_16x16x128_f8f6f4 v[126:129], v[2:9], v[220:227], v[126:129], v246, v247 op_sel_hi:[0,0,0]
	v_mfma_scale_f32_16x16x128_f8f6f4 v[118:121], v[10:17], v[220:227], v[118:121], v246, v247 op_sel_hi:[0,0,0]
	v_mfma_scale_f32_16x16x128_f8f6f4 v[110:113], v[2:9], v[228:235], v[110:113], v246, v247 op_sel_hi:[0,0,0]
	v_mfma_scale_f32_16x16x128_f8f6f4 v[102:105], v[10:17], v[228:235], v[102:105], v246, v247 op_sel_hi:[0,0,0]
	s_setprio 0
	s_setprio 1
	v_mfma_scale_f32_16x16x128_f8f6f4 v[158:161], v[18:25], v[204:211], v[158:161], v246, v247 op_sel_hi:[0,0,0]
	v_mfma_scale_f32_16x16x128_f8f6f4 v[146:149], v[26:33], v[204:211], v[146:149], v246, v247 op_sel_hi:[0,0,0]
	v_mfma_scale_f32_16x16x128_f8f6f4 v[138:141], v[18:25], v[212:219], v[138:141], v246, v247 op_sel_hi:[0,0,0]
	v_mfma_scale_f32_16x16x128_f8f6f4 v[130:133], v[26:33], v[212:219], v[130:133], v246, v247 op_sel_hi:[0,0,0]
	v_mfma_scale_f32_16x16x128_f8f6f4 v[122:125], v[18:25], v[220:227], v[122:125], v246, v247 op_sel_hi:[0,0,0]
	v_mfma_scale_f32_16x16x128_f8f6f4 v[114:117], v[26:33], v[220:227], v[114:117], v246, v247 op_sel_hi:[0,0,0]
	v_mfma_scale_f32_16x16x128_f8f6f4 v[106:109], v[18:25], v[228:235], v[106:109], v246, v247 op_sel_hi:[0,0,0]
	v_mfma_scale_f32_16x16x128_f8f6f4 v[98:101], v[26:33], v[228:235], v[98:101], v246, v247 op_sel_hi:[0,0,0]
	s_setprio 0
	s_barrier
	ds_read_b128 v[204:207], v191 offset:49152
	ds_read_b128 v[208:211], v191 offset:50176
	ds_read_b128 v[212:215], v191 offset:51200
	ds_read_b128 v[216:219], v191 offset:52224
	ds_read_b128 v[220:223], v191 offset:53248
	ds_read_b128 v[224:227], v191 offset:54272
	ds_read_b128 v[228:231], v191 offset:55296
	ds_read_b128 v[232:235], v191 offset:56320
	s_add_i32 s26, s28, s36
	v_lshl_add_u64 v[174:175], v[174:175], 0, s[92:93]
	s_mov_b32 m0, s26
	s_nop 0
	global_load_lds_dwordx4 v[174:175], off
	v_lshl_add_u64 v[174:175], v[176:177], 0, s[92:93]
	s_add_i32 m0, s26, 0x2000
	s_add_i32 s26, s29, s36
	global_load_lds_dwordx4 v[174:175], off
	v_lshl_add_u64 v[174:175], v[178:179], 0, s[92:93]
	s_mov_b32 m0, s26
	s_nop 0
	global_load_lds_dwordx4 v[174:175], off
	v_lshl_add_u64 v[174:175], v[180:181], 0, s[92:93]
	s_add_i32 m0, s26, 0x2000
	s_nop 0
	global_load_lds_dwordx4 v[174:175], off
	v_lshl_add_u64 v[174:175], v[182:183], 0, s[92:93]
	s_mov_b32 m0, s47
	s_nop 0
	global_load_lds_dwordx4 v[174:175], off
	v_lshl_add_u64 v[174:175], v[184:185], 0, s[92:93]
	s_mov_b32 m0, s48
	s_nop 0
	global_load_lds_dwordx4 v[174:175], off
	s_waitcnt vmcnt(8)
	s_waitcnt lgkmcnt(0)
	s_barrier
	s_setprio 1
	s_waitcnt lgkmcnt(0)
	v_mfma_scale_f32_16x16x128_f8f6f4 v[94:97], v[2:9], v[204:211], v[94:97], v246, v247 op_sel_hi:[0,0,0]
	v_mfma_scale_f32_16x16x128_f8f6f4 v[86:89], v[10:17], v[204:211], v[86:89], v246, v247 op_sel_hi:[0,0,0]
	v_mfma_scale_f32_16x16x128_f8f6f4 v[78:81], v[2:9], v[212:219], v[78:81], v246, v247 op_sel_hi:[0,0,0]
	v_mfma_scale_f32_16x16x128_f8f6f4 v[70:73], v[10:17], v[212:219], v[70:73], v246, v247 op_sel_hi:[0,0,0]
	v_mfma_scale_f32_16x16x128_f8f6f4 v[62:65], v[2:9], v[220:227], v[62:65], v246, v247 op_sel_hi:[0,0,0]
	v_mfma_scale_f32_16x16x128_f8f6f4 v[54:57], v[10:17], v[220:227], v[54:57], v246, v247 op_sel_hi:[0,0,0]
	v_mfma_scale_f32_16x16x128_f8f6f4 v[46:49], v[2:9], v[228:235], v[46:49], v246, v247 op_sel_hi:[0,0,0]
	v_mfma_scale_f32_16x16x128_f8f6f4 v[38:41], v[10:17], v[228:235], v[38:41], v246, v247 op_sel_hi:[0,0,0]
	s_setprio 0
	s_setprio 1
	v_mfma_scale_f32_16x16x128_f8f6f4 v[90:93], v[18:25], v[204:211], v[90:93], v246, v247 op_sel_hi:[0,0,0]
	v_mfma_scale_f32_16x16x128_f8f6f4 v[82:85], v[26:33], v[204:211], v[82:85], v246, v247 op_sel_hi:[0,0,0]
	v_mfma_scale_f32_16x16x128_f8f6f4 v[74:77], v[18:25], v[212:219], v[74:77], v246, v247 op_sel_hi:[0,0,0]
	v_mfma_scale_f32_16x16x128_f8f6f4 v[66:69], v[26:33], v[212:219], v[66:69], v246, v247 op_sel_hi:[0,0,0]
	s_add_u32 s24, s24, 0x100
	s_addc_u32 s25, s25, 0
	s_add_u32 s58, s58, 0x100
	s_addc_u32 s59, s59, 0
	s_cmp_ge_i32 s60, s49
	s_mov_b32 s26, s60
	v_mfma_scale_f32_16x16x128_f8f6f4 v[58:61], v[18:25], v[220:227], v[58:61], v246, v247 op_sel_hi:[0,0,0]
	v_mfma_scale_f32_16x16x128_f8f6f4 v[50:53], v[26:33], v[220:227], v[50:53], v246, v247 op_sel_hi:[0,0,0]
	v_mfma_scale_f32_16x16x128_f8f6f4 v[42:45], v[18:25], v[228:235], v[42:45], v246, v247 op_sel_hi:[0,0,0]
	v_mfma_scale_f32_16x16x128_f8f6f4 v[34:37], v[26:33], v[228:235], v[34:37], v246, v247 op_sel_hi:[0,0,0]
	s_setprio 0
	s_barrier
	s_cbranch_scc0 .LBB0_1728

; #define PG8_STAGE(bufoff, gbase, voff) do { _Pragma("unroll") for (int _i = 0; _i < 2; ++_i) \
;         __builtin_amdgcn_global_load_lds((const unsigned*)((const char*)(gbase) + (voff)[_i]), (PG8_LAS unsigned*)(lds + (bufoff) + ldsw + _i * 8192), 16, 0, 0); } while (0)
; #define PG8_WAIT_V(n) asm volatile("s_waitcnt vmcnt(" #n ")" ::: "memory")
; #define PG8_WAIT_L(n) asm volatile("s_waitcnt lgkmcnt(" #n ")" ::: "memory")
; #define PG8_BAR __builtin_amdgcn_s_barrier()
; #define PG8_SCHED __builtin_amdgcn_sched_barrier(0)
; template <class Epi, class Sched, bool ALIGN_EPI = false, bool SP2 = false, bool F8 = false>
; __device__ __forceinline__ void gemm_phase(PG8_LAS unsigned char* lds, const Gemm g, const Sched& S, const Epi& E, const int tidb  ) {
;     ...
;             const char* a1 = cA + (size_t)(t + 1) * kstep;
;             const char* a2 = last ? nA : cA + (size_t)(t + 2) * kstep; const char* b2 = last ? nB : cB + (size_t)(t + 2) * kstep;
;             const char* a3 = a2 + kstep; const char* b3 = b2 + kstep;
;             if (last && has_next) S.a_ready(nxt);
;             if constexpr (SP2) {
;             PG8_LDB(B0, 0, 0); PG8_LDB(B1, 0, 1); PG8_SCHED; PG8_LDA(At, 0, 0); PG8_STAGE(PG8_SA(1, 1), a1 + hstep, voffA);
;             PG8_WAIT_V(8); PG8_WAIT_L(0); PG8_BAR; PG8_MMA(0, 0, At, B0); PG8_MMA(0, 1, At, B1); PG8_BAR; PG8_SCHED;
;             PG8_LDA(At, 0, 1); PG8_STAGE(PG8_SB(0, 0), b2, voffB); PG8_STAGE(PG8_SB(0, 1), b2 + hstep, voffB); PG8_STAGE(PG8_SA(0, 0), a2, voffA);
;             PG8_WAIT_V(8); PG8_WAIT_L(0); PG8_BAR; PG8_MMA(1, 0, At, B0); PG8_MMA(1, 1, At, B1); PG8_BAR; PG8_SCHED;
.LBB0_1807:
	s_add_i32 s68, 0, 0x10000
	v_add_u32_e32 v142, s68, v192
	ds_read_b128 v[122:125], v142
	ds_read_b128 v[126:129], v142 offset:1024
	ds_read_b128 v[138:141], v142 offset:2048
	ds_read_b128 v[142:145], v142 offset:3072
	s_add_i32 s65, s30, 2
	s_add_u32 s66, s28, 0x80
	s_addc_u32 s31, s29, 0
	s_cmp_eq_u32 s47, s30
	s_cselect_b32 s31, s7, s31
	s_cselect_b32 s30, s6, s66
	s_cselect_b32 s67, s27, s63
	s_cselect_b32 s66, s26, s62
	s_add_i32 s70, 0, 0x14000
	v_add_u32_e32 v170, s70, v192
	ds_read_b128 v[146:149], v170
	ds_read_b128 v[150:153], v170 offset:1024
	ds_read_b128 v[154:157], v170 offset:2048
	ds_read_b128 v[170:173], v170 offset:3072
	v_lshl_add_u64 v[190:191], s[28:29], 0, v[166:167]
	s_add_i32 m0, s1, 0xc000
	ds_read_b128 v[174:177], v194
	ds_read_b128 v[178:181], v194 offset:1024
	ds_read_b128 v[182:185], v194 offset:2048
	ds_read_b128 v[186:189], v194 offset:3072
	ds_read_b128 v[204:207], v194 offset:4096
	ds_read_b128 v[208:211], v194 offset:5120
	ds_read_b128 v[212:215], v194 offset:6144
	ds_read_b128 v[216:219], v194 offset:7168
	global_load_lds_dwordx4 v[190:191], off
	v_lshl_add_u64 v[190:191], s[28:29], 0, v[168:169]
	s_add_i32 m0, s1, 0xe000
	s_nop 0
	global_load_lds_dwordx4 v[190:191], off
	s_waitcnt vmcnt(8)
	s_waitcnt lgkmcnt(0)
	s_barrier
	s_setprio 1
	s_waitcnt lgkmcnt(0)
	v_mfma_f32_16x16x32_bf16 v[134:137], v[122:125], v[174:177], v[134:137]
	v_mfma_f32_16x16x32_bf16 v[130:133], v[138:141], v[174:177], v[130:133]
	v_mfma_f32_16x16x32_bf16 v[110:113], v[122:125], v[182:185], v[110:113]
	v_mfma_f32_16x16x32_bf16 v[106:109], v[138:141], v[182:185], v[106:109]
	v_mfma_f32_16x16x32_bf16 v[94:97], v[122:125], v[204:207], v[94:97]
	v_mfma_f32_16x16x32_bf16 v[90:93], v[138:141], v[204:207], v[90:93]
	v_mfma_f32_16x16x32_bf16 v[78:81], v[122:125], v[212:215], v[78:81]
	v_mfma_f32_16x16x32_bf16 v[74:77], v[138:141], v[212:215], v[74:77]
	v_mfma_f32_16x16x32_bf16 v[134:137], v[126:129], v[178:181], v[134:137]
	v_mfma_f32_16x16x32_bf16 v[130:133], v[142:145], v[178:181], v[130:133]
	v_mfma_f32_16x16x32_bf16 v[110:113], v[126:129], v[186:189], v[110:113]
	v_mfma_f32_16x16x32_bf16 v[106:109], v[142:145], v[186:189], v[106:109]
	v_mfma_f32_16x16x32_bf16 v[94:97], v[126:129], v[208:211], v[94:97]
	v_mfma_f32_16x16x32_bf16 v[90:93], v[142:145], v[208:211], v[90:93]
	v_mfma_f32_16x16x32_bf16 v[78:81], v[126:129], v[216:219], v[78:81]
	v_mfma_f32_16x16x32_bf16 v[74:77], v[142:145], v[216:219], v[74:77]
	s_setprio 0
	s_setprio 1
	v_mfma_f32_16x16x32_bf16 v[118:121], v[146:149], v[174:177], v[118:121]
	v_mfma_f32_16x16x32_bf16 v[114:117], v[154:157], v[174:177], v[114:117]
	v_mfma_f32_16x16x32_bf16 v[102:105], v[146:149], v[182:185], v[102:105]
	v_mfma_f32_16x16x32_bf16 v[98:101], v[154:157], v[182:185], v[98:101]
	v_mfma_f32_16x16x32_bf16 v[86:89], v[146:149], v[204:207], v[86:89]
	v_mfma_f32_16x16x32_bf16 v[82:85], v[154:157], v[204:207], v[82:85]
	v_mfma_f32_16x16x32_bf16 v[70:73], v[146:149], v[212:215], v[70:73]
	v_mfma_f32_16x16x32_bf16 v[66:69], v[154:157], v[212:215], v[66:69]
	v_mfma_f32_16x16x32_bf16 v[118:121], v[150:153], v[178:181], v[118:121]
	v_mfma_f32_16x16x32_bf16 v[114:117], v[170:173], v[178:181], v[114:117]
	v_mfma_f32_16x16x32_bf16 v[102:105], v[150:153], v[186:189], v[102:105]
	v_mfma_f32_16x16x32_bf16 v[98:101], v[170:173], v[186:189], v[98:101]
	v_mfma_f32_16x16x32_bf16 v[86:89], v[150:153], v[208:211], v[86:89]
	v_mfma_f32_16x16x32_bf16 v[82:85], v[170:173], v[208:211], v[82:85]
	v_mfma_f32_16x16x32_bf16 v[70:73], v[150:153], v[216:219], v[70:73]
	v_mfma_f32_16x16x32_bf16 v[66:69], v[170:173], v[216:219], v[66:69]
	s_setprio 0
	s_barrier
	ds_read_b128 v[174:177], v194 offset:16384
	ds_read_b128 v[178:181], v194 offset:17408
	ds_read_b128 v[182:185], v194 offset:18432
	ds_read_b128 v[186:189], v194 offset:19456
	ds_read_b128 v[204:207], v194 offset:20480
	ds_read_b128 v[208:211], v194 offset:21504
	ds_read_b128 v[212:215], v194 offset:22528
	ds_read_b128 v[216:219], v194 offset:23552
	s_add_i32 s68, s68, s0
	v_lshl_add_u64 v[190:191], s[66:67], 0, v[0:1]
	s_mov_b32 m0, s68
	s_nop 0
	global_load_lds_dwordx4 v[190:191], off
	s_add_i32 m0, s68, 0x2000
	v_lshl_add_u64 v[196:197], s[66:67], 0, v[164:165]
	s_add_u32 s66, s66, s12
	s_addc_u32 s67, s67, s13
	s_add_i32 s68, s70, s0
	global_load_lds_dwordx4 v[196:197], off
	v_lshl_add_u64 v[198:199], s[66:67], 0, v[0:1]
	s_mov_b32 m0, s68
	v_lshl_add_u64 v[200:201], s[66:67], 0, v[164:165]
	global_load_lds_dwordx4 v[198:199], off
	s_add_i32 m0, s68, 0x2000
	v_lshl_add_u64 v[220:221], s[30:31], 0, v[158:159]
	global_load_lds_dwordx4 v[200:201], off
	s_mov_b32 m0, s1
	v_lshl_add_u64 v[222:223], s[30:31], 0, v[160:161]
	global_load_lds_dwordx4 v[220:221], off
	s_mov_b32 m0, s36
	s_nop 0
	global_load_lds_dwordx4 v[222:223], off
	s_waitcnt vmcnt(8)
	s_waitcnt lgkmcnt(0)
	s_barrier
; #define PG8_STAGE(bufoff, gbase, voff) do { _Pragma("unroll") for (int _i = 0; _i < 2; ++_i) \
;         __builtin_amdgcn_global_load_lds((const unsigned*)((const char*)(gbase) + (voff)[_i]), (PG8_LAS unsigned*)(lds + (bufoff) + ldsw + _i * 8192), 16, 0, 0); } while (0)
; #define PG8_WAIT_V(n) asm volatile("s_waitcnt vmcnt(" #n ")" ::: "memory")
; #define PG8_WAIT_L(n) asm volatile("s_waitcnt lgkmcnt(" #n ")" ::: "memory")
; #define PG8_BAR __builtin_amdgcn_s_barrier()
; #define PG8_SCHED __builtin_amdgcn_sched_barrier(0)
; template <class Epi, class Sched, bool ALIGN_EPI = false, bool SP2 = false, bool F8 = false>
; __device__ __forceinline__ void gemm_phase(PG8_LAS unsigned char* lds, const Gemm g, const Sched& S, const Epi& E, const int tidb  ) {
;     ...
;             PG8_WAIT_V(8); PG8_WAIT_L(0); PG8_BAR; PG8_MMA(1, 0, At, B0); PG8_MMA(1, 1, At, B1); PG8_BAR; PG8_SCHED;
;             PG8_LDB(B0, 1, 0); PG8_LDB(B1, 1, 1); PG8_SCHED; PG8_LDA(At, 1, 0); PG8_STAGE(PG8_SA(0, 1), a2 + hstep, voffA);
;             PG8_WAIT_V(8); PG8_WAIT_L(0); PG8_BAR; PG8_MMA(0, 0, At, B0); PG8_MMA(0, 1, At, B1); PG8_BAR; PG8_SCHED;
	s_setprio 1
	s_waitcnt lgkmcnt(0)
	v_mfma_f32_16x16x32_bf16 v[62:65], v[122:125], v[174:177], v[62:65]
	v_mfma_f32_16x16x32_bf16 v[58:61], v[138:141], v[174:177], v[58:61]
	v_mfma_f32_16x16x32_bf16 v[46:49], v[122:125], v[182:185], v[46:49]
	v_mfma_f32_16x16x32_bf16 v[42:45], v[138:141], v[182:185], v[42:45]
	v_mfma_f32_16x16x32_bf16 v[30:33], v[122:125], v[204:207], v[30:33]
	v_mfma_f32_16x16x32_bf16 v[26:29], v[138:141], v[204:207], v[26:29]
	v_mfma_f32_16x16x32_bf16 v[14:17], v[122:125], v[212:215], v[14:17]
	v_mfma_f32_16x16x32_bf16 v[10:13], v[138:141], v[212:215], v[10:13]
	v_mfma_f32_16x16x32_bf16 v[62:65], v[126:129], v[178:181], v[62:65]
	v_mfma_f32_16x16x32_bf16 v[58:61], v[142:145], v[178:181], v[58:61]
	v_mfma_f32_16x16x32_bf16 v[46:49], v[126:129], v[186:189], v[46:49]
	v_mfma_f32_16x16x32_bf16 v[42:45], v[142:145], v[186:189], v[42:45]
	v_mfma_f32_16x16x32_bf16 v[30:33], v[126:129], v[208:211], v[30:33]
	v_mfma_f32_16x16x32_bf16 v[26:29], v[142:145], v[208:211], v[26:29]
	v_mfma_f32_16x16x32_bf16 v[14:17], v[126:129], v[216:219], v[14:17]
	v_mfma_f32_16x16x32_bf16 v[10:13], v[142:145], v[216:219], v[10:13]
	s_setprio 0
	s_setprio 1
	v_mfma_f32_16x16x32_bf16 v[54:57], v[146:149], v[174:177], v[54:57]
	v_mfma_f32_16x16x32_bf16 v[50:53], v[154:157], v[174:177], v[50:53]
	v_mfma_f32_16x16x32_bf16 v[38:41], v[146:149], v[182:185], v[38:41]
	v_mfma_f32_16x16x32_bf16 v[34:37], v[154:157], v[182:185], v[34:37]
	v_mfma_f32_16x16x32_bf16 v[22:25], v[146:149], v[204:207], v[22:25]
	v_mfma_f32_16x16x32_bf16 v[18:21], v[154:157], v[204:207], v[18:21]
	v_mfma_f32_16x16x32_bf16 v[6:9], v[146:149], v[212:215], v[6:9]
	v_mfma_f32_16x16x32_bf16 v[2:5], v[154:157], v[212:215], v[2:5]
	v_mfma_f32_16x16x32_bf16 v[54:57], v[150:153], v[178:181], v[54:57]
	v_mfma_f32_16x16x32_bf16 v[50:53], v[170:173], v[178:181], v[50:53]
	v_mfma_f32_16x16x32_bf16 v[38:41], v[150:153], v[186:189], v[38:41]
	v_mfma_f32_16x16x32_bf16 v[34:37], v[170:173], v[186:189], v[34:37]
	v_mfma_f32_16x16x32_bf16 v[22:25], v[150:153], v[208:211], v[22:25]
	v_mfma_f32_16x16x32_bf16 v[18:21], v[170:173], v[208:211], v[18:21]
	v_mfma_f32_16x16x32_bf16 v[6:9], v[150:153], v[216:219], v[6:9]
	v_mfma_f32_16x16x32_bf16 v[2:5], v[170:173], v[216:219], v[2:5]
	s_setprio 0
	s_barrier
	s_add_i32 s66, 0, 0x18000
	s_add_i32 s67, 0, 0x1c000
	v_add_u32_e32 v142, s66, v192
	v_add_u32_e32 v170, s67, v192
	ds_read_b128 v[122:125], v142
	ds_read_b128 v[126:129], v142 offset:1024
	ds_read_b128 v[138:141], v142 offset:2048
	ds_read_b128 v[142:145], v142 offset:3072
	ds_read_b128 v[146:149], v170
	ds_read_b128 v[150:153], v170 offset:1024
	ds_read_b128 v[154:157], v170 offset:2048
	ds_read_b128 v[170:173], v170 offset:3072
	s_add_u32 s30, s30, s12
	s_addc_u32 s31, s31, s13
	s_mov_b32 m0, s37
	v_lshl_add_u64 v[224:225], s[30:31], 0, v[158:159]
	ds_read_b128 v[174:177], v194 offset:32768
	ds_read_b128 v[178:181], v194 offset:33792
	ds_read_b128 v[182:185], v194 offset:34816
	ds_read_b128 v[186:189], v194 offset:35840
	ds_read_b128 v[204:207], v194 offset:36864
	ds_read_b128 v[208:211], v194 offset:37888
	ds_read_b128 v[212:215], v194 offset:38912
	ds_read_b128 v[216:219], v194 offset:39936
	global_load_lds_dwordx4 v[224:225], off
	v_lshl_add_u64 v[224:225], s[30:31], 0, v[160:161]
	s_mov_b32 m0, s41
	s_nop 0
	global_load_lds_dwordx4 v[224:225], off
	s_waitcnt vmcnt(8)
	s_waitcnt lgkmcnt(0)
	s_barrier
	s_setprio 1
	s_waitcnt lgkmcnt(0)
	v_mfma_f32_16x16x32_bf16 v[134:137], v[122:125], v[174:177], v[134:137]
	v_mfma_f32_16x16x32_bf16 v[130:133], v[138:141], v[174:177], v[130:133]
	v_mfma_f32_16x16x32_bf16 v[110:113], v[122:125], v[182:185], v[110:113]
	v_mfma_f32_16x16x32_bf16 v[106:109], v[138:141], v[182:185], v[106:109]
	v_mfma_f32_16x16x32_bf16 v[94:97], v[122:125], v[204:207], v[94:97]
	v_mfma_f32_16x16x32_bf16 v[90:93], v[138:141], v[204:207], v[90:93]
	v_mfma_f32_16x16x32_bf16 v[78:81], v[122:125], v[212:215], v[78:81]
	v_mfma_f32_16x16x32_bf16 v[74:77], v[138:141], v[212:215], v[74:77]
	v_mfma_f32_16x16x32_bf16 v[134:137], v[126:129], v[178:181], v[134:137]
	v_mfma_f32_16x16x32_bf16 v[130:133], v[142:145], v[178:181], v[130:133]
	v_mfma_f32_16x16x32_bf16 v[110:113], v[126:129], v[186:189], v[110:113]
	v_mfma_f32_16x16x32_bf16 v[106:109], v[142:145], v[186:189], v[106:109]
	v_mfma_f32_16x16x32_bf16 v[94:97], v[126:129], v[208:211], v[94:97]
	v_mfma_f32_16x16x32_bf16 v[90:93], v[142:145], v[208:211], v[90:93]
	v_mfma_f32_16x16x32_bf16 v[78:81], v[126:129], v[216:219], v[78:81]
	v_mfma_f32_16x16x32_bf16 v[74:77], v[142:145], v[216:219], v[74:77]
	s_setprio 0
	s_setprio 1
	v_mfma_f32_16x16x32_bf16 v[118:121], v[146:149], v[174:177], v[118:121]
	v_mfma_f32_16x16x32_bf16 v[114:117], v[154:157], v[174:177], v[114:117]
	v_mfma_f32_16x16x32_bf16 v[102:105], v[146:149], v[182:185], v[102:105]
	v_mfma_f32_16x16x32_bf16 v[98:101], v[154:157], v[182:185], v[98:101]
	v_mfma_f32_16x16x32_bf16 v[86:89], v[146:149], v[204:207], v[86:89]
	v_mfma_f32_16x16x32_bf16 v[82:85], v[154:157], v[204:207], v[82:85]
	v_mfma_f32_16x16x32_bf16 v[70:73], v[146:149], v[212:215], v[70:73]
	v_mfma_f32_16x16x32_bf16 v[66:69], v[154:157], v[212:215], v[66:69]
	v_mfma_f32_16x16x32_bf16 v[118:121], v[150:153], v[178:181], v[118:121]
	v_mfma_f32_16x16x32_bf16 v[114:117], v[170:173], v[178:181], v[114:117]
	v_mfma_f32_16x16x32_bf16 v[102:105], v[150:153], v[186:189], v[102:105]
	v_mfma_f32_16x16x32_bf16 v[98:101], v[170:173], v[186:189], v[98:101]
	v_mfma_f32_16x16x32_bf16 v[86:89], v[150:153], v[208:211], v[86:89]
	v_mfma_f32_16x16x32_bf16 v[82:85], v[170:173], v[208:211], v[82:85]
	v_mfma_f32_16x16x32_bf16 v[70:73], v[150:153], v[216:219], v[70:73]
	v_mfma_f32_16x16x32_bf16 v[66:69], v[170:173], v[216:219], v[66:69]
	s_setprio 0
	s_barrier
; #define PG8_STAGE(bufoff, gbase, voff) do { _Pragma("unroll") for (int _i = 0; _i < 2; ++_i) \
;         __builtin_amdgcn_global_load_lds((const unsigned*)((const char*)(gbase) + (voff)[_i]), (PG8_LAS unsigned*)(lds + (bufoff) + ldsw + _i * 8192), 16, 0, 0); } while (0)
; #define PG8_WAIT_V(n) asm volatile("s_waitcnt vmcnt(" #n ")" ::: "memory")
; #define PG8_WAIT_L(n) asm volatile("s_waitcnt lgkmcnt(" #n ")" ::: "memory")
; #define PG8_BAR __builtin_amdgcn_s_barrier()
; #define PG8_SCHED __builtin_amdgcn_sched_barrier(0)
; template <class Epi, class Sched, bool ALIGN_EPI = false, bool SP2 = false, bool F8 = false>
; __device__ __forceinline__ void gemm_phase(PG8_LAS unsigned char* lds, const Gemm g, const Sched& S, const Epi& E, const int tidb  ) {
;     ...
;         for (int t = 0; t < nt; t += 2) {
;             const bool last = (t == nt - 2);
;             if constexpr (Epi::PREFETCH) { if (t == 0) E.prefetch(cur, wid, lane); }
;             const char* a1 = cA + (size_t)(t + 1) * kstep;
;             const char* a2 = last ? nA : cA + (size_t)(t + 2) * kstep; const char* b2 = last ? nB : cB + (size_t)(t + 2) * kstep;
;     ...
;             PG8_LDA(At, 1, 1); PG8_STAGE(PG8_SB(1, 0), b3, voffB); PG8_STAGE(PG8_SB(1, 1), b3 + hstep, voffB); PG8_STAGE(PG8_SA(1, 0), a3, voffA);
;             PG8_WAIT_V(8); PG8_WAIT_L(0); PG8_BAR; PG8_MMA(1, 0, At, B0); PG8_MMA(1, 1, At, B1); PG8_BAR; PG8_SCHED;
	ds_read_b128 v[174:177], v194 offset:49152
	ds_read_b128 v[178:181], v194 offset:50176
	ds_read_b128 v[182:185], v194 offset:51200
	ds_read_b128 v[186:189], v194 offset:52224
	ds_read_b128 v[204:207], v194 offset:53248
	ds_read_b128 v[208:211], v194 offset:54272
	ds_read_b128 v[212:215], v194 offset:55296
	ds_read_b128 v[216:219], v194 offset:56320
	s_add_i32 s30, s66, s0
	v_lshl_add_u64 v[190:191], v[190:191], 0, s[92:93]
	s_mov_b32 m0, s30
	s_nop 0
	global_load_lds_dwordx4 v[190:191], off
	v_lshl_add_u64 v[190:191], v[196:197], 0, s[92:93]
	s_add_i32 m0, s30, 0x2000
	s_add_i32 s30, s67, s0
	global_load_lds_dwordx4 v[190:191], off
	v_lshl_add_u64 v[190:191], v[198:199], 0, s[92:93]
	s_mov_b32 m0, s30
	s_nop 0
	global_load_lds_dwordx4 v[190:191], off
	v_lshl_add_u64 v[190:191], v[200:201], 0, s[92:93]
	s_add_i32 m0, s30, 0x2000
	s_nop 0
	global_load_lds_dwordx4 v[190:191], off
	v_lshl_add_u64 v[190:191], v[220:221], 0, s[92:93]
	s_mov_b32 m0, s43
	s_nop 0
	global_load_lds_dwordx4 v[190:191], off
	v_lshl_add_u64 v[190:191], v[222:223], 0, s[92:93]
	s_mov_b32 m0, s45
	s_nop 0
	global_load_lds_dwordx4 v[190:191], off
	s_waitcnt vmcnt(8)
	s_waitcnt lgkmcnt(0)
	s_barrier
	s_setprio 1
	s_waitcnt lgkmcnt(0)
	v_mfma_f32_16x16x32_bf16 v[62:65], v[122:125], v[174:177], v[62:65]
	v_mfma_f32_16x16x32_bf16 v[58:61], v[138:141], v[174:177], v[58:61]
	v_mfma_f32_16x16x32_bf16 v[46:49], v[122:125], v[182:185], v[46:49]
	v_mfma_f32_16x16x32_bf16 v[42:45], v[138:141], v[182:185], v[42:45]
	v_mfma_f32_16x16x32_bf16 v[30:33], v[122:125], v[204:207], v[30:33]
	v_mfma_f32_16x16x32_bf16 v[26:29], v[138:141], v[204:207], v[26:29]
	v_mfma_f32_16x16x32_bf16 v[14:17], v[122:125], v[212:215], v[14:17]
	v_mfma_f32_16x16x32_bf16 v[10:13], v[138:141], v[212:215], v[10:13]
	v_mfma_f32_16x16x32_bf16 v[62:65], v[126:129], v[178:181], v[62:65]
	v_mfma_f32_16x16x32_bf16 v[58:61], v[142:145], v[178:181], v[58:61]
	v_mfma_f32_16x16x32_bf16 v[46:49], v[126:129], v[186:189], v[46:49]
	v_mfma_f32_16x16x32_bf16 v[42:45], v[142:145], v[186:189], v[42:45]
	v_mfma_f32_16x16x32_bf16 v[30:33], v[126:129], v[208:211], v[30:33]
	v_mfma_f32_16x16x32_bf16 v[26:29], v[142:145], v[208:211], v[26:29]
	v_mfma_f32_16x16x32_bf16 v[14:17], v[126:129], v[216:219], v[14:17]
	v_mfma_f32_16x16x32_bf16 v[10:13], v[142:145], v[216:219], v[10:13]
	s_setprio 0
	s_setprio 1
	v_mfma_f32_16x16x32_bf16 v[54:57], v[146:149], v[174:177], v[54:57]
	v_mfma_f32_16x16x32_bf16 v[50:53], v[154:157], v[174:177], v[50:53]
	v_mfma_f32_16x16x32_bf16 v[38:41], v[146:149], v[182:185], v[38:41]
	v_mfma_f32_16x16x32_bf16 v[34:37], v[154:157], v[182:185], v[34:37]
	v_mfma_f32_16x16x32_bf16 v[22:25], v[146:149], v[204:207], v[22:25]
	v_mfma_f32_16x16x32_bf16 v[18:21], v[154:157], v[204:207], v[18:21]
	v_mfma_f32_16x16x32_bf16 v[6:9], v[146:149], v[212:215], v[6:9]
	v_mfma_f32_16x16x32_bf16 v[2:5], v[154:157], v[212:215], v[2:5]
	v_mfma_f32_16x16x32_bf16 v[54:57], v[150:153], v[178:181], v[54:57]
	v_mfma_f32_16x16x32_bf16 v[50:53], v[170:173], v[178:181], v[50:53]
	v_mfma_f32_16x16x32_bf16 v[38:41], v[150:153], v[186:189], v[38:41]
	v_mfma_f32_16x16x32_bf16 v[34:37], v[170:173], v[186:189], v[34:37]
	s_add_u32 s28, s28, 0x100
	s_addc_u32 s29, s29, 0
	s_add_u32 s62, s62, 0x100
	s_addc_u32 s63, s63, 0
	s_cmp_ge_i32 s65, s46
	s_mov_b32 s30, s65
	v_mfma_f32_16x16x32_bf16 v[22:25], v[150:153], v[208:211], v[22:25]
	v_mfma_f32_16x16x32_bf16 v[18:21], v[170:173], v[208:211], v[18:21]
	v_mfma_f32_16x16x32_bf16 v[6:9], v[150:153], v[216:219], v[6:9]
	v_mfma_f32_16x16x32_bf16 v[2:5], v[170:173], v[216:219], v[2:5]
	s_setprio 0
	s_barrier
	s_cbranch_scc0 .LBB0_1807
	s_movk_i32 s67, 0x300

; #define PG8_STAGE(bufoff, gbase, voff) do { _Pragma("unroll") for (int _i = 0; _i < 2; ++_i) \
;         __builtin_amdgcn_global_load_lds((const unsigned*)((const char*)(gbase) + (voff)[_i]), (PG8_LAS unsigned*)(lds + (bufoff) + ldsw + _i * 8192), 16, 0, 0); } while (0)
; #define PG8_WAIT_V(n) asm volatile("s_waitcnt vmcnt(" #n ")" ::: "memory")
; #define PG8_WAIT_L(n) asm volatile("s_waitcnt lgkmcnt(" #n ")" ::: "memory")
; #define PG8_BAR __builtin_amdgcn_s_barrier()
; #define PG8_SCHED __builtin_amdgcn_sched_barrier(0)
; template <class Epi, class Sched, bool ALIGN_EPI = false, bool SP2 = false, bool F8 = false>
; __device__ __forceinline__ void gemm_phase(PG8_LAS unsigned char* lds, const Gemm g, const Sched& S, const Epi& E, const int tidb  ) {
;     ...
;             const char* a1 = cA + (size_t)(t + 1) * kstep;
;             const char* a2 = last ? nA : cA + (size_t)(t + 2) * kstep; const char* b2 = last ? nB : cB + (size_t)(t + 2) * kstep;
;             const char* a3 = a2 + kstep; const char* b3 = b2 + kstep;
;             if (last && has_next) S.a_ready(nxt);
;             if constexpr (SP2) {
;             PG8_LDB(B0, 0, 0); PG8_LDB(B1, 0, 1); PG8_SCHED; PG8_LDA(At, 0, 0); PG8_STAGE(PG8_SA(1, 1), a1 + hstep, voffA);
;             PG8_WAIT_V(8); PG8_WAIT_L(0); PG8_BAR; PG8_MMA(0, 0, At, B0); PG8_MMA(0, 1, At, B1); PG8_BAR; PG8_SCHED;
;             PG8_LDA(At, 0, 1); PG8_STAGE(PG8_SB(0, 0), b2, voffB); PG8_STAGE(PG8_SB(0, 1), b2 + hstep, voffB); PG8_STAGE(PG8_SA(0, 0), a2, voffA);
;             PG8_WAIT_V(8); PG8_WAIT_L(0); PG8_BAR; PG8_MMA(1, 0, At, B0); PG8_MMA(1, 1, At, B1); PG8_BAR; PG8_SCHED;
.LBB0_1857:
	s_add_i32 s66, 0, 0x10000
	v_add_u32_e32 v2, s66, v192
	ds_read_b128 v[18:21], v2
	ds_read_b128 v[22:25], v2 offset:1024
	ds_read_b128 v[26:29], v2 offset:2048
	ds_read_b128 v[30:33], v2 offset:3072
	s_add_i32 s65, s28, 2
	s_add_u32 s30, s26, 0x80
	s_addc_u32 s29, s27, 0
	s_cmp_eq_u32 s47, s28
	s_cselect_b32 s29, s7, s29
	s_cselect_b32 s28, s6, s30
	s_cselect_b32 s31, s11, s63
	s_cselect_b32 s30, s10, s62
	s_add_i32 s67, 0, 0x14000
	v_add_u32_e32 v14, s67, v192
	ds_read_b128 v[2:5], v14
	ds_read_b128 v[6:9], v14 offset:1024
	ds_read_b128 v[10:13], v14 offset:2048
	ds_read_b128 v[14:17], v14 offset:3072
	v_lshl_add_u64 v[190:191], s[26:27], 0, v[170:171]
	s_add_i32 m0, s1, 0xc000
	ds_read_b128 v[174:177], v194
	ds_read_b128 v[178:181], v194 offset:1024
	ds_read_b128 v[182:185], v194 offset:2048
	ds_read_b128 v[186:189], v194 offset:3072
	ds_read_b128 v[204:207], v194 offset:4096
	ds_read_b128 v[208:211], v194 offset:5120
	ds_read_b128 v[212:215], v194 offset:6144
	ds_read_b128 v[216:219], v194 offset:7168
	global_load_lds_dwordx4 v[190:191], off
	v_lshl_add_u64 v[190:191], s[26:27], 0, v[172:173]
	s_add_i32 m0, s1, 0xe000
	s_nop 0
	global_load_lds_dwordx4 v[190:191], off
	s_waitcnt vmcnt(8)
	s_waitcnt lgkmcnt(0)
	s_barrier
	s_setprio 1
	s_waitcnt lgkmcnt(0)
	v_mfma_scale_f32_16x16x128_f8f6f4 v[158:161], v[18:25], v[174:181], v[158:161], v246, v247 op_sel_hi:[0,0,0]
	v_mfma_scale_f32_16x16x128_f8f6f4 v[154:157], v[26:33], v[174:181], v[154:157], v246, v247 op_sel_hi:[0,0,0]
	v_mfma_scale_f32_16x16x128_f8f6f4 v[142:145], v[18:25], v[182:189], v[142:145], v246, v247 op_sel_hi:[0,0,0]
	v_mfma_scale_f32_16x16x128_f8f6f4 v[138:141], v[26:33], v[182:189], v[138:141], v246, v247 op_sel_hi:[0,0,0]
	v_mfma_scale_f32_16x16x128_f8f6f4 v[126:129], v[18:25], v[204:211], v[126:129], v246, v247 op_sel_hi:[0,0,0]
	v_mfma_scale_f32_16x16x128_f8f6f4 v[122:125], v[26:33], v[204:211], v[122:125], v246, v247 op_sel_hi:[0,0,0]
	v_mfma_scale_f32_16x16x128_f8f6f4 v[110:113], v[18:25], v[212:219], v[110:113], v246, v247 op_sel_hi:[0,0,0]
	v_mfma_scale_f32_16x16x128_f8f6f4 v[106:109], v[26:33], v[212:219], v[106:109], v246, v247 op_sel_hi:[0,0,0]
	s_setprio 0
	s_setprio 1
	v_mfma_scale_f32_16x16x128_f8f6f4 v[150:153], v[2:9], v[174:181], v[150:153], v246, v247 op_sel_hi:[0,0,0]
	v_mfma_scale_f32_16x16x128_f8f6f4 v[146:149], v[10:17], v[174:181], v[146:149], v246, v247 op_sel_hi:[0,0,0]
	v_mfma_scale_f32_16x16x128_f8f6f4 v[134:137], v[2:9], v[182:189], v[134:137], v246, v247 op_sel_hi:[0,0,0]
	v_mfma_scale_f32_16x16x128_f8f6f4 v[130:133], v[10:17], v[182:189], v[130:133], v246, v247 op_sel_hi:[0,0,0]
	v_mfma_scale_f32_16x16x128_f8f6f4 v[118:121], v[2:9], v[204:211], v[118:121], v246, v247 op_sel_hi:[0,0,0]
	v_mfma_scale_f32_16x16x128_f8f6f4 v[114:117], v[10:17], v[204:211], v[114:117], v246, v247 op_sel_hi:[0,0,0]
	v_mfma_scale_f32_16x16x128_f8f6f4 v[102:105], v[2:9], v[212:219], v[102:105], v246, v247 op_sel_hi:[0,0,0]
	v_mfma_scale_f32_16x16x128_f8f6f4 v[98:101], v[10:17], v[212:219], v[98:101], v246, v247 op_sel_hi:[0,0,0]
	s_setprio 0
	s_barrier
	ds_read_b128 v[204:207], v194 offset:16384
	ds_read_b128 v[208:211], v194 offset:17408
	ds_read_b128 v[212:215], v194 offset:18432
	ds_read_b128 v[216:219], v194 offset:19456
	ds_read_b128 v[220:223], v194 offset:20480
	ds_read_b128 v[224:227], v194 offset:21504
	ds_read_b128 v[228:231], v194 offset:22528
	ds_read_b128 v[232:235], v194 offset:23552
	s_add_i32 s66, s66, s0
	v_lshl_add_u64 v[174:175], s[30:31], 0, v[0:1]
	s_mov_b32 m0, s66
	s_nop 0
	global_load_lds_dwordx4 v[174:175], off
	s_add_i32 m0, s66, 0x2000
	v_lshl_add_u64 v[176:177], s[30:31], 0, v[168:169]
	s_add_u32 s30, s30, s12
	s_addc_u32 s31, s31, s13
	s_add_i32 s66, s67, s0
	global_load_lds_dwordx4 v[176:177], off
	v_lshl_add_u64 v[178:179], s[30:31], 0, v[0:1]
	s_mov_b32 m0, s66
	v_lshl_add_u64 v[180:181], s[30:31], 0, v[168:169]
	global_load_lds_dwordx4 v[178:179], off
	s_add_i32 m0, s66, 0x2000
	v_lshl_add_u64 v[182:183], s[28:29], 0, v[164:165]
	global_load_lds_dwordx4 v[180:181], off
	s_mov_b32 m0, s1
	v_lshl_add_u64 v[184:185], s[28:29], 0, v[166:167]
	global_load_lds_dwordx4 v[182:183], off
	s_mov_b32 m0, s36
	s_nop 0
	global_load_lds_dwordx4 v[184:185], off
	s_waitcnt vmcnt(8)
	s_waitcnt lgkmcnt(0)
	s_barrier
	s_setprio 1
	s_waitcnt lgkmcnt(0)
	v_mfma_scale_f32_16x16x128_f8f6f4 v[94:97], v[18:25], v[204:211], v[94:97], v246, v247 op_sel_hi:[0,0,0]
	v_mfma_scale_f32_16x16x128_f8f6f4 v[90:93], v[26:33], v[204:211], v[90:93], v246, v247 op_sel_hi:[0,0,0]
	v_mfma_scale_f32_16x16x128_f8f6f4 v[78:81], v[18:25], v[212:219], v[78:81], v246, v247 op_sel_hi:[0,0,0]
	v_mfma_scale_f32_16x16x128_f8f6f4 v[74:77], v[26:33], v[212:219], v[74:77], v246, v247 op_sel_hi:[0,0,0]
	v_mfma_scale_f32_16x16x128_f8f6f4 v[62:65], v[18:25], v[220:227], v[62:65], v246, v247 op_sel_hi:[0,0,0]
	v_mfma_scale_f32_16x16x128_f8f6f4 v[58:61], v[26:33], v[220:227], v[58:61], v246, v247 op_sel_hi:[0,0,0]
	v_mfma_scale_f32_16x16x128_f8f6f4 v[46:49], v[18:25], v[228:235], v[46:49], v246, v247 op_sel_hi:[0,0,0]
	v_mfma_scale_f32_16x16x128_f8f6f4 v[42:45], v[26:33], v[228:235], v[42:45], v246, v247 op_sel_hi:[0,0,0]
	s_setprio 0
	s_setprio 1
	v_mfma_scale_f32_16x16x128_f8f6f4 v[86:89], v[2:9], v[204:211], v[86:89], v246, v247 op_sel_hi:[0,0,0]
	v_mfma_scale_f32_16x16x128_f8f6f4 v[82:85], v[10:17], v[204:211], v[82:85], v246, v247 op_sel_hi:[0,0,0]
	v_mfma_scale_f32_16x16x128_f8f6f4 v[70:73], v[2:9], v[212:219], v[70:73], v246, v247 op_sel_hi:[0,0,0]
	v_mfma_scale_f32_16x16x128_f8f6f4 v[66:69], v[10:17], v[212:219], v[66:69], v246, v247 op_sel_hi:[0,0,0]
	v_mfma_scale_f32_16x16x128_f8f6f4 v[54:57], v[2:9], v[220:227], v[54:57], v246, v247 op_sel_hi:[0,0,0]
	v_mfma_scale_f32_16x16x128_f8f6f4 v[50:53], v[10:17], v[220:227], v[50:53], v246, v247 op_sel_hi:[0,0,0]
	v_mfma_scale_f32_16x16x128_f8f6f4 v[38:41], v[2:9], v[228:235], v[38:41], v246, v247 op_sel_hi:[0,0,0]
	v_mfma_scale_f32_16x16x128_f8f6f4 v[34:37], v[10:17], v[228:235], v[34:37], v246, v247 op_sel_hi:[0,0,0]
	s_setprio 0
	s_barrier
; #define PG8_STAGE(bufoff, gbase, voff) do { _Pragma("unroll") for (int _i = 0; _i < 2; ++_i) \
;         __builtin_amdgcn_global_load_lds((const unsigned*)((const char*)(gbase) + (voff)[_i]), (PG8_LAS unsigned*)(lds + (bufoff) + ldsw + _i * 8192), 16, 0, 0); } while (0)
; #define PG8_WAIT_V(n) asm volatile("s_waitcnt vmcnt(" #n ")" ::: "memory")
; #define PG8_WAIT_L(n) asm volatile("s_waitcnt lgkmcnt(" #n ")" ::: "memory")
; #define PG8_BAR __builtin_amdgcn_s_barrier()
; #define PG8_SCHED __builtin_amdgcn_sched_barrier(0)
; template <class Epi, class Sched, bool ALIGN_EPI = false, bool SP2 = false, bool F8 = false>
; __device__ __forceinline__ void gemm_phase(PG8_LAS unsigned char* lds, const Gemm g, const Sched& S, const Epi& E, const int tidb  ) {
;     ...
;             PG8_LDB(B0, 1, 0); PG8_LDB(B1, 1, 1); PG8_SCHED; PG8_LDA(At, 1, 0); PG8_STAGE(PG8_SA(0, 1), a2 + hstep, voffA);
;             PG8_WAIT_V(8); PG8_WAIT_L(0); PG8_BAR; PG8_MMA(0, 0, At, B0); PG8_MMA(0, 1, At, B1); PG8_BAR; PG8_SCHED;
;             PG8_LDA(At, 1, 1); PG8_STAGE(PG8_SB(1, 0), b3, voffB); PG8_STAGE(PG8_SB(1, 1), b3 + hstep, voffB); PG8_STAGE(PG8_SA(1, 0), a3, voffA);
;             PG8_WAIT_V(8); PG8_WAIT_L(0); PG8_BAR; PG8_MMA(1, 0, At, B0); PG8_MMA(1, 1, At, B1); PG8_BAR; PG8_SCHED;
	s_add_i32 s30, 0, 0x18000
	s_add_i32 s31, 0, 0x1c000
	v_add_u32_e32 v14, s30, v192
	v_add_u32_e32 v30, s31, v192
	ds_read_b128 v[2:5], v14
	ds_read_b128 v[6:9], v14 offset:1024
	ds_read_b128 v[10:13], v14 offset:2048
	ds_read_b128 v[14:17], v14 offset:3072
	ds_read_b128 v[18:21], v30
	ds_read_b128 v[22:25], v30 offset:1024
	ds_read_b128 v[26:29], v30 offset:2048
	ds_read_b128 v[30:33], v30 offset:3072
	s_add_u32 s28, s28, s12
	s_addc_u32 s29, s29, s13
	s_mov_b32 m0, s37
	v_lshl_add_u64 v[186:187], s[28:29], 0, v[164:165]
	ds_read_b128 v[204:207], v194 offset:32768
	ds_read_b128 v[208:211], v194 offset:33792
	ds_read_b128 v[212:215], v194 offset:34816
	ds_read_b128 v[216:219], v194 offset:35840
	ds_read_b128 v[220:223], v194 offset:36864
	ds_read_b128 v[224:227], v194 offset:37888
	ds_read_b128 v[228:231], v194 offset:38912
	ds_read_b128 v[232:235], v194 offset:39936
	global_load_lds_dwordx4 v[186:187], off
	v_lshl_add_u64 v[186:187], s[28:29], 0, v[166:167]
	s_mov_b32 m0, s41
	s_nop 0
	global_load_lds_dwordx4 v[186:187], off
	s_waitcnt vmcnt(8)
	s_waitcnt lgkmcnt(0)
	s_barrier
	s_setprio 1
	s_waitcnt lgkmcnt(0)
	v_mfma_scale_f32_16x16x128_f8f6f4 v[158:161], v[2:9], v[204:211], v[158:161], v246, v247 op_sel_hi:[0,0,0]
	v_mfma_scale_f32_16x16x128_f8f6f4 v[154:157], v[10:17], v[204:211], v[154:157], v246, v247 op_sel_hi:[0,0,0]
	v_mfma_scale_f32_16x16x128_f8f6f4 v[142:145], v[2:9], v[212:219], v[142:145], v246, v247 op_sel_hi:[0,0,0]
	v_mfma_scale_f32_16x16x128_f8f6f4 v[138:141], v[10:17], v[212:219], v[138:141], v246, v247 op_sel_hi:[0,0,0]
	v_mfma_scale_f32_16x16x128_f8f6f4 v[126:129], v[2:9], v[220:227], v[126:129], v246, v247 op_sel_hi:[0,0,0]
	v_mfma_scale_f32_16x16x128_f8f6f4 v[122:125], v[10:17], v[220:227], v[122:125], v246, v247 op_sel_hi:[0,0,0]
	v_mfma_scale_f32_16x16x128_f8f6f4 v[110:113], v[2:9], v[228:235], v[110:113], v246, v247 op_sel_hi:[0,0,0]
	v_mfma_scale_f32_16x16x128_f8f6f4 v[106:109], v[10:17], v[228:235], v[106:109], v246, v247 op_sel_hi:[0,0,0]
	s_setprio 0
	s_setprio 1
	v_mfma_scale_f32_16x16x128_f8f6f4 v[150:153], v[18:25], v[204:211], v[150:153], v246, v247 op_sel_hi:[0,0,0]
	v_mfma_scale_f32_16x16x128_f8f6f4 v[146:149], v[26:33], v[204:211], v[146:149], v246, v247 op_sel_hi:[0,0,0]
	v_mfma_scale_f32_16x16x128_f8f6f4 v[134:137], v[18:25], v[212:219], v[134:137], v246, v247 op_sel_hi:[0,0,0]
	v_mfma_scale_f32_16x16x128_f8f6f4 v[130:133], v[26:33], v[212:219], v[130:133], v246, v247 op_sel_hi:[0,0,0]
	v_mfma_scale_f32_16x16x128_f8f6f4 v[118:121], v[18:25], v[220:227], v[118:121], v246, v247 op_sel_hi:[0,0,0]
	v_mfma_scale_f32_16x16x128_f8f6f4 v[114:117], v[26:33], v[220:227], v[114:117], v246, v247 op_sel_hi:[0,0,0]
	v_mfma_scale_f32_16x16x128_f8f6f4 v[102:105], v[18:25], v[228:235], v[102:105], v246, v247 op_sel_hi:[0,0,0]
	v_mfma_scale_f32_16x16x128_f8f6f4 v[98:101], v[26:33], v[228:235], v[98:101], v246, v247 op_sel_hi:[0,0,0]
	s_setprio 0
	s_barrier
	ds_read_b128 v[204:207], v194 offset:49152
	ds_read_b128 v[208:211], v194 offset:50176
	ds_read_b128 v[212:215], v194 offset:51200
	ds_read_b128 v[216:219], v194 offset:52224
	ds_read_b128 v[220:223], v194 offset:53248
	ds_read_b128 v[224:227], v194 offset:54272
	ds_read_b128 v[228:231], v194 offset:55296
	ds_read_b128 v[232:235], v194 offset:56320
	s_add_i32 s28, s30, s0
	v_lshl_add_u64 v[174:175], v[174:175], 0, s[92:93]
	s_mov_b32 m0, s28
	s_nop 0
	global_load_lds_dwordx4 v[174:175], off
	v_lshl_add_u64 v[174:175], v[176:177], 0, s[92:93]
	s_add_i32 m0, s28, 0x2000
	s_add_i32 s28, s31, s0
	global_load_lds_dwordx4 v[174:175], off
	v_lshl_add_u64 v[174:175], v[178:179], 0, s[92:93]
	s_mov_b32 m0, s28
	s_nop 0
	global_load_lds_dwordx4 v[174:175], off
	v_lshl_add_u64 v[174:175], v[180:181], 0, s[92:93]
	s_add_i32 m0, s28, 0x2000
	s_nop 0
	global_load_lds_dwordx4 v[174:175], off
	v_lshl_add_u64 v[174:175], v[182:183], 0, s[92:93]
	s_mov_b32 m0, s43
	s_nop 0
	global_load_lds_dwordx4 v[174:175], off
	v_lshl_add_u64 v[174:175], v[184:185], 0, s[92:93]
	s_mov_b32 m0, s45
	s_nop 0
	global_load_lds_dwordx4 v[174:175], off
	s_waitcnt vmcnt(8)
	s_waitcnt lgkmcnt(0)
	s_barrier
	s_setprio 1
	s_waitcnt lgkmcnt(0)
	v_mfma_scale_f32_16x16x128_f8f6f4 v[94:97], v[2:9], v[204:211], v[94:97], v246, v247 op_sel_hi:[0,0,0]
	v_mfma_scale_f32_16x16x128_f8f6f4 v[90:93], v[10:17], v[204:211], v[90:93], v246, v247 op_sel_hi:[0,0,0]
	v_mfma_scale_f32_16x16x128_f8f6f4 v[78:81], v[2:9], v[212:219], v[78:81], v246, v247 op_sel_hi:[0,0,0]
	v_mfma_scale_f32_16x16x128_f8f6f4 v[74:77], v[10:17], v[212:219], v[74:77], v246, v247 op_sel_hi:[0,0,0]
	v_mfma_scale_f32_16x16x128_f8f6f4 v[62:65], v[2:9], v[220:227], v[62:65], v246, v247 op_sel_hi:[0,0,0]
	v_mfma_scale_f32_16x16x128_f8f6f4 v[58:61], v[10:17], v[220:227], v[58:61], v246, v247 op_sel_hi:[0,0,0]
	v_mfma_scale_f32_16x16x128_f8f6f4 v[46:49], v[2:9], v[228:235], v[46:49], v246, v247 op_sel_hi:[0,0,0]
	v_mfma_scale_f32_16x16x128_f8f6f4 v[42:45], v[10:17], v[228:235], v[42:45], v246, v247 op_sel_hi:[0,0,0]
	s_setprio 0
	s_setprio 1
	v_mfma_scale_f32_16x16x128_f8f6f4 v[86:89], v[18:25], v[204:211], v[86:89], v246, v247 op_sel_hi:[0,0,0]
	v_mfma_scale_f32_16x16x128_f8f6f4 v[82:85], v[26:33], v[204:211], v[82:85], v246, v247 op_sel_hi:[0,0,0]
	v_mfma_scale_f32_16x16x128_f8f6f4 v[70:73], v[18:25], v[212:219], v[70:73], v246, v247 op_sel_hi:[0,0,0]
	v_mfma_scale_f32_16x16x128_f8f6f4 v[66:69], v[26:33], v[212:219], v[66:69], v246, v247 op_sel_hi:[0,0,0]
	s_add_u32 s26, s26, 0x100
	s_addc_u32 s27, s27, 0
	s_add_u32 s62, s62, 0x100
	s_addc_u32 s63, s63, 0
	s_cmp_ge_i32 s65, s46
	s_mov_b32 s28, s65
	v_mfma_scale_f32_16x16x128_f8f6f4 v[54:57], v[18:25], v[220:227], v[54:57], v246, v247 op_sel_hi:[0,0,0]
	v_mfma_scale_f32_16x16x128_f8f6f4 v[50:53], v[26:33], v[220:227], v[50:53], v246, v247 op_sel_hi:[0,0,0]
	v_mfma_scale_f32_16x16x128_f8f6f4 v[38:41], v[18:25], v[228:235], v[38:41], v246, v247 op_sel_hi:[0,0,0]
	v_mfma_scale_f32_16x16x128_f8f6f4 v[34:37], v[26:33], v[228:235], v[34:37], v246, v247 op_sel_hi:[0,0,0]
	s_setprio 0
	s_barrier
	s_cbranch_scc0 .LBB0_1857
	s_movk_i32 s67, 0x300
